# v11 with the LDS-DMA stage loads placed after MFMAs 5 and 8 of each phase
# speedup vs baseline: 1.0023x; 1.0023x over previous
.LBB0_249:
	s_add_u32 s31, s26, 0xfffc0080
	s_addc_u32 s33, s27, -1
	s_add_i32 s34, 0, 0x10000
	v_add_u32_e32 v0, s34, v138
	ds_read_b128 v[140:143], v0
	ds_read_b128 v[144:147], v0 offset:1024
	ds_read_b128 v[148:151], v0 offset:2048
	ds_read_b128 v[152:155], v0 offset:3072
	s_cmp_eq_u32 s30, 12
	s_cselect_b32 s49, s3, s33
	s_cselect_b32 s48, s5, s31
	s_cselect_b32 s47, s20, s25
	s_cselect_b32 s46, s21, s22
	v_mov_b32_e32 v0, v136
	ds_read_b128 v[156:159], v139
	ds_read_b128 v[160:163], v139 offset:1024
	ds_read_b128 v[172:175], v139 offset:2048
	ds_read_b128 v[176:179], v139 offset:3072
	ds_read_b128 v[180:183], v139 offset:4096
	ds_read_b128 v[184:187], v139 offset:5120
	ds_read_b128 v[188:191], v139 offset:6144
	ds_read_b128 v[192:195], v139 offset:7168
	s_nop 0
	v_mov_b32_e32 v0, v137
	s_nop 0
	s_waitcnt lgkmcnt(8)
	s_barrier
	s_waitcnt lgkmcnt(0)
	s_setprio 1
	v_mov_b64_e32 v[50:51], v[164:165]
	s_waitcnt lgkmcnt(0)
	v_mfma_scale_f32_16x16x128_f8f6f4 v[98:101], v[156:163], v[148:155], v[98:101], v202, v202 op_sel_hi:[0,0,0]
	v_mov_b64_e32 v[52:53], v[166:167]
	v_mfma_scale_f32_16x16x128_f8f6f4 v[164:167], v[172:179], v[140:147], v[118:121], v202, v202 op_sel_hi:[0,0,0]
	v_mfma_scale_f32_16x16x128_f8f6f4 v[90:93], v[180:187], v[148:155], v[90:93], v202, v202 op_sel_hi:[0,0,0]
	v_mfma_scale_f32_16x16x128_f8f6f4 v[130:133], v[156:163], v[140:147], v[126:129], v202, v202 op_sel_hi:[0,0,0]
	s_add_i32 m0, s1, 0xc000
	v_mfma_scale_f32_16x16x128_f8f6f4 v[168:171], v[172:179], v[148:155], v[86:89], v202, v202 op_sel_hi:[0,0,0]
	global_load_lds_dwordx4 v136, s[26:27]
	v_mfma_scale_f32_16x16x128_f8f6f4 v[196:199], v[180:187], v[140:147], v[122:125], v202, v202 op_sel_hi:[0,0,0]
	v_mfma_scale_f32_16x16x128_f8f6f4 v[206:209], v[188:195], v[140:147], v[114:117], v202, v202 op_sel_hi:[0,0,0]
	s_add_i32 m0, s1, 0xe000
	v_mfma_scale_f32_16x16x128_f8f6f4 v[210:213], v[188:195], v[148:155], v[82:85], v202, v202 op_sel_hi:[0,0,0]
	global_load_lds_dwordx4 v137, s[26:27]
	s_setprio 0
	s_barrier
	s_add_i32 s31, 0, 0x14000
	v_add_u32_e32 v0, s31, v138
	s_nop 2
	ds_read_b128 v[82:85], v0
	ds_read_b128 v[86:89], v0 offset:1024
	ds_read_b128 v[114:117], v0 offset:2048
	ds_read_b128 v[118:121], v0 offset:3072
	v_mov_b32_e32 v0, v136
	s_add_i32 s33, s34, s73
	s_nop 0
	v_mov_b32_e32 v0, v137
	s_nop 0
	s_barrier
	s_waitcnt lgkmcnt(0)
	s_setprio 1
	s_waitcnt lgkmcnt(0)
	v_mfma_scale_f32_16x16x128_f8f6f4 v[66:69], v[156:163], v[82:89], v[66:69], v202, v202 op_sel_hi:[0,0,0]
	v_mfma_scale_f32_16x16x128_f8f6f4 v[38:41], v[156:163], v[114:121], v[38:41], v202, v202 op_sel_hi:[0,0,0]
	v_mfma_scale_f32_16x16x128_f8f6f4 v[58:61], v[180:187], v[82:89], v[58:61], v202, v202 op_sel_hi:[0,0,0]
	v_mfma_scale_f32_16x16x128_f8f6f4 v[214:217], v[172:179], v[82:89], v[54:57], v202, v202 op_sel_hi:[0,0,0]
	s_mov_b32 m0, s33
	v_mfma_scale_f32_16x16x128_f8f6f4 v[172:175], v[172:179], v[114:121], v[22:25], v202, v202 op_sel_hi:[0,0,0]
	global_load_lds_dwordx4 v136, s[46:47]
	v_mfma_scale_f32_16x16x128_f8f6f4 v[176:179], v[180:187], v[114:121], v[30:33], v202, v202 op_sel_hi:[0,0,0]
	v_mfma_scale_f32_16x16x128_f8f6f4 v[180:183], v[188:195], v[82:89], v[18:21], v202, v202 op_sel_hi:[0,0,0]
	s_add_i32 m0, s33, 0x2000
	v_mfma_scale_f32_16x16x128_f8f6f4 v[184:187], v[188:195], v[114:121], v[50:53], v202, v202 op_sel_hi:[0,0,0]
	global_load_lds_dwordx4 v137, s[46:47]
	s_setprio 0
	v_mov_b32_e32 v0, v136
	s_barrier
	s_nop 1
	ds_read_b128 v[18:21], v139 offset:16384
	ds_read_b128 v[22:25], v139 offset:17408
	ds_read_b128 v[50:53], v139 offset:18432
	ds_read_b128 v[54:57], v139 offset:19456
	ds_read_b128 v[122:125], v139 offset:20480
	ds_read_b128 v[126:129], v139 offset:21504
	ds_read_b128 v[156:159], v139 offset:22528
	ds_read_b128 v[160:163], v139 offset:23552
	s_nop 0
	v_mov_b32_e32 v0, v137
	s_nop 0
	s_barrier
	s_waitcnt lgkmcnt(0)
	s_setprio 1
	s_waitcnt lgkmcnt(0)
	v_mfma_scale_f32_16x16x128_f8f6f4 v[110:113], v[18:25], v[140:147], v[110:113], v202, v202 op_sel_hi:[0,0,0]
	v_mfma_scale_f32_16x16x128_f8f6f4 v[78:81], v[18:25], v[148:155], v[78:81], v202, v202 op_sel_hi:[0,0,0]
	v_mfma_scale_f32_16x16x128_f8f6f4 v[102:105], v[50:57], v[140:147], v[102:105], v202, v202 op_sel_hi:[0,0,0]
	v_mfma_scale_f32_16x16x128_f8f6f4 v[106:109], v[122:129], v[140:147], v[106:109], v202, v202 op_sel_hi:[0,0,0]
	s_mov_b32 m0, s1
	v_mfma_scale_f32_16x16x128_f8f6f4 v[94:97], v[156:163], v[140:147], v[94:97], v202, v202 op_sel_hi:[0,0,0]
	global_load_lds_dwordx4 v136, s[48:49]
	v_mfma_scale_f32_16x16x128_f8f6f4 v[62:65], v[156:163], v[148:155], v[62:65], v202, v202 op_sel_hi:[0,0,0]
	v_mfma_scale_f32_16x16x128_f8f6f4 v[218:221], v[50:57], v[148:155], v[70:73], v202, v202 op_sel_hi:[0,0,0]
	s_mov_b32 m0, s13
	v_mfma_scale_f32_16x16x128_f8f6f4 v[222:225], v[122:129], v[148:155], v[74:77], v202, v202 op_sel_hi:[0,0,0]
	global_load_lds_dwordx4 v137, s[48:49]
	s_setprio 0
	s_barrier
	s_add_u32 s34, s46, 0x40000
	s_addc_u32 s35, s47, 0
	v_mov_b32_e32 v0, v136
	s_add_i32 s31, s31, s73
	s_mov_b32 s100, s31
	s_nop 0
	v_mov_b32_e32 v0, v137
	s_add_i32 s101, s31, 0x2000
	s_nop 0
	s_waitcnt vmcnt(4)
	s_barrier
	s_setprio 1
	v_mfma_scale_f32_16x16x128_f8f6f4 v[34:37], v[50:57], v[82:89], v[34:37], v202, v202 op_sel_hi:[0,0,0]
	v_mfma_scale_f32_16x16x128_f8f6f4 v[226:229], v[18:25], v[82:89], v[46:49], v202, v202 op_sel_hi:[0,0,0]
	v_mfma_scale_f32_16x16x128_f8f6f4 v[230:233], v[18:25], v[114:121], v[14:17], v202, v202 op_sel_hi:[0,0,0]
	v_mfma_scale_f32_16x16x128_f8f6f4 v[234:237], v[50:57], v[114:121], v[6:9], v202, v202 op_sel_hi:[0,0,0]
	s_mov_b32 m0, s100
	v_mfma_scale_f32_16x16x128_f8f6f4 v[238:241], v[122:129], v[82:89], v[42:45], v202, v202 op_sel_hi:[0,0,0]
	global_load_lds_dwordx4 v136, s[34:35]
	v_mfma_scale_f32_16x16x128_f8f6f4 v[242:245], v[122:129], v[114:121], v[10:13], v202, v202 op_sel_hi:[0,0,0]
	v_mfma_scale_f32_16x16x128_f8f6f4 v[246:249], v[156:163], v[82:89], v[26:29], v202, v202 op_sel_hi:[0,0,0]
	s_mov_b32 m0, s101
	v_mfma_scale_f32_16x16x128_f8f6f4 v[50:53], v[156:163], v[114:121], v[2:5], v202, v202 op_sel_hi:[0,0,0]
	global_load_lds_dwordx4 v137, s[34:35]
	s_setprio 0
	s_add_i32 s31, 0, 0x18000
	v_add_u32_e32 v0, s31, v138
	s_barrier
	s_nop 2
	ds_read_b128 v[2:5], v0
	ds_read_b128 v[6:9], v0 offset:1024
	ds_read_b128 v[10:13], v0 offset:2048
	ds_read_b128 v[14:17], v0 offset:3072
	s_add_u32 s34, s48, 0x40000
	v_mov_b32_e32 v0, v136
	ds_read_b128 v[18:21], v139 offset:32768
	ds_read_b128 v[22:25], v139 offset:33792
	ds_read_b128 v[26:29], v139 offset:34816
	ds_read_b128 v[30:33], v139 offset:35840
	ds_read_b128 v[42:45], v139 offset:36864
	ds_read_b128 v[46:49], v139 offset:37888
	ds_read_b128 v[70:73], v139 offset:38912
	ds_read_b128 v[74:77], v139 offset:39936
	s_addc_u32 s35, s49, 0
	s_nop 0
	v_mov_b32_e32 v0, v137
	s_nop 0
	s_waitcnt lgkmcnt(8)
	s_barrier
	s_waitcnt lgkmcnt(0)
	s_setprio 1
	s_waitcnt lgkmcnt(0)
	v_mfma_scale_f32_16x16x128_f8f6f4 v[126:129], v[18:25], v[2:9], v[130:133], v202, v202 op_sel_hi:[0,0,0]
	v_mfma_scale_f32_16x16x128_f8f6f4 v[98:101], v[18:25], v[10:17], v[98:101], v202, v202 op_sel_hi:[0,0,0]
	v_mfma_scale_f32_16x16x128_f8f6f4 v[118:121], v[26:33], v[2:9], v[164:167], v202, v202 op_sel_hi:[0,0,0]
	v_mfma_scale_f32_16x16x128_f8f6f4 v[86:89], v[26:33], v[10:17], v[168:171], v202, v202 op_sel_hi:[0,0,0]
	s_mov_b32 m0, s14
	v_mfma_scale_f32_16x16x128_f8f6f4 v[122:125], v[42:49], v[2:9], v[196:199], v202, v202 op_sel_hi:[0,0,0]
	global_load_lds_dwordx4 v136, s[34:35]
	v_mfma_scale_f32_16x16x128_f8f6f4 v[90:93], v[42:49], v[10:17], v[90:93], v202, v202 op_sel_hi:[0,0,0]
	v_mfma_scale_f32_16x16x128_f8f6f4 v[114:117], v[70:77], v[2:9], v[206:209], v202, v202 op_sel_hi:[0,0,0]
	s_mov_b32 m0, s15
	v_mfma_scale_f32_16x16x128_f8f6f4 v[82:85], v[70:77], v[10:17], v[210:213], v202, v202 op_sel_hi:[0,0,0]
	global_load_lds_dwordx4 v137, s[34:35]
	s_setprio 0
	s_barrier
	s_add_i32 s33, 0, 0x1c000
	v_add_u32_e32 v0, s33, v138
	ds_read_b128 v[140:143], v0
	ds_read_b128 v[144:147], v0 offset:1024
	ds_read_b128 v[148:151], v0 offset:2048
	ds_read_b128 v[152:155], v0 offset:3072
	v_mov_b32_e32 v0, v136
	s_add_i32 s31, s31, s73
	v_lshl_add_u64 v[54:55], s[46:47], 0, v[0:1]
	v_lshl_add_u64 v[54:55], v[54:55], 0, s[66:67]
	v_mov_b32_e32 v0, v137
	v_lshl_add_u64 v[54:55], s[46:47], 0, v[0:1]
	v_lshl_add_u64 v[54:55], v[54:55], 0, s[66:67]
	s_barrier
	s_waitcnt lgkmcnt(0)
	s_setprio 1
	s_waitcnt lgkmcnt(0)
	v_mfma_scale_f32_16x16x128_f8f6f4 v[66:69], v[18:25], v[140:147], v[66:69], v202, v202 op_sel_hi:[0,0,0]
	v_mfma_scale_f32_16x16x128_f8f6f4 v[38:41], v[18:25], v[148:155], v[38:41], v202, v202 op_sel_hi:[0,0,0]
	v_mfma_scale_f32_16x16x128_f8f6f4 v[54:57], v[26:33], v[140:147], v[214:217], v202, v202 op_sel_hi:[0,0,0]
	v_mfma_scale_f32_16x16x128_f8f6f4 v[22:25], v[26:33], v[148:155], v[172:175], v202, v202 op_sel_hi:[0,0,0]
	s_add_u32 s98, s46, s66
	s_addc_u32 s99, s47, s67
	s_mov_b32 m0, s31
	v_mfma_scale_f32_16x16x128_f8f6f4 v[58:61], v[42:49], v[140:147], v[58:61], v202, v202 op_sel_hi:[0,0,0]
	global_load_lds_dwordx4 v136, s[98:99]
	v_mfma_scale_f32_16x16x128_f8f6f4 v[30:33], v[42:49], v[148:155], v[176:179], v202, v202 op_sel_hi:[0,0,0]
	v_mfma_scale_f32_16x16x128_f8f6f4 v[18:21], v[70:77], v[140:147], v[180:183], v202, v202 op_sel_hi:[0,0,0]
	s_add_i32 m0, s31, 0x2000
	v_mfma_scale_f32_16x16x128_f8f6f4 v[164:167], v[70:77], v[148:155], v[184:187], v202, v202 op_sel_hi:[0,0,0]
	global_load_lds_dwordx4 v137, s[98:99]
	s_setprio 0
	v_mov_b32_e32 v0, v136
	s_barrier
	ds_read_b128 v[156:159], v139 offset:49152
	ds_read_b128 v[160:163], v139 offset:50176
	ds_read_b128 v[172:175], v139 offset:51200
	ds_read_b128 v[176:179], v139 offset:52224
	ds_read_b128 v[180:183], v139 offset:53248
	ds_read_b128 v[184:187], v139 offset:54272
	ds_read_b128 v[188:191], v139 offset:55296
	ds_read_b128 v[192:195], v139 offset:56320
	v_lshl_add_u64 v[26:27], s[48:49], 0, v[0:1]
	v_lshl_add_u64 v[26:27], v[26:27], 0, s[66:67]
	v_mov_b32_e32 v0, v137
	v_lshl_add_u64 v[26:27], s[48:49], 0, v[0:1]
	v_lshl_add_u64 v[26:27], v[26:27], 0, s[66:67]
	s_barrier
	s_waitcnt lgkmcnt(0)
	s_setprio 1
	s_waitcnt lgkmcnt(0)
	v_mfma_scale_f32_16x16x128_f8f6f4 v[110:113], v[156:163], v[2:9], v[110:113], v202, v202 op_sel_hi:[0,0,0]
	v_mfma_scale_f32_16x16x128_f8f6f4 v[78:81], v[156:163], v[10:17], v[78:81], v202, v202 op_sel_hi:[0,0,0]
	v_mfma_scale_f32_16x16x128_f8f6f4 v[102:105], v[172:179], v[2:9], v[102:105], v202, v202 op_sel_hi:[0,0,0]
	v_mfma_scale_f32_16x16x128_f8f6f4 v[70:73], v[172:179], v[10:17], v[218:221], v202, v202 op_sel_hi:[0,0,0]
	s_add_u32 s98, s48, s66
	s_addc_u32 s99, s49, s67
	s_mov_b32 m0, s17
	v_mfma_scale_f32_16x16x128_f8f6f4 v[106:109], v[180:187], v[2:9], v[106:109], v202, v202 op_sel_hi:[0,0,0]
	global_load_lds_dwordx4 v136, s[98:99]
	v_mfma_scale_f32_16x16x128_f8f6f4 v[74:77], v[180:187], v[10:17], v[222:225], v202, v202 op_sel_hi:[0,0,0]
	v_mfma_scale_f32_16x16x128_f8f6f4 v[94:97], v[188:195], v[2:9], v[94:97], v202, v202 op_sel_hi:[0,0,0]
	s_mov_b32 m0, s18
	v_mfma_scale_f32_16x16x128_f8f6f4 v[62:65], v[188:195], v[10:17], v[62:65], v202, v202 op_sel_hi:[0,0,0]
	global_load_lds_dwordx4 v137, s[98:99]
	s_setprio 0
	s_barrier
	s_add_u32 s34, s46, 0x40080
	s_addc_u32 s35, s47, 0
	v_mov_b32_e32 v0, v136
	s_add_i32 s31, s33, s73
	s_nop 0
	v_mov_b32_e32 v0, v137
	s_nop 0
	s_waitcnt vmcnt(4)
	s_barrier
	s_setprio 1
	v_mfma_scale_f32_16x16x128_f8f6f4 v[46:49], v[156:163], v[140:147], v[226:229], v202, v202 op_sel_hi:[0,0,0]
	v_mfma_scale_f32_16x16x128_f8f6f4 v[14:17], v[156:163], v[148:155], v[230:233], v202, v202 op_sel_hi:[0,0,0]
	v_mfma_scale_f32_16x16x128_f8f6f4 v[34:37], v[172:179], v[140:147], v[34:37], v202, v202 op_sel_hi:[0,0,0]
	v_mfma_scale_f32_16x16x128_f8f6f4 v[6:9], v[172:179], v[148:155], v[234:237], v202, v202 op_sel_hi:[0,0,0]
	s_mov_b32 m0, s31
	v_mfma_scale_f32_16x16x128_f8f6f4 v[42:45], v[180:187], v[140:147], v[238:241], v202, v202 op_sel_hi:[0,0,0]
	global_load_lds_dwordx4 v136, s[34:35]
	v_mfma_scale_f32_16x16x128_f8f6f4 v[10:13], v[180:187], v[148:155], v[242:245], v202, v202 op_sel_hi:[0,0,0]
	v_mfma_scale_f32_16x16x128_f8f6f4 v[26:29], v[188:195], v[140:147], v[246:249], v202, v202 op_sel_hi:[0,0,0]
	s_add_i32 m0, s31, 0x2000
	v_mfma_scale_f32_16x16x128_f8f6f4 v[2:5], v[188:195], v[148:155], v[50:53], v202, v202 op_sel_hi:[0,0,0]
	global_load_lds_dwordx4 v137, s[34:35]
	s_setprio 0
	s_add_i32 s30, s30, 2
	s_add_u32 s26, s26, 0x100
	s_addc_u32 s27, s27, 0
	s_add_u32 s22, s22, 0x100
	s_addc_u32 s25, s25, 0
	s_cmp_gt_u32 s30, 13
	s_barrier
	s_cbranch_scc0 .LBB0_249
	s_mul_hi_i32 s3, s24, 0x2aaaaaab
	s_lshr_b32 s5, s3, 31
	s_lshr_b32 s3, s3, 1
	s_add_i32 s3, s3, s5
	s_lshl_b32 s5, s24, 1
	s_and_b32 s5, s5, 6
	s_and_b32 s20, s12, -16
	s_lshl_b32 s3, s3, 3
	s_or_b32 s5, s5, s20
	s_add_i32 s24, s5, s3
	v_readlane_b32 s3, v252, 41
	v_mbcnt_lo_u32_b32 v0, -1, 0
	v_mbcnt_hi_u32_b32 v0, -1, v0
	s_ashr_i32 s25, s24, 31
	s_lshl_b64 s[20:21], s[24:25], 19
	v_and_or_b32 v51, v0, 15, s3
	s_lshl_b32 s3, s12, 8
	s_and_b32 s22, s3, 0xf00
	v_ashrrev_i32_e32 v50, 4, v0
	s_add_u32 s20, s87, s20
	v_readlane_b32 s3, v252, 59
	v_lshlrev_b32_e32 v0, 5, v50
	v_lshlrev_b32_e32 v50, 3, v50
	v_lshlrev_b32_e32 v132, 12, v51
	v_mov_b32_e32 v133, v1
	s_addc_u32 s21, s3, s21
	v_and_b32_e32 v130, -16, v50
	v_lshl_add_u64 v[50:51], s[20:21], 0, v[132:133]
	v_lshl_add_u64 v[50:51], v[50:51], 0, s[22:23]
	v_and_b32_e32 v0, 32, v0
	v_lshl_add_u64 v[50:51], v[50:51], 0, s[28:29]
	v_pk_mul_f32 v[52:53], v[126:127], s[68:69] op_sel_hi:[1,0]
	v_mov_b32_e32 v126, v1
	v_ashrrev_i32_e32 v131, 31, v130
	v_lshl_add_u64 v[50:51], v[50:51], 0, v[0:1]
	v_cvt_pk_fp8_f32 v126, v52, v53
	v_pk_mul_f32 v[52:53], v[122:123], s[68:69] op_sel_hi:[1,0]
	v_mov_b32_e32 v127, v1
	v_lshl_add_u64 v[134:135], v[50:51], 0, v[130:131]
	v_pk_mul_f32 v[50:51], v[128:129], s[68:69] op_sel_hi:[1,0]
	v_cvt_pk_fp8_f32 v127, v52, v53
	v_pk_mul_f32 v[52:53], v[118:119], s[68:69] op_sel_hi:[1,0]
	v_mov_b32_e32 v128, v1
	v_cvt_pk_fp8_f32 v128, v52, v53
	v_pk_mul_f32 v[52:53], v[114:115], s[68:69] op_sel_hi:[1,0]
	v_mov_b32_e32 v129, v1
	v_cvt_pk_fp8_f32 v129, v52, v53
	v_cvt_pk_fp8_f32 v126, v50, v51 op_sel:[0,0,1]
	v_pk_mul_f32 v[50:51], v[124:125], s[68:69] op_sel_hi:[1,0]
	v_pk_mul_f32 v[52:53], v[110:111], s[68:69] op_sel_hi:[1,0]
	v_cvt_pk_fp8_f32 v127, v50, v51 op_sel:[0,0,1]
	v_pk_mul_f32 v[50:51], v[120:121], s[68:69] op_sel_hi:[1,0]
	v_mov_b32_e32 v110, v1
	v_cvt_pk_fp8_f32 v128, v50, v51 op_sel:[0,0,1]
	v_pk_mul_f32 v[50:51], v[116:117], s[68:69] op_sel_hi:[1,0]
	v_cvt_pk_fp8_f32 v110, v52, v53
	v_pk_mul_f32 v[52:53], v[106:107], s[68:69] op_sel_hi:[1,0]
	v_mov_b32_e32 v111, v1
	v_cvt_pk_fp8_f32 v129, v50, v51 op_sel:[0,0,1]
	v_pk_mul_f32 v[50:51], v[112:113], s[68:69] op_sel_hi:[1,0]
	v_cvt_pk_fp8_f32 v111, v52, v53
	v_pk_mul_f32 v[52:53], v[102:103], s[68:69] op_sel_hi:[1,0]
	v_mov_b32_e32 v112, v1
	v_cvt_pk_fp8_f32 v112, v52, v53
	v_cvt_pk_fp8_f32 v110, v50, v51 op_sel:[0,0,1]
	v_pk_mul_f32 v[50:51], v[108:109], s[68:69] op_sel_hi:[1,0]
	v_pk_mul_f32 v[52:53], v[94:95], s[68:69] op_sel_hi:[1,0]
	v_cvt_pk_fp8_f32 v111, v50, v51 op_sel:[0,0,1]
	v_pk_mul_f32 v[50:51], v[104:105], s[68:69] op_sel_hi:[1,0]
	v_mov_b32_e32 v94, v1
	v_cvt_pk_fp8_f32 v112, v50, v51 op_sel:[0,0,1]
	v_pk_mul_f32 v[50:51], v[96:97], s[68:69] op_sel_hi:[1,0]
	v_pk_mul_f32 v[96:97], v[98:99], s[68:69] op_sel_hi:[1,0]
	v_pk_mul_f32 v[90:91], v[90:91], s[68:69] op_sel_hi:[1,0]
	v_cvt_pk_fp8_f32 v94, v96, v97
	v_mov_b32_e32 v95, v1
	v_cvt_pk_fp8_f32 v95, v90, v91
	v_pk_mul_f32 v[86:87], v[86:87], s[68:69] op_sel_hi:[1,0]
	v_mov_b32_e32 v96, v1
	v_mov_b32_e32 v113, v1
	v_cvt_pk_fp8_f32 v96, v86, v87
	v_pk_mul_f32 v[82:83], v[82:83], s[68:69] op_sel_hi:[1,0]
	v_mov_b32_e32 v97, v1
	v_cvt_pk_fp8_f32 v113, v52, v53
	v_pk_mul_f32 v[52:53], v[100:101], s[68:69] op_sel_hi:[1,0]
	v_cvt_pk_fp8_f32 v97, v82, v83
	v_cvt_pk_fp8_f32 v94, v52, v53 op_sel:[0,0,1]
	v_pk_mul_f32 v[52:53], v[92:93], s[68:69] op_sel_hi:[1,0]
	s_mov_b32 s5, 0x10000
	v_cvt_pk_fp8_f32 v95, v52, v53 op_sel:[0,0,1]
	v_pk_mul_f32 v[52:53], v[88:89], s[68:69] op_sel_hi:[1,0]
	v_pk_mul_f32 v[74:75], v[74:75], s[68:69] op_sel_hi:[1,0]
	v_cvt_pk_fp8_f32 v96, v52, v53 op_sel:[0,0,1]
	v_pk_mul_f32 v[52:53], v[84:85], s[68:69] op_sel_hi:[1,0]
	v_permlane32_swap_b32_e32 v94, v95
	v_cvt_pk_fp8_f32 v97, v52, v53 op_sel:[0,0,1]
	v_add_co_u32_e32 v52, vcc, s5, v134
	v_pk_mul_f32 v[70:71], v[70:71], s[68:69] op_sel_hi:[1,0]
	v_permlane32_swap_b32_e32 v96, v97
	v_addc_co_u32_e32 v53, vcc, 0, v135, vcc
	global_store_dwordx4 v[52:53], v[94:97], off
	v_pk_mul_f32 v[52:53], v[80:81], s[68:69] op_sel_hi:[1,0]
	v_pk_mul_f32 v[80:81], v[78:79], s[68:69] op_sel_hi:[1,0]
	v_mov_b32_e32 v78, v1
	v_cvt_pk_fp8_f32 v78, v80, v81
	v_mov_b32_e32 v79, v1
	v_cvt_pk_fp8_f32 v79, v74, v75
	v_mov_b32_e32 v80, v1
	v_cvt_pk_fp8_f32 v80, v70, v71
	v_pk_mul_f32 v[62:63], v[62:63], s[68:69] op_sel_hi:[1,0]
	v_mov_b32_e32 v81, v1
	v_cvt_pk_fp8_f32 v81, v62, v63
	v_cvt_pk_fp8_f32 v78, v52, v53 op_sel:[0,0,1]
	v_pk_mul_f32 v[52:53], v[76:77], s[68:69] op_sel_hi:[1,0]
	v_pk_mul_f32 v[18:19], v[18:19], s[68:69] op_sel_hi:[1,0]
	v_cvt_pk_fp8_f32 v79, v52, v53 op_sel:[0,0,1]
	v_pk_mul_f32 v[52:53], v[72:73], s[68:69] op_sel_hi:[1,0]
	v_pk_mul_f32 v[20:21], v[20:21], s[68:69] op_sel_hi:[1,0]
	v_cvt_pk_fp8_f32 v80, v52, v53 op_sel:[0,0,1]
	v_pk_mul_f32 v[52:53], v[64:65], s[68:69] op_sel_hi:[1,0]
	s_or_b32 s20, s24, 1
	v_cvt_pk_fp8_f32 v81, v52, v53 op_sel:[0,0,1]
	v_pk_mul_f32 v[52:53], v[66:67], s[68:69] op_sel_hi:[1,0]
	v_mov_b32_e32 v67, v1
	v_cvt_pk_fp8_f32 v67, v18, v19
	v_pk_mul_f32 v[18:19], v[48:49], s[68:69] op_sel_hi:[1,0]
	v_mov_b32_e32 v48, v1
	s_ashr_i32 s21, s20, 31
	v_cvt_pk_fp8_f32 v67, v20, v21 op_sel:[0,0,1]
	v_pk_mul_f32 v[20:21], v[46:47], s[68:69] op_sel_hi:[1,0]
	v_mov_b32_e32 v46, v1
	v_cvt_pk_fp8_f32 v46, v20, v21
	v_pk_mul_f32 v[20:21], v[42:43], s[68:69] op_sel_hi:[1,0]
	v_mov_b32_e32 v47, v1
	v_cvt_pk_fp8_f32 v47, v20, v21
	v_pk_mul_f32 v[20:21], v[34:35], s[68:69] op_sel_hi:[1,0]
	v_cvt_pk_fp8_f32 v46, v18, v19 op_sel:[0,0,1]
	v_cvt_pk_fp8_f32 v48, v20, v21
	v_pk_mul_f32 v[18:19], v[44:45], s[68:69] op_sel_hi:[1,0]
	v_pk_mul_f32 v[20:21], v[26:27], s[68:69] op_sel_hi:[1,0]
	v_cvt_pk_fp8_f32 v47, v18, v19 op_sel:[0,0,1]
	v_pk_mul_f32 v[18:19], v[36:37], s[68:69] op_sel_hi:[1,0]
	v_mov_b32_e32 v26, v1
	v_cvt_pk_fp8_f32 v48, v18, v19 op_sel:[0,0,1]
	v_pk_mul_f32 v[18:19], v[28:29], s[68:69] op_sel_hi:[1,0]
	v_pk_mul_f32 v[28:29], v[38:39], s[68:69] op_sel_hi:[1,0]
	v_mov_b32_e32 v27, v1
	v_cvt_pk_fp8_f32 v26, v28, v29
	v_pk_mul_f32 v[28:29], v[30:31], s[68:69] op_sel_hi:[1,0]
	v_pk_mul_f32 v[22:23], v[22:23], s[68:69] op_sel_hi:[1,0]
	v_cvt_pk_fp8_f32 v27, v28, v29
	v_mov_b32_e32 v28, v1
	s_lshl_b64 s[20:21], s[20:21], 19
	v_mov_b32_e32 v49, v1
	v_cvt_pk_fp8_f32 v28, v22, v23
	v_pk_mul_f32 v[22:23], v[164:165], s[68:69] op_sel_hi:[1,0]
	v_mov_b32_e32 v29, v1
	s_mov_b64 s[26:27], 0x10000
	s_add_u32 s20, s87, s20
	v_cvt_pk_fp8_f32 v49, v20, v21
	v_pk_mul_f32 v[20:21], v[40:41], s[68:69] op_sel_hi:[1,0]
	v_cvt_pk_fp8_f32 v29, v22, v23
	v_cvt_pk_fp8_f32 v113, v50, v51 op_sel:[0,0,1]
	v_lshl_add_u64 v[50:51], v[134:135], 0, s[26:27]
	v_permlane32_swap_b32_e32 v78, v79
	v_permlane32_swap_b32_e32 v80, v81
	s_addc_u32 s21, s3, s21
	v_cvt_pk_fp8_f32 v26, v20, v21 op_sel:[0,0,1]
	v_pk_mul_f32 v[20:21], v[32:33], s[68:69] op_sel_hi:[1,0]
	global_store_dwordx4 v[50:51], v[78:81], off offset:128
	v_lshl_add_u64 v[50:51], s[20:21], 0, v[132:133]
	v_cvt_pk_fp8_f32 v27, v20, v21 op_sel:[0,0,1]
	v_pk_mul_f32 v[20:21], v[24:25], s[68:69] op_sel_hi:[1,0]
	v_lshl_add_u64 v[50:51], v[50:51], 0, s[22:23]
	v_cvt_pk_fp8_f32 v28, v20, v21 op_sel:[0,0,1]
	v_pk_mul_f32 v[20:21], v[166:167], s[68:69] op_sel_hi:[1,0]
	v_lshl_add_u64 v[50:51], v[50:51], 0, s[28:29]
	v_cvt_pk_fp8_f32 v29, v20, v21 op_sel:[0,0,1]
	v_lshl_add_u64 v[50:51], v[50:51], 0, v[0:1]
	v_lshl_add_u64 v[62:63], v[50:51], 0, v[130:131]
	v_add_co_u32_e32 v20, vcc, s5, v62
	v_permlane32_swap_b32_e32 v26, v27
	v_permlane32_swap_b32_e32 v28, v29
	v_addc_co_u32_e32 v21, vcc, 0, v63, vcc
	global_store_dwordx4 v[20:21], v[26:29], off
	v_pk_mul_f32 v[20:21], v[14:15], s[68:69] op_sel_hi:[1,0]
	v_mov_b32_e32 v14, v1
	v_cvt_pk_fp8_f32 v14, v20, v21
	v_mov_b32_e32 v64, v1
	v_cvt_pk_fp8_f32 v64, v52, v53
	v_pk_mul_f32 v[52:53], v[58:59], s[68:69] op_sel_hi:[1,0]
	v_mov_b32_e32 v65, v1
	v_pk_mul_f32 v[16:17], v[16:17], s[68:69] op_sel_hi:[1,0]
	v_cvt_pk_fp8_f32 v65, v52, v53
	v_pk_mul_f32 v[52:53], v[54:55], s[68:69] op_sel_hi:[1,0]
	v_mov_b32_e32 v66, v1
	v_cvt_pk_fp8_f32 v14, v16, v17 op_sel:[0,0,1]
	v_pk_mul_f32 v[10:11], v[10:11], s[68:69] op_sel_hi:[1,0]
	v_mov_b32_e32 v15, v1
	v_pk_mul_f32 v[6:7], v[6:7], s[68:69] op_sel_hi:[1,0]
	v_mov_b32_e32 v16, v1
	v_pk_mul_f32 v[2:3], v[2:3], s[68:69] op_sel_hi:[1,0]
	v_mov_b32_e32 v17, v1
	v_cvt_pk_fp8_f32 v66, v52, v53
	v_cvt_pk_fp8_f32 v15, v10, v11
	v_cvt_pk_fp8_f32 v16, v6, v7
	v_cvt_pk_fp8_f32 v17, v2, v3
	v_pk_mul_f32 v[50:51], v[68:69], s[68:69] op_sel_hi:[1,0]
	v_pk_mul_f32 v[12:13], v[12:13], s[68:69] op_sel_hi:[1,0]
	v_cvt_pk_fp8_f32 v64, v50, v51 op_sel:[0,0,1]
	v_pk_mul_f32 v[50:51], v[60:61], s[68:69] op_sel_hi:[1,0]
	v_pk_mul_f32 v[8:9], v[8:9], s[68:69] op_sel_hi:[1,0]
	v_cvt_pk_fp8_f32 v65, v50, v51 op_sel:[0,0,1]
	v_pk_mul_f32 v[50:51], v[56:57], s[68:69] op_sel_hi:[1,0]
	v_pk_mul_f32 v[4:5], v[4:5], s[68:69] op_sel_hi:[1,0]
	v_cvt_pk_fp8_f32 v66, v50, v51 op_sel:[0,0,1]
	v_cvt_pk_fp8_f32 v49, v18, v19 op_sel:[0,0,1]
	v_cvt_pk_fp8_f32 v15, v12, v13 op_sel:[0,0,1]
	v_cvt_pk_fp8_f32 v16, v8, v9 op_sel:[0,0,1]
	v_cvt_pk_fp8_f32 v17, v4, v5 op_sel:[0,0,1]
	v_permlane32_swap_b32_e32 v126, v127
	v_permlane32_swap_b32_e32 v128, v129
	v_permlane32_swap_b32_e32 v110, v111
	v_permlane32_swap_b32_e32 v112, v113
	v_permlane32_swap_b32_e32 v64, v65
	v_permlane32_swap_b32_e32 v66, v67
	v_permlane32_swap_b32_e32 v46, v47
	v_permlane32_swap_b32_e32 v48, v49
	v_lshl_add_u64 v[18:19], v[62:63], 0, s[26:27]
	v_permlane32_swap_b32_e32 v14, v15
	v_permlane32_swap_b32_e32 v16, v17
	s_and_b64 vcc, exec, s[10:11]
	s_mov_b32 s12, s2
	s_mov_b32 s24, s4
	s_mov_b64 s[46:47], s[8:9]
	s_mov_b64 s[26:27], s[6:7]
	global_store_dwordx4 v[134:135], v[126:129], off
	global_store_dwordx4 v[134:135], v[110:113], off offset:128
	global_store_dwordx4 v[62:63], v[64:67], off
	global_store_dwordx4 v[62:63], v[46:49], off offset:128
	global_store_dwordx4 v[18:19], v[14:17], off offset:128
	s_cbranch_vccz .LBB0_241
	v_readlane_b32 s0, v252, 50
	s_waitcnt vmcnt(0)
	v_readlane_b32 s1, v252, 51
	s_andn2_b64 vcc, exec, s[0:1]
	s_cbranch_vccnz .LBB0_253
	s_barrier

.LBB0_278:
	s_add_u32 s6, s4, 0xfffc0080
	s_addc_u32 s7, s5, -1
	s_add_i32 s25, 0, 0x10000
	v_add_u32_e32 v0, s25, v207
	ds_read_b128 v[52:55], v0
	ds_read_b128 v[56:59], v0 offset:1024
	ds_read_b128 v[68:71], v0 offset:2048
	ds_read_b128 v[72:75], v0 offset:3072
	s_cmp_eq_u32 s17, 12
	s_cselect_b32 s11, s3, s7
	s_cselect_b32 s10, s9, s6
	s_cselect_b32 s7, s12, s16
	s_cselect_b32 s6, s13, s15
	v_mov_b32_e32 v0, v205
	ds_read_b128 v[84:87], v208
	ds_read_b128 v[88:91], v208 offset:1024
	ds_read_b128 v[92:95], v208 offset:2048
	ds_read_b128 v[96:99], v208 offset:3072
	ds_read_b128 v[172:175], v208 offset:4096
	ds_read_b128 v[176:179], v208 offset:5120
	ds_read_b128 v[180:183], v208 offset:6144
	ds_read_b128 v[184:187], v208 offset:7168
	s_nop 0
	v_mov_b32_e32 v0, v206
	s_nop 0
	s_waitcnt lgkmcnt(8)
	s_barrier
	s_waitcnt lgkmcnt(0)
	s_setprio 1
	s_waitcnt lgkmcnt(0)
	v_mfma_scale_f32_16x16x128_f8f6f4 v[164:167], v[52:59], v[84:91], v[164:167], v202, v202 op_sel_hi:[0,0,0]
	v_mfma_scale_f32_16x16x128_f8f6f4 v[160:163], v[68:75], v[84:91], v[160:163], v202, v202 op_sel_hi:[0,0,0]
	v_mfma_scale_f32_16x16x128_f8f6f4 v[156:159], v[52:59], v[92:99], v[156:159], v202, v202 op_sel_hi:[0,0,0]
	v_mfma_scale_f32_16x16x128_f8f6f4 v[152:155], v[68:75], v[92:99], v[152:155], v202, v202 op_sel_hi:[0,0,0]
	s_add_i32 m0, s18, 0xc000
	v_mfma_scale_f32_16x16x128_f8f6f4 v[148:151], v[52:59], v[172:179], v[148:151], v202, v202 op_sel_hi:[0,0,0]
	global_load_lds_dwordx4 v205, s[4:5]
	v_mfma_scale_f32_16x16x128_f8f6f4 v[188:191], v[68:75], v[172:179], v[144:147], v202, v202 op_sel_hi:[0,0,0]
	v_mfma_scale_f32_16x16x128_f8f6f4 v[192:195], v[52:59], v[180:187], v[136:139], v202, v202 op_sel_hi:[0,0,0]
	s_add_i32 m0, s18, 0xe000
	v_mfma_scale_f32_16x16x128_f8f6f4 v[196:199], v[68:75], v[180:187], v[132:135], v202, v202 op_sel_hi:[0,0,0]
	global_load_lds_dwordx4 v206, s[4:5]
	s_setprio 0
	s_barrier
	s_add_i32 s30, 0, 0x14000
	v_add_u32_e32 v0, s30, v207
	s_nop 2
	ds_read_b128 v[132:135], v0
	ds_read_b128 v[136:139], v0 offset:1024
	ds_read_b128 v[140:143], v0 offset:2048
	ds_read_b128 v[144:147], v0 offset:3072
	v_mov_b32_e32 v0, v205
	s_add_i32 s25, s25, s73
	s_nop 0
	v_mov_b32_e32 v0, v206
	s_nop 0
	s_barrier
	s_waitcnt lgkmcnt(0)
	s_setprio 1
	s_waitcnt lgkmcnt(0)
	v_mfma_scale_f32_16x16x128_f8f6f4 v[128:131], v[132:139], v[84:91], v[128:131], v202, v202 op_sel_hi:[0,0,0]
	v_mfma_scale_f32_16x16x128_f8f6f4 v[124:127], v[140:147], v[84:91], v[124:127], v202, v202 op_sel_hi:[0,0,0]
	v_mfma_scale_f32_16x16x128_f8f6f4 v[120:123], v[132:139], v[92:99], v[120:123], v202, v202 op_sel_hi:[0,0,0]
	v_mfma_scale_f32_16x16x128_f8f6f4 v[116:119], v[140:147], v[92:99], v[116:119], v202, v202 op_sel_hi:[0,0,0]
	s_mov_b32 m0, s25
	v_mfma_scale_f32_16x16x128_f8f6f4 v[210:213], v[132:139], v[172:179], v[112:115], v202, v202 op_sel_hi:[0,0,0]
	global_load_lds_dwordx4 v205, s[6:7]
	v_mfma_scale_f32_16x16x128_f8f6f4 v[172:175], v[140:147], v[172:179], v[108:111], v202, v202 op_sel_hi:[0,0,0]
	v_mfma_scale_f32_16x16x128_f8f6f4 v[176:179], v[132:139], v[180:187], v[104:107], v202, v202 op_sel_hi:[0,0,0]
	s_add_i32 m0, s25, 0x2000
	v_mfma_scale_f32_16x16x128_f8f6f4 v[180:183], v[140:147], v[180:187], v[100:103], v202, v202 op_sel_hi:[0,0,0]
	global_load_lds_dwordx4 v206, s[6:7]
	s_setprio 0
	v_mov_b32_e32 v0, v205
	s_barrier
	ds_read_b128 v[84:87], v208 offset:16384
	ds_read_b128 v[88:91], v208 offset:17408
	ds_read_b128 v[92:95], v208 offset:18432
	ds_read_b128 v[96:99], v208 offset:19456
	ds_read_b128 v[100:103], v208 offset:20480
	ds_read_b128 v[104:107], v208 offset:21504
	ds_read_b128 v[108:111], v208 offset:22528
	ds_read_b128 v[112:115], v208 offset:23552
	s_nop 0
	v_mov_b32_e32 v0, v206
	s_nop 0
	s_barrier
	s_waitcnt lgkmcnt(0)
	s_setprio 1
	s_waitcnt lgkmcnt(0)
	v_mfma_scale_f32_16x16x128_f8f6f4 v[80:83], v[52:59], v[84:91], v[80:83], v202, v202 op_sel_hi:[0,0,0]
	v_mfma_scale_f32_16x16x128_f8f6f4 v[76:79], v[68:75], v[84:91], v[76:79], v202, v202 op_sel_hi:[0,0,0]
	v_mfma_scale_f32_16x16x128_f8f6f4 v[64:67], v[52:59], v[92:99], v[64:67], v202, v202 op_sel_hi:[0,0,0]
	v_mfma_scale_f32_16x16x128_f8f6f4 v[60:63], v[68:75], v[92:99], v[60:63], v202, v202 op_sel_hi:[0,0,0]
	s_mov_b32 m0, s18
	v_mfma_scale_f32_16x16x128_f8f6f4 v[184:187], v[52:59], v[100:107], v[48:51], v202, v202 op_sel_hi:[0,0,0]
	global_load_lds_dwordx4 v205, s[10:11]
	v_mfma_scale_f32_16x16x128_f8f6f4 v[214:217], v[68:75], v[100:107], v[44:47], v202, v202 op_sel_hi:[0,0,0]
	v_mfma_scale_f32_16x16x128_f8f6f4 v[218:221], v[52:59], v[108:115], v[40:43], v202, v202 op_sel_hi:[0,0,0]
	s_mov_b32 m0, s19
	v_mfma_scale_f32_16x16x128_f8f6f4 v[222:225], v[68:75], v[108:115], v[36:39], v202, v202 op_sel_hi:[0,0,0]
	global_load_lds_dwordx4 v206, s[10:11]
	s_setprio 0
	s_barrier
	s_add_u32 s26, s6, 0x40000
	s_addc_u32 s27, s7, 0
	v_mov_b32_e32 v0, v205
	s_add_i32 s25, s30, s73
	s_mov_b32 s100, s25
	s_nop 0
	v_mov_b32_e32 v0, v206
	s_add_i32 s101, s25, 0x2000
	s_nop 0
	s_waitcnt vmcnt(4)
	s_barrier
	s_setprio 1
	v_mfma_scale_f32_16x16x128_f8f6f4 v[226:229], v[132:139], v[84:91], v[32:35], v202, v202 op_sel_hi:[0,0,0]
	v_mfma_scale_f32_16x16x128_f8f6f4 v[230:233], v[140:147], v[84:91], v[28:31], v202, v202 op_sel_hi:[0,0,0]
	v_mfma_scale_f32_16x16x128_f8f6f4 v[234:237], v[132:139], v[92:99], v[24:27], v202, v202 op_sel_hi:[0,0,0]
	v_mfma_scale_f32_16x16x128_f8f6f4 v[238:241], v[140:147], v[92:99], v[20:23], v202, v202 op_sel_hi:[0,0,0]
	s_mov_b32 m0, s100
	v_mfma_scale_f32_16x16x128_f8f6f4 v[242:245], v[132:139], v[100:107], v[16:19], v202, v202 op_sel_hi:[0,0,0]
	global_load_lds_dwordx4 v205, s[26:27]
	v_mfma_scale_f32_16x16x128_f8f6f4 v[246:249], v[140:147], v[100:107], v[12:15], v202, v202 op_sel_hi:[0,0,0]
	v_mfma_scale_f32_16x16x128_f8f6f4 v[168:171], v[132:139], v[108:115], v[8:11], v202, v202 op_sel_hi:[0,0,0]
	s_mov_b32 m0, s101
	v_mfma_scale_f32_16x16x128_f8f6f4 v[140:143], v[140:147], v[108:115], v[4:7], v202, v202 op_sel_hi:[0,0,0]
	global_load_lds_dwordx4 v206, s[26:27]
	s_setprio 0
	s_add_i32 s25, 0, 0x18000
	v_add_u32_e32 v0, s25, v207
	s_barrier
	s_nop 2
	ds_read_b128 v[2:5], v0
	ds_read_b128 v[6:9], v0 offset:1024
	ds_read_b128 v[10:13], v0 offset:2048
	ds_read_b128 v[14:17], v0 offset:3072
	s_add_u32 s26, s10, 0x40000
	v_mov_b32_e32 v0, v205
	ds_read_b128 v[18:21], v208 offset:32768
	ds_read_b128 v[22:25], v208 offset:33792
	ds_read_b128 v[26:29], v208 offset:34816
	ds_read_b128 v[30:33], v208 offset:35840
	ds_read_b128 v[34:37], v208 offset:36864
	ds_read_b128 v[38:41], v208 offset:37888
	ds_read_b128 v[42:45], v208 offset:38912
	ds_read_b128 v[46:49], v208 offset:39936
	s_addc_u32 s27, s11, 0
	s_nop 0
	v_mov_b32_e32 v0, v206
	s_nop 0
	s_waitcnt lgkmcnt(8)
	s_barrier
	s_waitcnt lgkmcnt(0)
	s_setprio 1
	s_waitcnt lgkmcnt(0)
	v_mfma_scale_f32_16x16x128_f8f6f4 v[164:167], v[2:9], v[18:25], v[164:167], v202, v202 op_sel_hi:[0,0,0]
	v_mfma_scale_f32_16x16x128_f8f6f4 v[160:163], v[10:17], v[18:25], v[160:163], v202, v202 op_sel_hi:[0,0,0]
	v_mfma_scale_f32_16x16x128_f8f6f4 v[156:159], v[2:9], v[26:33], v[156:159], v202, v202 op_sel_hi:[0,0,0]
	v_mfma_scale_f32_16x16x128_f8f6f4 v[152:155], v[10:17], v[26:33], v[152:155], v202, v202 op_sel_hi:[0,0,0]
	s_mov_b32 m0, s20
	v_mfma_scale_f32_16x16x128_f8f6f4 v[148:151], v[2:9], v[34:41], v[148:151], v202, v202 op_sel_hi:[0,0,0]
	global_load_lds_dwordx4 v205, s[26:27]
	v_mfma_scale_f32_16x16x128_f8f6f4 v[144:147], v[10:17], v[34:41], v[188:191], v202, v202 op_sel_hi:[0,0,0]
	v_mfma_scale_f32_16x16x128_f8f6f4 v[136:139], v[2:9], v[42:49], v[192:195], v202, v202 op_sel_hi:[0,0,0]
	s_mov_b32 m0, s21
	v_mfma_scale_f32_16x16x128_f8f6f4 v[132:135], v[10:17], v[42:49], v[196:199], v202, v202 op_sel_hi:[0,0,0]
	global_load_lds_dwordx4 v206, s[26:27]
	s_setprio 0
	s_barrier
	s_add_i32 s26, 0, 0x1c000
	v_add_u32_e32 v0, s26, v207
	ds_read_b128 v[52:55], v0
	ds_read_b128 v[56:59], v0 offset:1024
	ds_read_b128 v[68:71], v0 offset:2048
	ds_read_b128 v[72:75], v0 offset:3072
	v_mov_b32_e32 v0, v205
	s_add_i32 s25, s25, s73
	v_lshl_add_u64 v[50:51], s[6:7], 0, v[0:1]
	v_lshl_add_u64 v[50:51], v[50:51], 0, s[66:67]
	v_mov_b32_e32 v0, v206
	v_lshl_add_u64 v[50:51], s[6:7], 0, v[0:1]
	v_lshl_add_u64 v[50:51], v[50:51], 0, s[66:67]
	s_barrier
	s_waitcnt lgkmcnt(0)
	s_setprio 1
	s_waitcnt lgkmcnt(0)
	v_mfma_scale_f32_16x16x128_f8f6f4 v[128:131], v[52:59], v[18:25], v[128:131], v202, v202 op_sel_hi:[0,0,0]
	v_mfma_scale_f32_16x16x128_f8f6f4 v[124:127], v[68:75], v[18:25], v[124:127], v202, v202 op_sel_hi:[0,0,0]
	v_mfma_scale_f32_16x16x128_f8f6f4 v[120:123], v[52:59], v[26:33], v[120:123], v202, v202 op_sel_hi:[0,0,0]
	v_mfma_scale_f32_16x16x128_f8f6f4 v[116:119], v[68:75], v[26:33], v[116:119], v202, v202 op_sel_hi:[0,0,0]
	s_add_u32 s98, s6, s66
	s_addc_u32 s99, s7, s67
	s_mov_b32 m0, s25
	v_mfma_scale_f32_16x16x128_f8f6f4 v[112:115], v[52:59], v[34:41], v[210:213], v202, v202 op_sel_hi:[0,0,0]
	global_load_lds_dwordx4 v205, s[98:99]
	v_mfma_scale_f32_16x16x128_f8f6f4 v[108:111], v[68:75], v[34:41], v[172:175], v202, v202 op_sel_hi:[0,0,0]
	v_mfma_scale_f32_16x16x128_f8f6f4 v[104:107], v[52:59], v[42:49], v[176:179], v202, v202 op_sel_hi:[0,0,0]
	s_add_i32 m0, s25, 0x2000
	v_mfma_scale_f32_16x16x128_f8f6f4 v[100:103], v[68:75], v[42:49], v[180:183], v202, v202 op_sel_hi:[0,0,0]
	global_load_lds_dwordx4 v206, s[98:99]
	s_setprio 0
	v_mov_b32_e32 v0, v205
	s_barrier
	ds_read_b128 v[18:21], v208 offset:49152
	ds_read_b128 v[22:25], v208 offset:50176
	ds_read_b128 v[84:87], v208 offset:51200
	ds_read_b128 v[88:91], v208 offset:52224
	ds_read_b128 v[92:95], v208 offset:53248
	ds_read_b128 v[96:99], v208 offset:54272
	ds_read_b128 v[172:175], v208 offset:55296
	ds_read_b128 v[176:179], v208 offset:56320
	v_lshl_add_u64 v[26:27], s[10:11], 0, v[0:1]
	v_lshl_add_u64 v[26:27], v[26:27], 0, s[66:67]
	v_mov_b32_e32 v0, v206
	v_lshl_add_u64 v[26:27], s[10:11], 0, v[0:1]
	v_lshl_add_u64 v[26:27], v[26:27], 0, s[66:67]
	s_barrier
	s_waitcnt lgkmcnt(0)
	s_setprio 1
	s_waitcnt lgkmcnt(0)
	v_mfma_scale_f32_16x16x128_f8f6f4 v[80:83], v[2:9], v[18:25], v[80:83], v202, v202 op_sel_hi:[0,0,0]
	v_mfma_scale_f32_16x16x128_f8f6f4 v[76:79], v[10:17], v[18:25], v[76:79], v202, v202 op_sel_hi:[0,0,0]
	v_mfma_scale_f32_16x16x128_f8f6f4 v[64:67], v[2:9], v[84:91], v[64:67], v202, v202 op_sel_hi:[0,0,0]
	v_mfma_scale_f32_16x16x128_f8f6f4 v[60:63], v[10:17], v[84:91], v[60:63], v202, v202 op_sel_hi:[0,0,0]
	s_add_u32 s98, s10, s66
	s_addc_u32 s99, s11, s67
	s_mov_b32 m0, s22
	v_mfma_scale_f32_16x16x128_f8f6f4 v[48:51], v[2:9], v[92:99], v[184:187], v202, v202 op_sel_hi:[0,0,0]
	global_load_lds_dwordx4 v205, s[98:99]
	v_mfma_scale_f32_16x16x128_f8f6f4 v[44:47], v[10:17], v[92:99], v[214:217], v202, v202 op_sel_hi:[0,0,0]
	v_mfma_scale_f32_16x16x128_f8f6f4 v[40:43], v[2:9], v[172:179], v[218:221], v202, v202 op_sel_hi:[0,0,0]
	s_mov_b32 m0, s34
	v_mfma_scale_f32_16x16x128_f8f6f4 v[36:39], v[10:17], v[172:179], v[222:225], v202, v202 op_sel_hi:[0,0,0]
	global_load_lds_dwordx4 v206, s[98:99]
	s_setprio 0
	s_barrier
	s_add_u32 s6, s6, 0x40080
	s_addc_u32 s7, s7, 0
	v_mov_b32_e32 v0, v205
	s_add_i32 s10, s26, s73
	s_nop 0
	v_mov_b32_e32 v0, v206
	s_nop 0
	s_waitcnt vmcnt(4)
	s_barrier
	s_setprio 1
	v_mfma_scale_f32_16x16x128_f8f6f4 v[32:35], v[52:59], v[18:25], v[226:229], v202, v202 op_sel_hi:[0,0,0]
	v_mfma_scale_f32_16x16x128_f8f6f4 v[28:31], v[68:75], v[18:25], v[230:233], v202, v202 op_sel_hi:[0,0,0]
	v_mfma_scale_f32_16x16x128_f8f6f4 v[24:27], v[52:59], v[84:91], v[234:237], v202, v202 op_sel_hi:[0,0,0]
	v_mfma_scale_f32_16x16x128_f8f6f4 v[20:23], v[68:75], v[84:91], v[238:241], v202, v202 op_sel_hi:[0,0,0]
	s_mov_b32 m0, s10
	v_mfma_scale_f32_16x16x128_f8f6f4 v[16:19], v[52:59], v[92:99], v[242:245], v202, v202 op_sel_hi:[0,0,0]
	global_load_lds_dwordx4 v205, s[6:7]
	v_mfma_scale_f32_16x16x128_f8f6f4 v[12:15], v[68:75], v[92:99], v[246:249], v202, v202 op_sel_hi:[0,0,0]
	v_mfma_scale_f32_16x16x128_f8f6f4 v[8:11], v[52:59], v[172:179], v[168:171], v202, v202 op_sel_hi:[0,0,0]
	s_add_i32 m0, s10, 0x2000
	v_mfma_scale_f32_16x16x128_f8f6f4 v[4:7], v[68:75], v[172:179], v[140:143], v202, v202 op_sel_hi:[0,0,0]
	global_load_lds_dwordx4 v206, s[6:7]
	s_setprio 0
	s_add_i32 s17, s17, 2
	s_add_u32 s4, s4, 0x100
	s_addc_u32 s5, s5, 0
	s_add_u32 s15, s15, 0x100
	s_addc_u32 s16, s16, 0
	s_cmp_gt_u32 s17, 13
	s_barrier
	s_cbranch_scc0 .LBB0_278
	s_ashr_i32 s3, s8, 2
	s_mul_hi_i32 s4, s3, 0x55555556
	s_lshr_b32 s5, s4, 31
	s_add_i32 s4, s4, s5
	s_mul_i32 s4, s4, 3
	s_sub_i32 s15, s3, s4
	s_add_i32 s3, s8, 11
	s_cmp_lt_u32 s3, 23
	s_cselect_b64 s[12:13], -1, 0
	s_cmp_lt_i32 s15, 2
	v_readlane_b32 s6, v252, 53
	s_cselect_b64 s[4:5], -1, 0
	v_readlane_b32 s7, v252, 54
	s_and_b64 s[4:5], s[6:7], s[4:5]
	v_mbcnt_lo_u32_b32 v211, -1, 0
	v_mbcnt_hi_u32_b32 v211, -1, v211
	s_and_b64 s[6:7], s[12:13], s[4:5]
	v_ashrrev_i32_e32 v210, 4, v211
	s_lshl_b32 s3, s74, 8
	v_lshlrev_b32_e32 v172, 2, v210
	v_mov_b32_e32 v140, 0
	v_cndmask_b32_e64 v0, 0, 1, s[6:7]
	v_and_b32_e32 v209, 15, v211
	s_add_i32 s46, s3, s28
	v_ashrrev_i32_e32 v173, 31, v172
	v_cmp_ne_u32_e64 s[10:11], 1, v0
	s_andn2_b64 vcc, exec, s[6:7]
	v_mov_b32_e32 v141, v140
	v_mov_b32_e32 v142, v140
	v_mov_b32_e32 v143, v140
	v_mov_b32_e32 v92, v140
	v_mov_b32_e32 v93, v140
	v_mov_b32_e32 v94, v140
	v_mov_b32_e32 v95, v140
	v_mov_b32_e32 v88, v140
	v_mov_b32_e32 v89, v140
	v_mov_b32_e32 v90, v140
	v_mov_b32_e32 v91, v140
	v_mov_b32_e32 v72, v140
	v_mov_b32_e32 v73, v140
	v_mov_b32_e32 v74, v140
	v_mov_b32_e32 v75, v140
	v_mov_b32_e32 v56, v140
	v_mov_b32_e32 v57, v140
	v_mov_b32_e32 v58, v140
	v_mov_b32_e32 v59, v140
	s_cbranch_vccnz .LBB0_281
	s_and_b32 s3, s46, 0xfc0
	v_readlane_b32 s4, v252, 31
	v_or_b32_e32 v0, s3, v209
	v_readlane_b32 s5, v252, 32
	v_lshlrev_b32_e32 v0, 7, v0
	s_movk_i32 s3, 0x1000
	v_lshl_add_u64 v[2:3], v[172:173], 2, s[4:5]
	v_lshl_add_u64 v[2:3], v[2:3], 0, v[0:1]
	global_load_dwordx4 v[92:95], v[2:3], off
	global_load_dwordx4 v[96:99], v[2:3], off offset:64
	v_add_co_u32_e32 v52, vcc, s3, v2
	s_nop 1
	v_addc_co_u32_e32 v53, vcc, 0, v3, vcc
	global_load_dwordx4 v[140:143], v[52:53], off offset:2048
	global_load_dwordx4 v[88:91], v[2:3], off offset:2048
	global_load_dwordx4 v[84:87], v[2:3], off offset:2112
	global_load_dwordx4 v[72:75], v[52:53], off
	global_load_dwordx4 v[68:71], v[52:53], off offset:64
	s_nop 0
	global_load_dwordx4 v[52:55], v[52:53], off offset:2112
	s_waitcnt vmcnt(0)
	v_mov_b32_e32 v56, v140
	v_mov_b32_e32 v57, v141
	v_mov_b32_e32 v58, v142
	v_mov_b32_e32 v59, v143

.LBB0_1503:
	s_add_u32 s24, s2, 0xfffc0080
	s_addc_u32 s25, s3, -1
	s_add_i32 s28, 0, 0x10000
	v_add_u32_e32 v128, s28, v150
	ds_read_b128 v[136:139], v128
	ds_read_b128 v[140:143], v128 offset:1024
	ds_read_b128 v[152:155], v128 offset:2048
	ds_read_b128 v[156:159], v128 offset:3072
	s_cmp_eq_u32 s22, 12
	s_cselect_b32 s41, s49, s25
	s_cselect_b32 s40, s48, s24
	s_cselect_b32 s39, s59, s20
	s_cselect_b32 s38, s58, s7
	v_mov_b32_e32 v128, v148
	ds_read_b128 v[160:163], v151
	ds_read_b128 v[164:167], v151 offset:1024
	ds_read_b128 v[168:171], v151 offset:2048
	ds_read_b128 v[172:175], v151 offset:3072
	ds_read_b128 v[176:179], v151 offset:4096
	ds_read_b128 v[180:183], v151 offset:5120
	ds_read_b128 v[184:187], v151 offset:6144
	ds_read_b128 v[188:191], v151 offset:7168
	s_nop 0
	v_mov_b32_e32 v128, v149
	s_nop 0
	s_waitcnt lgkmcnt(8)
	s_barrier
	s_waitcnt lgkmcnt(0)
	s_setprio 1
	s_waitcnt lgkmcnt(0)
	v_mfma_scale_f32_16x16x128_f8f6f4 v[124:127], v[136:143], v[160:167], v[124:127], v146, v146 op_sel_hi:[0,0,0]
	v_mfma_scale_f32_16x16x128_f8f6f4 v[120:123], v[152:159], v[160:167], v[120:123], v146, v146 op_sel_hi:[0,0,0]
	v_mfma_scale_f32_16x16x128_f8f6f4 v[116:119], v[136:143], v[168:175], v[116:119], v146, v146 op_sel_hi:[0,0,0]
	v_mfma_scale_f32_16x16x128_f8f6f4 v[112:115], v[152:159], v[168:175], v[112:115], v146, v146 op_sel_hi:[0,0,0]
	s_add_i32 m0, s0, 0xc000
	v_mfma_scale_f32_16x16x128_f8f6f4 v[128:131], v[136:143], v[176:183], v[108:111], v146, v146 op_sel_hi:[0,0,0]
	global_load_lds_dwordx4 v148, s[2:3]
	v_mfma_scale_f32_16x16x128_f8f6f4 v[192:195], v[152:159], v[176:183], v[104:107], v146, v146 op_sel_hi:[0,0,0]
	v_mfma_scale_f32_16x16x128_f8f6f4 v[196:199], v[136:143], v[184:191], v[100:103], v146, v146 op_sel_hi:[0,0,0]
	s_add_i32 m0, s0, 0xe000
	v_mfma_scale_f32_16x16x128_f8f6f4 v[200:203], v[152:159], v[184:191], v[96:99], v146, v146 op_sel_hi:[0,0,0]
	global_load_lds_dwordx4 v149, s[2:3]
	s_setprio 0
	s_barrier
	s_add_i32 s29, 0, 0x14000
	s_nop 0
	v_add_u32_e32 v108, s29, v150
	v_mov_b32_e32 v132, v148
	s_add_i32 s24, s28, s21
	ds_read_b128 v[96:99], v108
	ds_read_b128 v[100:103], v108 offset:1024
	ds_read_b128 v[104:107], v108 offset:2048
	ds_read_b128 v[108:111], v108 offset:3072
	s_nop 0
	v_mov_b32_e32 v132, v149
	s_nop 0
	s_barrier
	s_waitcnt lgkmcnt(0)
	s_setprio 1
	s_waitcnt lgkmcnt(0)
	v_mfma_scale_f32_16x16x128_f8f6f4 v[204:207], v[96:103], v[160:167], v[60:63], v146, v146 op_sel_hi:[0,0,0]
	v_mfma_scale_f32_16x16x128_f8f6f4 v[160:163], v[104:111], v[160:167], v[56:59], v146, v146 op_sel_hi:[0,0,0]
	v_mfma_scale_f32_16x16x128_f8f6f4 v[164:167], v[96:103], v[168:175], v[52:55], v146, v146 op_sel_hi:[0,0,0]
	v_mfma_scale_f32_16x16x128_f8f6f4 v[168:171], v[104:111], v[168:175], v[48:51], v146, v146 op_sel_hi:[0,0,0]
	s_mov_b32 m0, s24
	v_mfma_scale_f32_16x16x128_f8f6f4 v[172:175], v[96:103], v[176:183], v[44:47], v146, v146 op_sel_hi:[0,0,0]
	global_load_lds_dwordx4 v148, s[38:39]
	v_mfma_scale_f32_16x16x128_f8f6f4 v[176:179], v[104:111], v[176:183], v[40:43], v146, v146 op_sel_hi:[0,0,0]
	v_mfma_scale_f32_16x16x128_f8f6f4 v[180:183], v[96:103], v[184:191], v[36:39], v146, v146 op_sel_hi:[0,0,0]
	s_add_i32 m0, s24, 0x2000
	v_mfma_scale_f32_16x16x128_f8f6f4 v[184:187], v[104:111], v[184:191], v[32:35], v146, v146 op_sel_hi:[0,0,0]
	global_load_lds_dwordx4 v149, s[38:39]
	s_setprio 0
	v_mov_b32_e32 v132, v148
	s_barrier
	s_nop 2
	ds_read_b128 v[32:35], v151 offset:16384
	ds_read_b128 v[36:39], v151 offset:17408
	ds_read_b128 v[40:43], v151 offset:18432
	ds_read_b128 v[44:47], v151 offset:19456
	ds_read_b128 v[48:51], v151 offset:20480
	ds_read_b128 v[52:55], v151 offset:21504
	ds_read_b128 v[56:59], v151 offset:22528
	ds_read_b128 v[60:63], v151 offset:23552
	s_nop 0
	v_mov_b32_e32 v132, v149
	s_nop 0
	s_barrier
	s_waitcnt lgkmcnt(0)
	s_setprio 1
	s_waitcnt lgkmcnt(0)
	v_mfma_scale_f32_16x16x128_f8f6f4 v[92:95], v[136:143], v[32:39], v[92:95], v146, v146 op_sel_hi:[0,0,0]
	v_mfma_scale_f32_16x16x128_f8f6f4 v[88:91], v[152:159], v[32:39], v[88:91], v146, v146 op_sel_hi:[0,0,0]
	v_mfma_scale_f32_16x16x128_f8f6f4 v[84:87], v[136:143], v[40:47], v[84:87], v146, v146 op_sel_hi:[0,0,0]
	v_mfma_scale_f32_16x16x128_f8f6f4 v[80:83], v[152:159], v[40:47], v[80:83], v146, v146 op_sel_hi:[0,0,0]
	s_mov_b32 m0, s0
	v_mfma_scale_f32_16x16x128_f8f6f4 v[76:79], v[136:143], v[48:55], v[76:79], v146, v146 op_sel_hi:[0,0,0]
	global_load_lds_dwordx4 v148, s[40:41]
	v_mfma_scale_f32_16x16x128_f8f6f4 v[72:75], v[152:159], v[48:55], v[72:75], v146, v146 op_sel_hi:[0,0,0]
	v_mfma_scale_f32_16x16x128_f8f6f4 v[188:191], v[136:143], v[56:63], v[68:71], v146, v146 op_sel_hi:[0,0,0]
	s_mov_b32 m0, s1
	v_mfma_scale_f32_16x16x128_f8f6f4 v[208:211], v[152:159], v[56:63], v[64:67], v146, v146 op_sel_hi:[0,0,0]
	global_load_lds_dwordx4 v149, s[40:41]
	s_setprio 0
	s_barrier
	s_add_u32 s24, s38, 0x40000
	s_addc_u32 s25, s39, 0
	s_nop 2
	v_mov_b32_e32 v64, v148
	s_add_i32 s28, s29, s21
	s_mov_b32 s100, s28
	s_nop 0
	v_mov_b32_e32 v64, v149
	s_add_i32 s101, s28, 0x2000
	s_nop 0
	s_waitcnt vmcnt(4)
	s_barrier
	s_setprio 1
	v_mfma_scale_f32_16x16x128_f8f6f4 v[212:215], v[96:103], v[32:39], v[28:31], v146, v146 op_sel_hi:[0,0,0]
	v_mfma_scale_f32_16x16x128_f8f6f4 v[216:219], v[104:111], v[32:39], v[24:27], v146, v146 op_sel_hi:[0,0,0]
	v_mfma_scale_f32_16x16x128_f8f6f4 v[220:223], v[96:103], v[40:47], v[20:23], v146, v146 op_sel_hi:[0,0,0]
	v_mfma_scale_f32_16x16x128_f8f6f4 v[224:227], v[104:111], v[40:47], v[16:19], v146, v146 op_sel_hi:[0,0,0]
	s_mov_b32 m0, s100
	v_mfma_scale_f32_16x16x128_f8f6f4 v[228:231], v[96:103], v[48:55], v[12:15], v146, v146 op_sel_hi:[0,0,0]
	global_load_lds_dwordx4 v148, s[24:25]
	v_mfma_scale_f32_16x16x128_f8f6f4 v[232:235], v[104:111], v[48:55], v[8:11], v146, v146 op_sel_hi:[0,0,0]
	v_mfma_scale_f32_16x16x128_f8f6f4 v[236:239], v[96:103], v[56:63], v[4:7], v146, v146 op_sel_hi:[0,0,0]
	s_mov_b32 m0, s101
	v_mfma_scale_f32_16x16x128_f8f6f4 v[240:243], v[104:111], v[56:63], v[0:3], v146, v146 op_sel_hi:[0,0,0]
	global_load_lds_dwordx4 v149, s[24:25]
	s_setprio 0
	s_add_i32 s28, 0, 0x18000
	s_nop 1
	v_add_u32_e32 v12, s28, v150
	s_barrier
	s_nop 0
	ds_read_b128 v[0:3], v12
	ds_read_b128 v[4:7], v12 offset:1024
	ds_read_b128 v[8:11], v12 offset:2048
	ds_read_b128 v[12:15], v12 offset:3072
	s_add_u32 s24, s40, 0x40000
	v_mov_b32_e32 v40, v148
	ds_read_b128 v[16:19], v151 offset:32768
	ds_read_b128 v[20:23], v151 offset:33792
	ds_read_b128 v[24:27], v151 offset:34816
	ds_read_b128 v[28:31], v151 offset:35840
	ds_read_b128 v[32:35], v151 offset:36864
	ds_read_b128 v[36:39], v151 offset:37888
	ds_read_b128 v[64:67], v151 offset:38912
	ds_read_b128 v[68:71], v151 offset:39936
	s_addc_u32 s25, s41, 0
	s_nop 0
	v_mov_b32_e32 v40, v149
	s_nop 0
	s_waitcnt lgkmcnt(8)
	s_barrier
	s_waitcnt lgkmcnt(0)
	s_setprio 1
	s_waitcnt lgkmcnt(0)
	v_mfma_scale_f32_16x16x128_f8f6f4 v[124:127], v[0:7], v[16:23], v[124:127], v146, v146 op_sel_hi:[0,0,0]
	v_mfma_scale_f32_16x16x128_f8f6f4 v[120:123], v[8:15], v[16:23], v[120:123], v146, v146 op_sel_hi:[0,0,0]
	v_mfma_scale_f32_16x16x128_f8f6f4 v[116:119], v[0:7], v[24:31], v[116:119], v146, v146 op_sel_hi:[0,0,0]
	v_mfma_scale_f32_16x16x128_f8f6f4 v[112:115], v[8:15], v[24:31], v[112:115], v146, v146 op_sel_hi:[0,0,0]
	s_mov_b32 m0, s8
	v_mfma_scale_f32_16x16x128_f8f6f4 v[108:111], v[0:7], v[32:39], v[128:131], v146, v146 op_sel_hi:[0,0,0]
	global_load_lds_dwordx4 v148, s[24:25]
	v_mfma_scale_f32_16x16x128_f8f6f4 v[104:107], v[8:15], v[32:39], v[192:195], v146, v146 op_sel_hi:[0,0,0]
	v_mfma_scale_f32_16x16x128_f8f6f4 v[100:103], v[0:7], v[64:71], v[196:199], v146, v146 op_sel_hi:[0,0,0]
	s_mov_b32 m0, s9
	v_mfma_scale_f32_16x16x128_f8f6f4 v[96:99], v[8:15], v[64:71], v[200:203], v146, v146 op_sel_hi:[0,0,0]
	global_load_lds_dwordx4 v149, s[24:25]
	s_setprio 0
	s_barrier
	s_add_i32 s29, 0, 0x1c000
	v_add_u32_e32 v40, s29, v150
	v_mov_b32_e32 v132, v148
	ds_read_b128 v[136:139], v40
	ds_read_b128 v[140:143], v40 offset:1024
	ds_read_b128 v[152:155], v40 offset:2048
	ds_read_b128 v[156:159], v40 offset:3072
	s_add_i32 s24, s28, s21
	v_lshl_add_u64 v[40:41], s[38:39], 0, v[132:133]
	v_lshl_add_u64 v[40:41], v[40:41], 0, s[52:53]
	v_mov_b32_e32 v132, v149
	v_lshl_add_u64 v[40:41], s[38:39], 0, v[132:133]
	v_lshl_add_u64 v[40:41], v[40:41], 0, s[52:53]
	s_barrier
	s_waitcnt lgkmcnt(0)
	s_setprio 1
	s_waitcnt lgkmcnt(0)
	v_mfma_scale_f32_16x16x128_f8f6f4 v[60:63], v[136:143], v[16:23], v[204:207], v146, v146 op_sel_hi:[0,0,0]
	v_mfma_scale_f32_16x16x128_f8f6f4 v[56:59], v[152:159], v[16:23], v[160:163], v146, v146 op_sel_hi:[0,0,0]
	v_mfma_scale_f32_16x16x128_f8f6f4 v[52:55], v[136:143], v[24:31], v[164:167], v146, v146 op_sel_hi:[0,0,0]
	v_mfma_scale_f32_16x16x128_f8f6f4 v[48:51], v[152:159], v[24:31], v[168:171], v146, v146 op_sel_hi:[0,0,0]
	s_add_u32 s98, s38, s52
	s_addc_u32 s99, s39, s53
	s_mov_b32 m0, s24
	v_mfma_scale_f32_16x16x128_f8f6f4 v[44:47], v[136:143], v[32:39], v[172:175], v146, v146 op_sel_hi:[0,0,0]
	global_load_lds_dwordx4 v148, s[98:99]
	v_mfma_scale_f32_16x16x128_f8f6f4 v[40:43], v[152:159], v[32:39], v[176:179], v146, v146 op_sel_hi:[0,0,0]
	v_mfma_scale_f32_16x16x128_f8f6f4 v[36:39], v[136:143], v[64:71], v[180:183], v146, v146 op_sel_hi:[0,0,0]
	s_add_i32 m0, s24, 0x2000
	v_mfma_scale_f32_16x16x128_f8f6f4 v[32:35], v[152:159], v[64:71], v[184:187], v146, v146 op_sel_hi:[0,0,0]
	global_load_lds_dwordx4 v149, s[98:99]
	s_setprio 0
	v_mov_b32_e32 v132, v148
	s_barrier
	ds_read_b128 v[16:19], v151 offset:49152
	ds_read_b128 v[20:23], v151 offset:50176
	ds_read_b128 v[160:163], v151 offset:51200
	ds_read_b128 v[164:167], v151 offset:52224
	ds_read_b128 v[168:171], v151 offset:53248
	ds_read_b128 v[172:175], v151 offset:54272
	ds_read_b128 v[176:179], v151 offset:55296
	ds_read_b128 v[180:183], v151 offset:56320
	v_lshl_add_u64 v[24:25], s[40:41], 0, v[132:133]
	v_lshl_add_u64 v[24:25], v[24:25], 0, s[52:53]
	v_mov_b32_e32 v132, v149
	v_lshl_add_u64 v[24:25], s[40:41], 0, v[132:133]
	v_lshl_add_u64 v[24:25], v[24:25], 0, s[52:53]
	s_barrier
	s_waitcnt lgkmcnt(0)
	s_setprio 1
	s_waitcnt lgkmcnt(0)
	v_mfma_scale_f32_16x16x128_f8f6f4 v[92:95], v[0:7], v[16:23], v[92:95], v146, v146 op_sel_hi:[0,0,0]
	v_mfma_scale_f32_16x16x128_f8f6f4 v[88:91], v[8:15], v[16:23], v[88:91], v146, v146 op_sel_hi:[0,0,0]
	v_mfma_scale_f32_16x16x128_f8f6f4 v[84:87], v[0:7], v[160:167], v[84:87], v146, v146 op_sel_hi:[0,0,0]
	v_mfma_scale_f32_16x16x128_f8f6f4 v[80:83], v[8:15], v[160:167], v[80:83], v146, v146 op_sel_hi:[0,0,0]
	s_add_u32 s98, s40, s52
	s_addc_u32 s99, s41, s53
	s_mov_b32 m0, s10
	v_mfma_scale_f32_16x16x128_f8f6f4 v[76:79], v[0:7], v[168:175], v[76:79], v146, v146 op_sel_hi:[0,0,0]
	global_load_lds_dwordx4 v148, s[98:99]
	v_mfma_scale_f32_16x16x128_f8f6f4 v[72:75], v[8:15], v[168:175], v[72:75], v146, v146 op_sel_hi:[0,0,0]
	v_mfma_scale_f32_16x16x128_f8f6f4 v[68:71], v[0:7], v[176:183], v[188:191], v146, v146 op_sel_hi:[0,0,0]
	s_mov_b32 m0, s11
	v_mfma_scale_f32_16x16x128_f8f6f4 v[64:67], v[8:15], v[176:183], v[208:211], v146, v146 op_sel_hi:[0,0,0]
	global_load_lds_dwordx4 v149, s[98:99]
	s_setprio 0
	s_barrier
	s_add_u32 s24, s38, 0x40080
	s_addc_u32 s25, s39, 0
	v_mov_b32_e32 v0, v148
	s_add_i32 s28, s29, s21
	s_nop 0
	v_mov_b32_e32 v0, v149
	s_nop 0
	s_waitcnt vmcnt(4)
	s_barrier
	s_setprio 1
	v_mfma_scale_f32_16x16x128_f8f6f4 v[28:31], v[136:143], v[16:23], v[212:215], v146, v146 op_sel_hi:[0,0,0]
	v_mfma_scale_f32_16x16x128_f8f6f4 v[24:27], v[152:159], v[16:23], v[216:219], v146, v146 op_sel_hi:[0,0,0]
	v_mfma_scale_f32_16x16x128_f8f6f4 v[20:23], v[136:143], v[160:167], v[220:223], v146, v146 op_sel_hi:[0,0,0]
	v_mfma_scale_f32_16x16x128_f8f6f4 v[16:19], v[152:159], v[160:167], v[224:227], v146, v146 op_sel_hi:[0,0,0]
	s_mov_b32 m0, s28
	v_mfma_scale_f32_16x16x128_f8f6f4 v[12:15], v[136:143], v[168:175], v[228:231], v146, v146 op_sel_hi:[0,0,0]
	global_load_lds_dwordx4 v148, s[24:25]
	v_mfma_scale_f32_16x16x128_f8f6f4 v[8:11], v[152:159], v[168:175], v[232:235], v146, v146 op_sel_hi:[0,0,0]
	v_mfma_scale_f32_16x16x128_f8f6f4 v[4:7], v[136:143], v[176:183], v[236:239], v146, v146 op_sel_hi:[0,0,0]
	s_add_i32 m0, s28, 0x2000
	v_mfma_scale_f32_16x16x128_f8f6f4 v[0:3], v[152:159], v[176:183], v[240:243], v146, v146 op_sel_hi:[0,0,0]
	global_load_lds_dwordx4 v149, s[24:25]
	s_setprio 0
	s_add_i32 s22, s22, 2
	s_add_u32 s2, s2, 0x100
	s_addc_u32 s3, s3, 0
	s_add_u32 s7, s7, 0x100
	s_addc_u32 s20, s20, 0
	s_cmp_gt_u32 s22, 13
	s_barrier
	s_cbranch_scc0 .LBB0_1503
	s_ashr_i32 s2, s13, 4
	s_mul_hi_i32 s3, s2, 0xc000
	s_mul_i32 s2, s2, 0xc000
	s_add_u32 s7, s69, s2
	s_addc_u32 s20, s71, s3
	s_lshl_b32 s2, s15, 8
	s_ashr_i32 s3, s2, 31
	s_lshl_b64 s[24:25], s[2:3], 2
	s_add_u32 s7, s7, s24
	v_mbcnt_lo_u32_b32 v132, -1, 0
	v_mbcnt_hi_u32_b32 v132, -1, v132
	s_addc_u32 s15, s20, s25
	v_ashrrev_i32_e32 v136, 4, v132
	s_lshl_b32 s20, s23, 2
	s_add_u32 s24, s7, s20
	v_lshlrev_b32_e32 v128, 2, v136
	s_addc_u32 s25, s15, 0
	v_ashrrev_i32_e32 v129, 31, v128
	v_lshl_add_u64 v[130:131], v[128:129], 2, s[24:25]
	v_lshlrev_b32_e32 v128, 3, v136
	global_load_dwordx4 v[136:139], v[130:131], off
	global_load_dwordx4 v[152:155], v[130:131], off offset:64
	s_lshl_b32 s7, s13, 8
	s_add_i32 s24, s7, s16
	s_ashr_i32 s25, s24, 31
	s_lshl_b64 s[24:25], s[24:25], 11
	s_add_u32 s7, s61, s24
	s_addc_u32 s13, s65, s25
	s_add_u32 s2, s7, s2
	s_addc_u32 s3, s13, s3
	v_bfi_b32 v128, -16, v128, v132
	s_add_u32 s2, s2, s23
	v_ashrrev_i32_e32 v129, 31, v128
	s_addc_u32 s3, s3, 0
	v_lshlrev_b64 v[128:129], 11, v[128:129]
	v_lshl_add_u64 v[128:129], s[2:3], 0, v[128:129]
	v_and_b32_e32 v132, 16, v132
	v_lshl_add_u64 v[128:129], v[128:129], 0, v[132:133]
	s_mov_b32 s2, 0x10000
	s_mov_b32 s13, s36
	s_mov_b32 s15, s6
	s_mov_b64 s[34:35], s[58:59]
	s_waitcnt vmcnt(0)
	v_pk_mul_f32 v[140:141], v[138:139], s[54:55] op_sel_hi:[1,0]
	v_pk_mul_f32 v[138:139], v[136:137], s[54:55] op_sel_hi:[1,0]
	v_pk_mul_f32 v[136:137], v[152:153], s[54:55] op_sel_hi:[1,0]
	v_pk_mul_f32 v[152:153], v[124:125], v[138:139]
	v_mov_b32_e32 v124, v133
	v_cvt_pk_fp8_f32 v124, v152, v153
	v_pk_mul_f32 v[126:127], v[126:127], v[140:141]
	v_pk_mul_f32 v[112:113], v[112:113], v[136:137]
	v_pk_mul_f32 v[110:111], v[110:111], v[140:141]
	v_cvt_pk_fp8_f32 v124, v126, v127 op_sel:[0,0,1]
	v_mov_b32_e32 v127, v133
	v_cvt_pk_fp8_f32 v127, v112, v113
	v_pk_mul_f32 v[112:113], v[108:109], v[138:139]
	v_mov_b32_e32 v108, v133
	v_cvt_pk_fp8_f32 v108, v112, v113
	v_pk_mul_f32 v[96:97], v[96:97], v[136:137]
	v_pk_mul_f32 v[142:143], v[154:155], s[54:55] op_sel_hi:[1,0]
	v_pk_mul_f32 v[94:95], v[94:95], v[140:141]
	v_cvt_pk_fp8_f32 v108, v110, v111 op_sel:[0,0,1]
	v_mov_b32_e32 v111, v133
	v_cvt_pk_fp8_f32 v111, v96, v97
	v_pk_mul_f32 v[98:99], v[98:99], v[142:143]
	v_pk_mul_f32 v[80:81], v[80:81], v[136:137]
	v_pk_mul_f32 v[78:79], v[78:79], v[140:141]
	v_cvt_pk_fp8_f32 v111, v98, v99 op_sel:[0,0,1]
	v_pk_mul_f32 v[98:99], v[92:93], v[138:139]
	v_mov_b32_e32 v92, v133
	v_cvt_pk_fp8_f32 v92, v98, v99
	v_pk_mul_f32 v[120:121], v[120:121], v[136:137]
	v_mov_b32_e32 v125, v133
	v_pk_mul_f32 v[116:117], v[116:117], v[138:139]
	v_cvt_pk_fp8_f32 v92, v94, v95 op_sel:[0,0,1]
	v_mov_b32_e32 v95, v133
	v_cvt_pk_fp8_f32 v95, v80, v81
	v_pk_mul_f32 v[80:81], v[76:77], v[138:139]
	v_mov_b32_e32 v76, v133
	v_cvt_pk_fp8_f32 v76, v80, v81
	v_mov_b32_e32 v126, v133
	v_pk_mul_f32 v[104:105], v[104:105], v[136:137]
	v_mov_b32_e32 v109, v133
	v_pk_mul_f32 v[100:101], v[100:101], v[138:139]
	v_mov_b32_e32 v110, v133
	v_pk_mul_f32 v[88:89], v[88:89], v[136:137]
	v_mov_b32_e32 v93, v133
	v_pk_mul_f32 v[84:85], v[84:85], v[138:139]
	v_mov_b32_e32 v94, v133
	v_cvt_pk_fp8_f32 v76, v78, v79 op_sel:[0,0,1]
	v_pk_mul_f32 v[72:73], v[72:73], v[136:137]
	v_mov_b32_e32 v77, v133
	v_pk_mul_f32 v[68:69], v[68:69], v[138:139]
	v_mov_b32_e32 v78, v133
	v_pk_mul_f32 v[64:65], v[64:65], v[136:137]
	v_mov_b32_e32 v79, v133
	v_cvt_pk_fp8_f32 v125, v120, v121
	v_cvt_pk_fp8_f32 v126, v116, v117
	v_cvt_pk_fp8_f32 v109, v104, v105
	v_cvt_pk_fp8_f32 v110, v100, v101
	v_cvt_pk_fp8_f32 v93, v88, v89
	v_cvt_pk_fp8_f32 v94, v84, v85
	v_cvt_pk_fp8_f32 v77, v72, v73
	v_cvt_pk_fp8_f32 v78, v68, v69
	v_cvt_pk_fp8_f32 v79, v64, v65
	v_pk_mul_f32 v[122:123], v[122:123], v[142:143]
	v_pk_mul_f32 v[118:119], v[118:119], v[140:141]
	v_pk_mul_f32 v[114:115], v[114:115], v[142:143]
	v_pk_mul_f32 v[106:107], v[106:107], v[142:143]
	v_pk_mul_f32 v[102:103], v[102:103], v[140:141]
	v_pk_mul_f32 v[90:91], v[90:91], v[142:143]
	v_pk_mul_f32 v[86:87], v[86:87], v[140:141]
	v_pk_mul_f32 v[82:83], v[82:83], v[142:143]
	v_pk_mul_f32 v[74:75], v[74:75], v[142:143]
	v_pk_mul_f32 v[70:71], v[70:71], v[140:141]
	v_pk_mul_f32 v[66:67], v[66:67], v[142:143]
	v_cvt_pk_fp8_f32 v125, v122, v123 op_sel:[0,0,1]
	v_cvt_pk_fp8_f32 v126, v118, v119 op_sel:[0,0,1]
	v_cvt_pk_fp8_f32 v127, v114, v115 op_sel:[0,0,1]
	v_cvt_pk_fp8_f32 v109, v106, v107 op_sel:[0,0,1]
	v_cvt_pk_fp8_f32 v110, v102, v103 op_sel:[0,0,1]
	v_add_co_u32_e32 v96, vcc, s2, v128
	v_cvt_pk_fp8_f32 v93, v90, v91 op_sel:[0,0,1]
	v_cvt_pk_fp8_f32 v94, v86, v87 op_sel:[0,0,1]
	v_cvt_pk_fp8_f32 v95, v82, v83 op_sel:[0,0,1]
	v_cvt_pk_fp8_f32 v77, v74, v75 op_sel:[0,0,1]
	v_cvt_pk_fp8_f32 v78, v70, v71 op_sel:[0,0,1]
	v_cvt_pk_fp8_f32 v79, v66, v67 op_sel:[0,0,1]
	v_addc_co_u32_e32 v97, vcc, 0, v129, vcc
	s_mov_b32 s2, 0x40000
	v_add_co_u32_e32 v64, vcc, s2, v128
	s_mov_b32 s2, 0x50000
	s_nop 0
	v_addc_co_u32_e32 v65, vcc, 0, v129, vcc
	v_permlane32_swap_b32_e32 v124, v126
	v_permlane32_swap_b32_e32 v125, v127
	v_permlane32_swap_b32_e32 v108, v110
	v_permlane32_swap_b32_e32 v109, v111
	v_permlane32_swap_b32_e32 v92, v94
	v_permlane32_swap_b32_e32 v93, v95
	v_permlane32_swap_b32_e32 v76, v78
	v_permlane32_swap_b32_e32 v77, v79
	v_add_co_u32_e32 v66, vcc, s2, v128
	v_permlane16_swap_b32_e32 v124, v125
	v_permlane16_swap_b32_e32 v126, v127
	v_permlane16_swap_b32_e32 v108, v109
	v_permlane16_swap_b32_e32 v110, v111
	v_permlane16_swap_b32_e32 v92, v93
	v_permlane16_swap_b32_e32 v94, v95
	v_permlane16_swap_b32_e32 v76, v77
	v_permlane16_swap_b32_e32 v78, v79
	v_addc_co_u32_e32 v67, vcc, 0, v129, vcc
	global_store_dwordx4 v[128:129], v[124:127], off
	global_store_dwordx4 v[96:97], v[108:111], off
	global_store_dwordx4 v[64:65], v[92:95], off
	global_store_dwordx4 v[66:67], v[76:79], off
	global_load_dwordx4 v[68:71], v[130:131], off offset:512
	s_and_b64 vcc, exec, s[4:5]
	global_load_dwordx4 v[76:79], v[130:131], off offset:576
	s_mov_b64 s[2:3], s[48:49]
	s_waitcnt vmcnt(0)
	v_pk_mul_f32 v[72:73], v[70:71], s[54:55] op_sel_hi:[1,0]
	v_pk_mul_f32 v[70:71], v[68:69], s[54:55] op_sel_hi:[1,0]
	v_pk_mul_f32 v[68:69], v[76:77], s[54:55] op_sel_hi:[1,0]
	v_pk_mul_f32 v[76:77], v[60:61], v[70:71]
	v_mov_b32_e32 v60, v133
	v_cvt_pk_fp8_f32 v60, v76, v77
	v_pk_mul_f32 v[62:63], v[62:63], v[72:73]
	v_pk_mul_f32 v[48:49], v[48:49], v[68:69]
	v_pk_mul_f32 v[46:47], v[46:47], v[72:73]
	v_cvt_pk_fp8_f32 v60, v62, v63 op_sel:[0,0,1]
	v_mov_b32_e32 v63, v133
	v_cvt_pk_fp8_f32 v63, v48, v49
	v_pk_mul_f32 v[48:49], v[44:45], v[70:71]
	v_mov_b32_e32 v44, v133
	v_cvt_pk_fp8_f32 v44, v48, v49
	v_pk_mul_f32 v[32:33], v[32:33], v[68:69]
	v_pk_mul_f32 v[30:31], v[30:31], v[72:73]
	v_pk_mul_f32 v[16:17], v[16:17], v[68:69]
	v_cvt_pk_fp8_f32 v44, v46, v47 op_sel:[0,0,1]
	v_mov_b32_e32 v47, v133
	v_cvt_pk_fp8_f32 v47, v32, v33
	v_pk_mul_f32 v[32:33], v[28:29], v[70:71]
	v_mov_b32_e32 v28, v133
	v_cvt_pk_fp8_f32 v28, v32, v33
	v_pk_mul_f32 v[56:57], v[56:57], v[68:69]
	v_mov_b32_e32 v61, v133
	v_pk_mul_f32 v[52:53], v[52:53], v[70:71]
	v_cvt_pk_fp8_f32 v28, v30, v31 op_sel:[0,0,1]
	v_mov_b32_e32 v31, v133
	v_cvt_pk_fp8_f32 v31, v16, v17
	v_pk_mul_f32 v[16:17], v[12:13], v[70:71]
	v_mov_b32_e32 v12, v133
	v_cvt_pk_fp8_f32 v12, v16, v17
	v_mov_b32_e32 v62, v133
	v_pk_mul_f32 v[24:25], v[24:25], v[68:69]
	v_mov_b32_e32 v29, v133
	v_pk_mul_f32 v[20:21], v[20:21], v[70:71]
	v_mov_b32_e32 v30, v133
	v_pk_mul_f32 v[14:15], v[14:15], v[72:73]
	v_cvt_pk_fp8_f32 v61, v56, v57
	v_cvt_pk_fp8_f32 v62, v52, v53
	v_pk_mul_f32 v[40:41], v[40:41], v[68:69]
	v_mov_b32_e32 v45, v133
	v_pk_mul_f32 v[36:37], v[36:37], v[70:71]
	v_mov_b32_e32 v46, v133
	v_cvt_pk_fp8_f32 v29, v24, v25
	v_cvt_pk_fp8_f32 v30, v20, v21
	v_cvt_pk_fp8_f32 v12, v14, v15 op_sel:[0,0,1]
	v_pk_mul_f32 v[8:9], v[8:9], v[68:69]
	v_mov_b32_e32 v13, v133
	v_pk_mul_f32 v[4:5], v[4:5], v[70:71]
	v_mov_b32_e32 v14, v133
	v_pk_mul_f32 v[0:1], v[0:1], v[68:69]
	v_mov_b32_e32 v15, v133
	v_cvt_pk_fp8_f32 v45, v40, v41
	v_cvt_pk_fp8_f32 v46, v36, v37
	v_cvt_pk_fp8_f32 v13, v8, v9
	v_cvt_pk_fp8_f32 v14, v4, v5
	v_cvt_pk_fp8_f32 v15, v0, v1
	v_pk_mul_f32 v[74:75], v[78:79], s[54:55] op_sel_hi:[1,0]
	v_pk_mul_f32 v[54:55], v[54:55], v[72:73]
	v_pk_mul_f32 v[58:59], v[58:59], v[74:75]
	v_pk_mul_f32 v[50:51], v[50:51], v[74:75]
	v_pk_mul_f32 v[26:27], v[26:27], v[74:75]
	v_pk_mul_f32 v[22:23], v[22:23], v[72:73]
	v_pk_mul_f32 v[18:19], v[18:19], v[74:75]
	v_cvt_pk_fp8_f32 v61, v58, v59 op_sel:[0,0,1]
	v_cvt_pk_fp8_f32 v62, v54, v55 op_sel:[0,0,1]
	v_cvt_pk_fp8_f32 v63, v50, v51 op_sel:[0,0,1]
	v_pk_mul_f32 v[42:43], v[42:43], v[74:75]
	v_pk_mul_f32 v[38:39], v[38:39], v[72:73]
	v_pk_mul_f32 v[34:35], v[34:35], v[74:75]
	v_cvt_pk_fp8_f32 v29, v26, v27 op_sel:[0,0,1]
	v_cvt_pk_fp8_f32 v30, v22, v23 op_sel:[0,0,1]
	v_cvt_pk_fp8_f32 v31, v18, v19 op_sel:[0,0,1]
	v_pk_mul_f32 v[10:11], v[10:11], v[74:75]
	v_pk_mul_f32 v[6:7], v[6:7], v[72:73]
	v_pk_mul_f32 v[2:3], v[2:3], v[74:75]
	v_cvt_pk_fp8_f32 v45, v42, v43 op_sel:[0,0,1]
	v_cvt_pk_fp8_f32 v46, v38, v39 op_sel:[0,0,1]
	v_cvt_pk_fp8_f32 v47, v34, v35 op_sel:[0,0,1]
	v_cvt_pk_fp8_f32 v13, v10, v11 op_sel:[0,0,1]
	v_cvt_pk_fp8_f32 v14, v6, v7 op_sel:[0,0,1]
	v_cvt_pk_fp8_f32 v15, v2, v3 op_sel:[0,0,1]
	v_permlane32_swap_b32_e32 v60, v62
	v_permlane32_swap_b32_e32 v61, v63
	v_permlane32_swap_b32_e32 v28, v30
	v_permlane32_swap_b32_e32 v29, v31
	v_permlane16_swap_b32_e32 v60, v61
	v_permlane16_swap_b32_e32 v62, v63
	v_permlane32_swap_b32_e32 v44, v46
	v_permlane32_swap_b32_e32 v45, v47
	v_permlane16_swap_b32_e32 v28, v29
	v_permlane16_swap_b32_e32 v30, v31
	v_permlane32_swap_b32_e32 v12, v14
	v_permlane32_swap_b32_e32 v13, v15
	v_permlane16_swap_b32_e32 v44, v45
	v_permlane16_swap_b32_e32 v46, v47
	global_store_dwordx4 v[128:129], v[60:63], off offset:128
	global_store_dwordx4 v[96:97], v[44:47], off offset:128
	v_permlane16_swap_b32_e32 v12, v13
	v_permlane16_swap_b32_e32 v14, v15
	global_store_dwordx4 v[64:65], v[28:31], off offset:128
	global_store_dwordx4 v[66:67], v[12:15], off offset:128
	s_cbranch_vccz .LBB0_1496
	v_readlane_b32 s0, v252, 18
	s_waitcnt vmcnt(0)
	v_readlane_b32 s1, v252, 19
	s_andn2_b64 vcc, exec, s[0:1]
	s_cbranch_vccnz .LBB0_1227
	s_barrier
	s_branch .LBB0_1227

.LBB0_2382:
	ds_read_b128 v[140:143], v134
	ds_read_b128 v[144:147], v134 offset:1024
	ds_read_b128 v[148:151], v134 offset:2048
	ds_read_b128 v[152:155], v134 offset:3072
	s_add_u32 s18, s16, 0xfffd0080
	s_addc_u32 s19, s17, -1
	s_cmp_eq_u32 s54, 8
	s_cselect_b32 s21, s15, s19
	s_cselect_b32 s20, s14, s18
	s_cselect_b32 s19, s13, s53
	s_cselect_b32 s18, s12, s52
	v_mov_b32_e32 v128, v132
	ds_read_b128 v[156:159], v135
	ds_read_b128 v[160:163], v135 offset:1024
	ds_read_b128 v[164:167], v135 offset:2048
	ds_read_b128 v[168:171], v135 offset:3072
	ds_read_b128 v[172:175], v135 offset:4096
	ds_read_b128 v[176:179], v135 offset:5120
	ds_read_b128 v[180:183], v135 offset:6144
	ds_read_b128 v[184:187], v135 offset:7168
	s_nop 0
	v_mov_b32_e32 v128, v133
	s_nop 0
	s_waitcnt lgkmcnt(8)
	s_barrier
	s_waitcnt lgkmcnt(0)
	s_setprio 1
	s_waitcnt lgkmcnt(0)
	v_mfma_scale_f32_16x16x128_f8f6f4 v[124:127], v[140:147], v[156:163], v[124:127], v136, v136 op_sel_hi:[0,0,0]
	v_mfma_scale_f32_16x16x128_f8f6f4 v[120:123], v[148:155], v[156:163], v[120:123], v136, v136 op_sel_hi:[0,0,0]
	v_mfma_scale_f32_16x16x128_f8f6f4 v[116:119], v[140:147], v[164:171], v[116:119], v136, v136 op_sel_hi:[0,0,0]
	v_mfma_scale_f32_16x16x128_f8f6f4 v[112:115], v[148:155], v[164:171], v[112:115], v136, v136 op_sel_hi:[0,0,0]
	s_mov_b32 m0, s39
	v_mfma_scale_f32_16x16x128_f8f6f4 v[188:191], v[140:147], v[172:179], v[108:111], v136, v136 op_sel_hi:[0,0,0]
	global_load_lds_dwordx4 v132, s[16:17]
	v_mfma_scale_f32_16x16x128_f8f6f4 v[192:195], v[148:155], v[172:179], v[104:107], v136, v136 op_sel_hi:[0,0,0]
	v_mfma_scale_f32_16x16x128_f8f6f4 v[196:199], v[140:147], v[180:187], v[100:103], v136, v136 op_sel_hi:[0,0,0]
	s_mov_b32 m0, s40
	v_mfma_scale_f32_16x16x128_f8f6f4 v[200:203], v[148:155], v[180:187], v[96:99], v136, v136 op_sel_hi:[0,0,0]
	global_load_lds_dwordx4 v133, s[16:17]
	s_setprio 0
	s_barrier
	v_mov_b32_e32 v128, v132
	s_nop 2
	ds_read_b128 v[96:99], v137
	ds_read_b128 v[100:103], v137 offset:1024
	ds_read_b128 v[104:107], v137 offset:2048
	ds_read_b128 v[108:111], v137 offset:3072
	s_nop 0
	v_mov_b32_e32 v128, v133
	s_nop 0
	s_barrier
	s_waitcnt lgkmcnt(0)
	s_setprio 1
	s_waitcnt lgkmcnt(0)
	v_mfma_scale_f32_16x16x128_f8f6f4 v[204:207], v[96:103], v[156:163], v[92:95], v136, v136 op_sel_hi:[0,0,0]
	v_mfma_scale_f32_16x16x128_f8f6f4 v[156:159], v[104:111], v[156:163], v[88:91], v136, v136 op_sel_hi:[0,0,0]
	v_mfma_scale_f32_16x16x128_f8f6f4 v[160:163], v[96:103], v[164:171], v[84:87], v136, v136 op_sel_hi:[0,0,0]
	v_mfma_scale_f32_16x16x128_f8f6f4 v[164:167], v[104:111], v[164:171], v[80:83], v136, v136 op_sel_hi:[0,0,0]
	s_mov_b32 m0, s41
	v_mfma_scale_f32_16x16x128_f8f6f4 v[168:171], v[96:103], v[172:179], v[76:79], v136, v136 op_sel_hi:[0,0,0]
	global_load_lds_dwordx4 v132, s[18:19]
	v_mfma_scale_f32_16x16x128_f8f6f4 v[172:175], v[104:111], v[172:179], v[72:75], v136, v136 op_sel_hi:[0,0,0]
	v_mfma_scale_f32_16x16x128_f8f6f4 v[176:179], v[96:103], v[180:187], v[68:71], v136, v136 op_sel_hi:[0,0,0]
	s_mov_b32 m0, s42
	v_mfma_scale_f32_16x16x128_f8f6f4 v[180:183], v[104:111], v[180:187], v[64:67], v136, v136 op_sel_hi:[0,0,0]
	global_load_lds_dwordx4 v133, s[18:19]
	s_setprio 0
	v_mov_b32_e32 v128, v132
	s_barrier
	s_nop 2
	ds_read_b128 v[64:67], v135 offset:16384
	ds_read_b128 v[68:71], v135 offset:17408
	ds_read_b128 v[72:75], v135 offset:18432
	ds_read_b128 v[76:79], v135 offset:19456
	ds_read_b128 v[80:83], v135 offset:20480
	ds_read_b128 v[84:87], v135 offset:21504
	ds_read_b128 v[88:91], v135 offset:22528
	ds_read_b128 v[92:95], v135 offset:23552
	s_nop 0
	v_mov_b32_e32 v128, v133
	s_nop 0
	s_barrier
	s_waitcnt lgkmcnt(0)
	s_setprio 1
	s_waitcnt lgkmcnt(0)
	v_mfma_scale_f32_16x16x128_f8f6f4 v[60:63], v[140:147], v[64:71], v[60:63], v136, v136 op_sel_hi:[0,0,0]
	v_mfma_scale_f32_16x16x128_f8f6f4 v[56:59], v[148:155], v[64:71], v[56:59], v136, v136 op_sel_hi:[0,0,0]
	v_mfma_scale_f32_16x16x128_f8f6f4 v[52:55], v[140:147], v[72:79], v[52:55], v136, v136 op_sel_hi:[0,0,0]
	v_mfma_scale_f32_16x16x128_f8f6f4 v[48:51], v[148:155], v[72:79], v[48:51], v136, v136 op_sel_hi:[0,0,0]
	s_mov_b32 m0, s25
	v_mfma_scale_f32_16x16x128_f8f6f4 v[184:187], v[140:147], v[80:87], v[44:47], v136, v136 op_sel_hi:[0,0,0]
	global_load_lds_dwordx4 v132, s[20:21]
	v_mfma_scale_f32_16x16x128_f8f6f4 v[208:211], v[148:155], v[80:87], v[40:43], v136, v136 op_sel_hi:[0,0,0]
	v_mfma_scale_f32_16x16x128_f8f6f4 v[212:215], v[140:147], v[88:95], v[36:39], v136, v136 op_sel_hi:[0,0,0]
	s_mov_b32 m0, s26
	v_mfma_scale_f32_16x16x128_f8f6f4 v[216:219], v[148:155], v[88:95], v[32:35], v136, v136 op_sel_hi:[0,0,0]
	global_load_lds_dwordx4 v133, s[20:21]
	s_setprio 0
	s_barrier
	s_add_u32 s56, s18, 0x30000
	s_nop 3
	v_mov_b32_e32 v32, v132
	s_addc_u32 s57, s19, 0
	s_nop 0
	v_mov_b32_e32 v32, v133
	s_nop 0
	s_waitcnt vmcnt(4)
	s_barrier
	s_setprio 1
	v_mfma_scale_f32_16x16x128_f8f6f4 v[220:223], v[96:103], v[64:71], v[28:31], v136, v136 op_sel_hi:[0,0,0]
	v_mfma_scale_f32_16x16x128_f8f6f4 v[224:227], v[104:111], v[64:71], v[24:27], v136, v136 op_sel_hi:[0,0,0]
	v_mfma_scale_f32_16x16x128_f8f6f4 v[228:231], v[96:103], v[72:79], v[20:23], v136, v136 op_sel_hi:[0,0,0]
	v_mfma_scale_f32_16x16x128_f8f6f4 v[232:235], v[104:111], v[72:79], v[16:19], v136, v136 op_sel_hi:[0,0,0]
	s_mov_b32 m0, s43
	v_mfma_scale_f32_16x16x128_f8f6f4 v[236:239], v[96:103], v[80:87], v[12:15], v136, v136 op_sel_hi:[0,0,0]
	global_load_lds_dwordx4 v132, s[56:57]
	v_mfma_scale_f32_16x16x128_f8f6f4 v[240:243], v[104:111], v[80:87], v[8:11], v136, v136 op_sel_hi:[0,0,0]
	v_mfma_scale_f32_16x16x128_f8f6f4 v[244:247], v[96:103], v[88:95], v[4:7], v136, v136 op_sel_hi:[0,0,0]
	s_mov_b32 m0, s44
	v_mfma_scale_f32_16x16x128_f8f6f4 v[248:251], v[104:111], v[88:95], v[0:3], v136, v136 op_sel_hi:[0,0,0]
	global_load_lds_dwordx4 v133, s[56:57]
	s_setprio 0
	s_barrier
	s_nop 4
	ds_read_b128 v[0:3], v138
	ds_read_b128 v[4:7], v138 offset:1024
	ds_read_b128 v[8:11], v138 offset:2048
	ds_read_b128 v[12:15], v138 offset:3072
	s_add_u32 s56, s20, 0x30000
	v_mov_b32_e32 v64, v132
	ds_read_b128 v[16:19], v135 offset:32768
	ds_read_b128 v[20:23], v135 offset:33792
	ds_read_b128 v[24:27], v135 offset:34816
	ds_read_b128 v[28:31], v135 offset:35840
	ds_read_b128 v[32:35], v135 offset:36864
	ds_read_b128 v[36:39], v135 offset:37888
	ds_read_b128 v[40:43], v135 offset:38912
	ds_read_b128 v[44:47], v135 offset:39936
	s_addc_u32 s57, s21, 0
	s_nop 0
	v_mov_b32_e32 v64, v133
	s_nop 0
	s_waitcnt lgkmcnt(8)
	s_barrier
	s_waitcnt lgkmcnt(0)
	s_setprio 1
	s_waitcnt lgkmcnt(0)
	v_mfma_scale_f32_16x16x128_f8f6f4 v[124:127], v[0:7], v[16:23], v[124:127], v136, v136 op_sel_hi:[0,0,0]
	v_mfma_scale_f32_16x16x128_f8f6f4 v[120:123], v[8:15], v[16:23], v[120:123], v136, v136 op_sel_hi:[0,0,0]
	v_mfma_scale_f32_16x16x128_f8f6f4 v[116:119], v[0:7], v[24:31], v[116:119], v136, v136 op_sel_hi:[0,0,0]
	v_mfma_scale_f32_16x16x128_f8f6f4 v[112:115], v[8:15], v[24:31], v[112:115], v136, v136 op_sel_hi:[0,0,0]
	s_mov_b32 m0, s27
	v_mfma_scale_f32_16x16x128_f8f6f4 v[108:111], v[0:7], v[32:39], v[188:191], v136, v136 op_sel_hi:[0,0,0]
	global_load_lds_dwordx4 v132, s[56:57]
	v_mfma_scale_f32_16x16x128_f8f6f4 v[104:107], v[8:15], v[32:39], v[192:195], v136, v136 op_sel_hi:[0,0,0]
	v_mfma_scale_f32_16x16x128_f8f6f4 v[100:103], v[0:7], v[40:47], v[196:199], v136, v136 op_sel_hi:[0,0,0]
	s_mov_b32 m0, s28
	v_mfma_scale_f32_16x16x128_f8f6f4 v[96:99], v[8:15], v[40:47], v[200:203], v136, v136 op_sel_hi:[0,0,0]
	global_load_lds_dwordx4 v133, s[56:57]
	s_setprio 0
	s_barrier
	v_mov_b32_e32 v128, v132
	ds_read_b128 v[140:143], v139
	ds_read_b128 v[144:147], v139 offset:1024
	ds_read_b128 v[148:151], v139 offset:2048
	ds_read_b128 v[152:155], v139 offset:3072
	v_lshl_add_u64 v[64:65], s[18:19], 0, v[128:129]
	v_lshl_add_u64 v[64:65], v[64:65], 0, s[4:5]
	v_mov_b32_e32 v128, v133
	v_lshl_add_u64 v[64:65], s[18:19], 0, v[128:129]
	v_lshl_add_u64 v[64:65], v[64:65], 0, s[4:5]
	s_barrier
	s_waitcnt lgkmcnt(0)
	s_setprio 1
	s_waitcnt lgkmcnt(0)
	v_mfma_scale_f32_16x16x128_f8f6f4 v[92:95], v[140:147], v[16:23], v[204:207], v136, v136 op_sel_hi:[0,0,0]
	v_mfma_scale_f32_16x16x128_f8f6f4 v[88:91], v[148:155], v[16:23], v[156:159], v136, v136 op_sel_hi:[0,0,0]
	v_mfma_scale_f32_16x16x128_f8f6f4 v[84:87], v[140:147], v[24:31], v[160:163], v136, v136 op_sel_hi:[0,0,0]
	v_mfma_scale_f32_16x16x128_f8f6f4 v[80:83], v[148:155], v[24:31], v[164:167], v136, v136 op_sel_hi:[0,0,0]
	s_add_u32 s98, s18, s4
	s_addc_u32 s99, s19, s5
	s_mov_b32 m0, s46
	v_mfma_scale_f32_16x16x128_f8f6f4 v[76:79], v[140:147], v[32:39], v[168:171], v136, v136 op_sel_hi:[0,0,0]
	global_load_lds_dwordx4 v132, s[98:99]
	v_mfma_scale_f32_16x16x128_f8f6f4 v[72:75], v[148:155], v[32:39], v[172:175], v136, v136 op_sel_hi:[0,0,0]
	v_mfma_scale_f32_16x16x128_f8f6f4 v[68:71], v[140:147], v[40:47], v[176:179], v136, v136 op_sel_hi:[0,0,0]
	s_mov_b32 m0, s47
	v_mfma_scale_f32_16x16x128_f8f6f4 v[64:67], v[148:155], v[40:47], v[180:183], v136, v136 op_sel_hi:[0,0,0]
	global_load_lds_dwordx4 v133, s[98:99]
	s_setprio 0
	v_mov_b32_e32 v128, v132
	s_barrier
	ds_read_b128 v[16:19], v135 offset:49152
	ds_read_b128 v[20:23], v135 offset:50176
	ds_read_b128 v[156:159], v135 offset:51200
	ds_read_b128 v[160:163], v135 offset:52224
	ds_read_b128 v[164:167], v135 offset:53248
	ds_read_b128 v[168:171], v135 offset:54272
	ds_read_b128 v[172:175], v135 offset:55296
	ds_read_b128 v[176:179], v135 offset:56320
	v_lshl_add_u64 v[24:25], s[20:21], 0, v[128:129]
	v_lshl_add_u64 v[24:25], v[24:25], 0, s[4:5]
	v_mov_b32_e32 v128, v133
	v_lshl_add_u64 v[24:25], s[20:21], 0, v[128:129]
	v_lshl_add_u64 v[24:25], v[24:25], 0, s[4:5]
	s_barrier
	s_waitcnt lgkmcnt(0)
	s_setprio 1
	s_waitcnt lgkmcnt(0)
	v_mfma_scale_f32_16x16x128_f8f6f4 v[60:63], v[0:7], v[16:23], v[60:63], v136, v136 op_sel_hi:[0,0,0]
	v_mfma_scale_f32_16x16x128_f8f6f4 v[56:59], v[8:15], v[16:23], v[56:59], v136, v136 op_sel_hi:[0,0,0]
	v_mfma_scale_f32_16x16x128_f8f6f4 v[52:55], v[0:7], v[156:163], v[52:55], v136, v136 op_sel_hi:[0,0,0]
	v_mfma_scale_f32_16x16x128_f8f6f4 v[48:51], v[8:15], v[156:163], v[48:51], v136, v136 op_sel_hi:[0,0,0]
	s_add_u32 s98, s20, s4
	s_addc_u32 s99, s21, s5
	s_mov_b32 m0, s36
	v_mfma_scale_f32_16x16x128_f8f6f4 v[44:47], v[0:7], v[164:171], v[184:187], v136, v136 op_sel_hi:[0,0,0]
	global_load_lds_dwordx4 v132, s[98:99]
	v_mfma_scale_f32_16x16x128_f8f6f4 v[40:43], v[8:15], v[164:171], v[208:211], v136, v136 op_sel_hi:[0,0,0]
	v_mfma_scale_f32_16x16x128_f8f6f4 v[36:39], v[0:7], v[172:179], v[212:215], v136, v136 op_sel_hi:[0,0,0]
	s_mov_b32 m0, s37
	v_mfma_scale_f32_16x16x128_f8f6f4 v[32:35], v[8:15], v[172:179], v[216:219], v136, v136 op_sel_hi:[0,0,0]
	global_load_lds_dwordx4 v133, s[98:99]
	s_setprio 0
	s_barrier
	s_add_u32 s18, s18, 0x30080
	s_addc_u32 s19, s19, 0
	v_mov_b32_e32 v0, v132
	s_add_i32 s20, s45, s24
	s_nop 0
	v_mov_b32_e32 v0, v133
	s_nop 0
	s_waitcnt vmcnt(4)
	s_barrier
	s_setprio 1
	v_mfma_scale_f32_16x16x128_f8f6f4 v[28:31], v[140:147], v[16:23], v[220:223], v136, v136 op_sel_hi:[0,0,0]
	v_mfma_scale_f32_16x16x128_f8f6f4 v[24:27], v[148:155], v[16:23], v[224:227], v136, v136 op_sel_hi:[0,0,0]
	v_mfma_scale_f32_16x16x128_f8f6f4 v[20:23], v[140:147], v[156:163], v[228:231], v136, v136 op_sel_hi:[0,0,0]
	v_mfma_scale_f32_16x16x128_f8f6f4 v[16:19], v[148:155], v[156:163], v[232:235], v136, v136 op_sel_hi:[0,0,0]
	s_mov_b32 m0, s20
	v_mfma_scale_f32_16x16x128_f8f6f4 v[12:15], v[140:147], v[164:171], v[236:239], v136, v136 op_sel_hi:[0,0,0]
	global_load_lds_dwordx4 v132, s[18:19]
	v_mfma_scale_f32_16x16x128_f8f6f4 v[8:11], v[148:155], v[164:171], v[240:243], v136, v136 op_sel_hi:[0,0,0]
	v_mfma_scale_f32_16x16x128_f8f6f4 v[4:7], v[140:147], v[172:179], v[244:247], v136, v136 op_sel_hi:[0,0,0]
	s_add_i32 m0, s20, 0x2000
	v_mfma_scale_f32_16x16x128_f8f6f4 v[0:3], v[148:155], v[172:179], v[248:251], v136, v136 op_sel_hi:[0,0,0]
	global_load_lds_dwordx4 v133, s[18:19]
	s_setprio 0
	s_add_i32 s54, s54, 2
	s_add_u32 s16, s16, 0x100
	s_addc_u32 s17, s17, 0
	s_add_u32 s52, s52, 0x100
	s_addc_u32 s53, s53, 0
	s_cmp_gt_u32 s54, 9
	s_barrier
	s_cbranch_scc0 .LBB0_2382
	v_pk_mul_f32 v[140:141], v[124:125], s[8:9] op_sel_hi:[1,0]
	v_pk_mul_f32 v[120:121], v[120:121], s[8:9] op_sel_hi:[1,0]
	v_mov_b32_e32 v125, v129
	v_cvt_pk_fp8_f32 v125, v120, v121
	v_pk_mul_f32 v[120:121], v[126:127], s[8:9] op_sel_hi:[1,0]
	v_pk_mul_f32 v[116:117], v[116:117], s[8:9] op_sel_hi:[1,0]
	v_mov_b32_e32 v126, v129
	v_cvt_pk_fp8_f32 v126, v116, v117
	v_pk_mul_f32 v[112:113], v[112:113], s[8:9] op_sel_hi:[1,0]
	v_mov_b32_e32 v127, v129
	v_cvt_pk_fp8_f32 v127, v112, v113
	v_pk_mul_f32 v[112:113], v[118:119], s[8:9] op_sel_hi:[1,0]
	v_pk_mul_f32 v[104:105], v[104:105], s[8:9] op_sel_hi:[1,0]
	v_cvt_pk_fp8_f32 v126, v112, v113 op_sel:[0,0,1]
	v_pk_mul_f32 v[112:113], v[114:115], s[8:9] op_sel_hi:[1,0]
	v_pk_mul_f32 v[100:101], v[100:101], s[8:9] op_sel_hi:[1,0]
	v_cvt_pk_fp8_f32 v127, v112, v113 op_sel:[0,0,1]
	v_pk_mul_f32 v[112:113], v[108:109], s[8:9] op_sel_hi:[1,0]
	v_mov_b32_e32 v109, v129
	v_cvt_pk_fp8_f32 v109, v104, v105
	v_pk_mul_f32 v[104:105], v[110:111], s[8:9] op_sel_hi:[1,0]
	v_mov_b32_e32 v110, v129
	v_cvt_pk_fp8_f32 v110, v100, v101
	v_pk_mul_f32 v[100:101], v[92:93], s[8:9] op_sel_hi:[1,0]
	v_pk_mul_f32 v[88:89], v[88:89], s[8:9] op_sel_hi:[1,0]
	v_mov_b32_e32 v93, v129
	v_cvt_pk_fp8_f32 v93, v88, v89
	v_pk_mul_f32 v[88:89], v[94:95], s[8:9] op_sel_hi:[1,0]
	v_pk_mul_f32 v[84:85], v[84:85], s[8:9] op_sel_hi:[1,0]
	v_mov_b32_e32 v94, v129
	v_cvt_pk_fp8_f32 v94, v84, v85
	v_pk_mul_f32 v[80:81], v[80:81], s[8:9] op_sel_hi:[1,0]
	v_mov_b32_e32 v95, v129
	v_cvt_pk_fp8_f32 v95, v80, v81
	v_pk_mul_f32 v[80:81], v[86:87], s[8:9] op_sel_hi:[1,0]
	v_pk_mul_f32 v[72:73], v[72:73], s[8:9] op_sel_hi:[1,0]
	v_cvt_pk_fp8_f32 v94, v80, v81 op_sel:[0,0,1]
	v_pk_mul_f32 v[80:81], v[82:83], s[8:9] op_sel_hi:[1,0]
	v_pk_mul_f32 v[68:69], v[68:69], s[8:9] op_sel_hi:[1,0]
	v_cvt_pk_fp8_f32 v95, v80, v81 op_sel:[0,0,1]
	v_pk_mul_f32 v[80:81], v[76:77], s[8:9] op_sel_hi:[1,0]
	v_mov_b32_e32 v77, v129
	v_cvt_pk_fp8_f32 v77, v72, v73
	v_pk_mul_f32 v[72:73], v[78:79], s[8:9] op_sel_hi:[1,0]
	v_mov_b32_e32 v78, v129
	v_cvt_pk_fp8_f32 v78, v68, v69
	v_pk_mul_f32 v[64:65], v[64:65], s[8:9] op_sel_hi:[1,0]
	v_mov_b32_e32 v79, v129
	v_cvt_pk_fp8_f32 v79, v64, v65
	v_pk_mul_f32 v[64:65], v[70:71], s[8:9] op_sel_hi:[1,0]
	v_pk_mul_f32 v[56:57], v[56:57], s[8:9] op_sel_hi:[1,0]
	v_cvt_pk_fp8_f32 v78, v64, v65 op_sel:[0,0,1]
	v_pk_mul_f32 v[64:65], v[66:67], s[8:9] op_sel_hi:[1,0]
	v_pk_mul_f32 v[52:53], v[52:53], s[8:9] op_sel_hi:[1,0]
	v_cvt_pk_fp8_f32 v79, v64, v65 op_sel:[0,0,1]
	v_pk_mul_f32 v[64:65], v[60:61], s[8:9] op_sel_hi:[1,0]
	v_mov_b32_e32 v61, v129
	v_cvt_pk_fp8_f32 v61, v56, v57
	v_pk_mul_f32 v[56:57], v[62:63], s[8:9] op_sel_hi:[1,0]
	v_mov_b32_e32 v62, v129
	v_cvt_pk_fp8_f32 v62, v52, v53
	v_pk_mul_f32 v[48:49], v[48:49], s[8:9] op_sel_hi:[1,0]
	v_mov_b32_e32 v63, v129
	v_cvt_pk_fp8_f32 v63, v48, v49
	s_lshl_b32 s16, s50, 8
	v_pk_mul_f32 v[48:49], v[54:55], s[8:9] op_sel_hi:[1,0]
	s_add_i32 s16, s16, s34
	v_cvt_pk_fp8_f32 v62, v48, v49 op_sel:[0,0,1]
	v_pk_mul_f32 v[48:49], v[50:51], s[8:9] op_sel_hi:[1,0]
	s_lshl_b32 s18, s51, 8
	s_ashr_i32 s17, s16, 31
	v_cvt_pk_fp8_f32 v63, v48, v49 op_sel:[0,0,1]
	v_pk_mul_f32 v[48:49], v[44:45], s[8:9] op_sel_hi:[1,0]
	v_pk_mul_f32 v[40:41], v[40:41], s[8:9] op_sel_hi:[1,0]
	v_mov_b32_e32 v45, v129
	s_ashr_i32 s19, s18, 31
	s_lshl_b64 s[20:21], s[16:17], 11
	v_cvt_pk_fp8_f32 v45, v40, v41
	v_pk_mul_f32 v[40:41], v[46:47], s[8:9] op_sel_hi:[1,0]
	v_pk_mul_f32 v[36:37], v[36:37], s[8:9] op_sel_hi:[1,0]
	v_mov_b32_e32 v46, v129
	s_add_u32 s17, s31, s20
	v_cvt_pk_fp8_f32 v46, v36, v37
	v_pk_mul_f32 v[36:37], v[28:29], s[8:9] op_sel_hi:[1,0]
	v_pk_mul_f32 v[24:25], v[24:25], s[8:9] op_sel_hi:[1,0]
	v_mov_b32_e32 v29, v129
	s_addc_u32 s20, s33, s21
	v_cvt_pk_fp8_f32 v29, v24, v25
	v_pk_mul_f32 v[24:25], v[30:31], s[8:9] op_sel_hi:[1,0]
	v_pk_mul_f32 v[20:21], v[20:21], s[8:9] op_sel_hi:[1,0]
	v_mov_b32_e32 v30, v129
	s_add_u32 s17, s17, s18
	v_cvt_pk_fp8_f32 v30, v20, v21
	v_pk_mul_f32 v[16:17], v[16:17], s[8:9] op_sel_hi:[1,0]
	v_mov_b32_e32 v31, v129
	s_addc_u32 s21, s20, s19
	v_cvt_pk_fp8_f32 v31, v16, v17
	s_add_u32 s20, s17, s35
	s_addc_u32 s21, s21, 0
	s_addk_i32 s16, 0x80
	v_pk_mul_f32 v[16:17], v[22:23], s[8:9] op_sel_hi:[1,0]
	s_ashr_i32 s17, s16, 31
	v_cvt_pk_fp8_f32 v30, v16, v17 op_sel:[0,0,1]
	v_pk_mul_f32 v[16:17], v[18:19], s[8:9] op_sel_hi:[1,0]
	v_mov_b32_e32 v124, v129
	v_mov_b32_e32 v108, v129
	v_pk_mul_f32 v[96:97], v[96:97], s[8:9] op_sel_hi:[1,0]
	v_mov_b32_e32 v111, v129
	v_mov_b32_e32 v92, v129
	s_lshl_b64 s[16:17], s[16:17], 11
	v_mov_b32_e32 v60, v129
	v_mov_b32_e32 v44, v129
	v_mov_b32_e32 v28, v129
	v_cvt_pk_fp8_f32 v31, v16, v17 op_sel:[0,0,1]
	v_pk_mul_f32 v[16:17], v[12:13], s[8:9] op_sel_hi:[1,0]
	v_pk_mul_f32 v[8:9], v[8:9], s[8:9] op_sel_hi:[1,0]
	v_mov_b32_e32 v13, v129
	v_mbcnt_lo_u32_b32 v128, -1, 0
	v_mbcnt_hi_u32_b32 v128, -1, v128
	v_cvt_pk_fp8_f32 v124, v140, v141
	v_ashrrev_i32_e32 v130, 1, v128
	v_cvt_pk_fp8_f32 v108, v112, v113
	v_cvt_pk_fp8_f32 v111, v96, v97
	v_cvt_pk_fp8_f32 v92, v100, v101
	v_mov_b32_e32 v76, v129
	v_cvt_pk_fp8_f32 v60, v64, v65
	v_cvt_pk_fp8_f32 v44, v48, v49
	v_pk_mul_f32 v[32:33], v[32:33], s[8:9] op_sel_hi:[1,0]
	v_mov_b32_e32 v47, v129
	s_add_u32 s16, s31, s16
	v_cvt_pk_fp8_f32 v28, v36, v37
	v_mov_b32_e32 v12, v129
	v_cvt_pk_fp8_f32 v13, v8, v9
	v_pk_mul_f32 v[8:9], v[14:15], s[8:9] op_sel_hi:[1,0]
	v_pk_mul_f32 v[4:5], v[4:5], s[8:9] op_sel_hi:[1,0]
	v_mov_b32_e32 v14, v129
	v_bfi_b32 v130, -16, v130, v128
	v_cvt_pk_fp8_f32 v76, v80, v81
	v_cvt_pk_fp8_f32 v47, v32, v33
	s_addc_u32 s17, s33, s17
	v_cvt_pk_fp8_f32 v12, v16, v17
	v_cvt_pk_fp8_f32 v14, v4, v5
	v_pk_mul_f32 v[0:1], v[0:1], s[8:9] op_sel_hi:[1,0]
	v_mov_b32_e32 v15, v129
	v_ashrrev_i32_e32 v131, 31, v130
	v_pk_mul_f32 v[96:97], v[102:103], s[8:9] op_sel_hi:[1,0]
	s_add_u32 s16, s16, s18
	v_cvt_pk_fp8_f32 v15, v0, v1
	v_lshlrev_b64 v[130:131], 11, v[130:131]
	v_cvt_pk_fp8_f32 v110, v96, v97 op_sel:[0,0,1]
	v_pk_mul_f32 v[96:97], v[98:99], s[8:9] op_sel_hi:[1,0]
	v_pk_mul_f32 v[32:33], v[38:39], s[8:9] op_sel_hi:[1,0]
	s_addc_u32 s17, s17, s19
	v_and_b32_e32 v128, 16, v128
	v_cvt_pk_fp8_f32 v124, v120, v121 op_sel:[0,0,1]
	v_pk_mul_f32 v[120:121], v[122:123], s[8:9] op_sel_hi:[1,0]
	v_cvt_pk_fp8_f32 v108, v104, v105 op_sel:[0,0,1]
	v_pk_mul_f32 v[104:105], v[106:107], s[8:9] op_sel_hi:[1,0]
	v_cvt_pk_fp8_f32 v111, v96, v97 op_sel:[0,0,1]
	v_lshl_add_u64 v[96:97], s[20:21], 0, v[130:131]
	v_cvt_pk_fp8_f32 v92, v88, v89 op_sel:[0,0,1]
	v_pk_mul_f32 v[88:89], v[90:91], s[8:9] op_sel_hi:[1,0]
	v_cvt_pk_fp8_f32 v60, v56, v57 op_sel:[0,0,1]
	v_pk_mul_f32 v[56:57], v[58:59], s[8:9] op_sel_hi:[1,0]
	v_cvt_pk_fp8_f32 v44, v40, v41 op_sel:[0,0,1]
	v_pk_mul_f32 v[40:41], v[42:43], s[8:9] op_sel_hi:[1,0]
	v_cvt_pk_fp8_f32 v46, v32, v33 op_sel:[0,0,1]
	v_pk_mul_f32 v[32:33], v[34:35], s[8:9] op_sel_hi:[1,0]
	s_add_u32 s16, s16, s35
	v_cvt_pk_fp8_f32 v28, v24, v25 op_sel:[0,0,1]
	v_pk_mul_f32 v[24:25], v[26:27], s[8:9] op_sel_hi:[1,0]
	v_pk_mul_f32 v[0:1], v[6:7], s[8:9] op_sel_hi:[1,0]
	v_cvt_pk_fp8_f32 v125, v120, v121 op_sel:[0,0,1]
	v_cvt_pk_fp8_f32 v109, v104, v105 op_sel:[0,0,1]
	v_lshl_add_u64 v[96:97], v[96:97], 0, v[128:129]
	v_cvt_pk_fp8_f32 v93, v88, v89 op_sel:[0,0,1]
	v_cvt_pk_fp8_f32 v76, v72, v73 op_sel:[0,0,1]
	v_pk_mul_f32 v[72:73], v[74:75], s[8:9] op_sel_hi:[1,0]
	v_cvt_pk_fp8_f32 v61, v56, v57 op_sel:[0,0,1]
	v_cvt_pk_fp8_f32 v45, v40, v41 op_sel:[0,0,1]
	v_cvt_pk_fp8_f32 v47, v32, v33 op_sel:[0,0,1]
	s_addc_u32 s17, s17, 0
	v_cvt_pk_fp8_f32 v29, v24, v25 op_sel:[0,0,1]
	v_cvt_pk_fp8_f32 v12, v8, v9 op_sel:[0,0,1]
	v_pk_mul_f32 v[8:9], v[10:11], s[8:9] op_sel_hi:[1,0]
	v_cvt_pk_fp8_f32 v14, v0, v1 op_sel:[0,0,1]
	v_pk_mul_f32 v[0:1], v[2:3], s[8:9] op_sel_hi:[1,0]
	v_add_co_u32_e32 v98, vcc, s30, v96
	v_cvt_pk_fp8_f32 v77, v72, v73 op_sel:[0,0,1]
	v_lshl_add_u64 v[32:33], s[16:17], 0, v[130:131]
	v_cvt_pk_fp8_f32 v13, v8, v9 op_sel:[0,0,1]
	v_cvt_pk_fp8_f32 v15, v0, v1 op_sel:[0,0,1]
	v_addc_co_u32_e32 v99, vcc, 0, v97, vcc
	v_lshl_add_u64 v[32:33], v[32:33], 0, v[128:129]
	v_add_co_u32_e32 v34, vcc, s30, v32
	v_permlane32_swap_b32_e32 v124, v126
	v_permlane32_swap_b32_e32 v125, v127
	v_permlane32_swap_b32_e32 v108, v110
	v_permlane32_swap_b32_e32 v109, v111
	v_permlane32_swap_b32_e32 v92, v94
	v_permlane32_swap_b32_e32 v93, v95
	v_permlane32_swap_b32_e32 v60, v62
	v_permlane32_swap_b32_e32 v61, v63
	v_permlane32_swap_b32_e32 v44, v46
	v_permlane32_swap_b32_e32 v45, v47
	v_addc_co_u32_e32 v35, vcc, 0, v33, vcc
	v_permlane32_swap_b32_e32 v28, v30
	v_permlane32_swap_b32_e32 v29, v31
	v_permlane16_swap_b32_e32 v124, v125
	v_permlane16_swap_b32_e32 v126, v127
	v_permlane16_swap_b32_e32 v108, v109
	v_permlane16_swap_b32_e32 v110, v111
	v_permlane16_swap_b32_e32 v92, v93
	v_permlane16_swap_b32_e32 v94, v95
	v_permlane32_swap_b32_e32 v76, v78
	v_permlane32_swap_b32_e32 v77, v79
	v_permlane16_swap_b32_e32 v60, v61
	v_permlane16_swap_b32_e32 v62, v63
	v_permlane16_swap_b32_e32 v44, v45
	v_permlane16_swap_b32_e32 v46, v47
	v_permlane16_swap_b32_e32 v28, v29
	v_permlane16_swap_b32_e32 v30, v31
	v_permlane32_swap_b32_e32 v12, v14
	v_permlane32_swap_b32_e32 v13, v15
	s_and_b64 vcc, exec, s[10:11]
	s_mov_b32 s51, s49
	s_mov_b32 s50, s48
	s_mov_b64 s[18:19], s[12:13]
	s_mov_b64 s[16:17], s[14:15]
	global_store_dwordx4 v[96:97], v[124:127], off
	global_store_dwordx4 v[98:99], v[108:111], off
	v_permlane16_swap_b32_e32 v76, v77
	v_permlane16_swap_b32_e32 v78, v79
	global_store_dwordx4 v[96:97], v[92:95], off offset:128
	global_store_dwordx4 v[98:99], v[76:79], off offset:128
	global_store_dwordx4 v[32:33], v[60:63], off
	global_store_dwordx4 v[34:35], v[44:47], off
	v_permlane16_swap_b32_e32 v12, v13
	v_permlane16_swap_b32_e32 v14, v15
	global_store_dwordx4 v[32:33], v[28:31], off offset:128
	global_store_dwordx4 v[34:35], v[12:15], off offset:128
	s_cbranch_vccz .LBB0_2377
	s_waitcnt vmcnt(0)
	v_readlane_b32 s0, v252, 2
	s_cmpk_gt_u32 s0, 0xff
	s_cbranch_scc1 .LBB0_2386
	s_barrier

.LBB0_3995:
	s_add_i32 s34, s6, 2
	s_add_u32 s8, s4, 0xfffe0080
	s_addc_u32 s7, s5, -1
	s_add_i32 s30, 0, 0x10000
	v_add_u32_e32 v140, s30, v200
	ds_read_b128 v[128:131], v140
	ds_read_b128 v[132:135], v140 offset:1024
	ds_read_b128 v[136:139], v140 offset:2048
	ds_read_b128 v[140:143], v140 offset:3072
	s_cmp_eq_u32 s12, s6
	s_cselect_b32 s6, s52, s8
	s_cselect_b32 s7, s53, s7
	s_cselect_b32 s9, s55, s27
	s_cselect_b32 s8, s54, s25
	v_mov_b32_e32 v168, v169
	ds_read_b128 v[144:147], v182
	ds_read_b128 v[148:151], v182 offset:1024
	ds_read_b128 v[152:155], v182 offset:2048
	ds_read_b128 v[156:159], v182 offset:3072
	ds_read_b128 v[160:163], v182 offset:4096
	ds_read_b128 v[164:167], v182 offset:5120
	ds_read_b128 v[184:187], v182 offset:6144
	ds_read_b128 v[188:191], v182 offset:7168
	s_nop 0
	v_mov_b32_e32 v168, v181
	s_nop 0
	s_waitcnt lgkmcnt(8)
	s_barrier
	s_waitcnt lgkmcnt(0)
	s_setprio 1
	s_waitcnt lgkmcnt(0)
	v_mfma_scale_f32_16x16x128_f8f6f4 v[120:123], v[128:135], v[144:151], v[120:123], v183, v183 op_sel_hi:[0,0,0]
	v_mov_b32_e32 v170, v200
	v_mfma_scale_f32_16x16x128_f8f6f4 v[124:127], v[136:143], v[144:151], v[124:127], v183, v183 op_sel_hi:[0,0,0]
	v_mfma_scale_f32_16x16x128_f8f6f4 v[200:203], v[136:143], v[160:167], v[88:91], v183, v183 op_sel_hi:[0,0,0]
	v_mfma_scale_f32_16x16x128_f8f6f4 v[176:179], v[128:135], v[152:159], v[108:111], v183, v183 op_sel_hi:[0,0,0]
	s_add_i32 m0, s3, 0xc000
	v_mfma_scale_f32_16x16x128_f8f6f4 v[192:195], v[136:143], v[152:159], v[104:107], v183, v183 op_sel_hi:[0,0,0]
	global_load_lds_dwordx4 v169, s[4:5]
	v_mfma_scale_f32_16x16x128_f8f6f4 v[196:199], v[128:135], v[160:167], v[92:95], v183, v183 op_sel_hi:[0,0,0]
	v_mfma_scale_f32_16x16x128_f8f6f4 v[204:207], v[128:135], v[184:191], v[76:79], v183, v183 op_sel_hi:[0,0,0]
	s_add_i32 m0, s3, 0xe000
	v_mfma_scale_f32_16x16x128_f8f6f4 v[208:211], v[136:143], v[184:191], v[72:75], v183, v183 op_sel_hi:[0,0,0]
	global_load_lds_dwordx4 v181, s[4:5]
	s_setprio 0
	s_barrier
	s_add_i32 s35, 0, 0x14000
	s_nop 1
	v_add_u32_e32 v92, s35, v170
	v_mov_b32_e32 v104, v180
	s_add_i32 s30, s30, s33
	ds_read_b128 v[72:75], v92
	ds_read_b128 v[76:79], v92 offset:1024
	ds_read_b128 v[88:91], v92 offset:2048
	ds_read_b128 v[92:95], v92 offset:3072
	s_mov_b32 m0, s30
	s_nop 0
	global_load_lds_dwordx4 v104, s[8:9]
	v_mov_b32_e32 v104, v212
	s_add_i32 m0, s30, 0x2000
	s_nop 0
	global_load_lds_dwordx4 v104, s[8:9]
	s_barrier
	s_waitcnt lgkmcnt(0)
	s_setprio 1
	s_waitcnt lgkmcnt(0)
	v_mfma_scale_f32_16x16x128_f8f6f4 v[116:119], v[144:151], v[72:79], v[116:119], v183, v183 op_sel_hi:[0,0,0]
	v_mov_b32_e32 v168, v212
	v_mfma_scale_f32_16x16x128_f8f6f4 v[112:115], v[144:151], v[88:95], v[112:115], v183, v183 op_sel_hi:[0,0,0]
	v_mfma_scale_f32_16x16x128_f8f6f4 v[212:215], v[152:159], v[72:79], v[100:103], v183, v183 op_sel_hi:[0,0,0]
	v_mfma_scale_f32_16x16x128_f8f6f4 v[216:219], v[152:159], v[88:95], v[96:99], v183, v183 op_sel_hi:[0,0,0]
	v_mfma_scale_f32_16x16x128_f8f6f4 v[220:223], v[160:167], v[72:79], v[84:87], v183, v183 op_sel_hi:[0,0,0]
	v_mfma_scale_f32_16x16x128_f8f6f4 v[160:163], v[160:167], v[88:95], v[80:83], v183, v183 op_sel_hi:[0,0,0]
	v_mfma_scale_f32_16x16x128_f8f6f4 v[164:167], v[184:191], v[72:79], v[68:71], v183, v183 op_sel_hi:[0,0,0]
	v_mfma_scale_f32_16x16x128_f8f6f4 v[184:187], v[184:191], v[88:95], v[64:67], v183, v183 op_sel_hi:[0,0,0]
	s_setprio 0
	v_mov_b32_e32 v144, v169
	s_barrier
	s_nop 2
	ds_read_b128 v[64:67], v182 offset:16384
	ds_read_b128 v[68:71], v182 offset:17408
	ds_read_b128 v[80:83], v182 offset:18432
	ds_read_b128 v[84:87], v182 offset:19456
	ds_read_b128 v[96:99], v182 offset:20480
	ds_read_b128 v[100:103], v182 offset:21504
	ds_read_b128 v[104:107], v182 offset:22528
	ds_read_b128 v[108:111], v182 offset:23552
	s_nop 0
	v_mov_b32_e32 v144, v181
	s_nop 0
	s_barrier
	s_waitcnt lgkmcnt(0)
	s_setprio 1
	s_waitcnt lgkmcnt(0)
	v_mfma_scale_f32_16x16x128_f8f6f4 v[224:227], v[128:135], v[64:71], v[60:63], v183, v183 op_sel_hi:[0,0,0]
	v_mfma_scale_f32_16x16x128_f8f6f4 v[228:231], v[136:143], v[64:71], v[56:59], v183, v183 op_sel_hi:[0,0,0]
	v_mfma_scale_f32_16x16x128_f8f6f4 v[232:235], v[128:135], v[80:87], v[44:47], v183, v183 op_sel_hi:[0,0,0]
	v_mfma_scale_f32_16x16x128_f8f6f4 v[236:239], v[136:143], v[80:87], v[40:43], v183, v183 op_sel_hi:[0,0,0]
	s_mov_b32 m0, s3
	v_mfma_scale_f32_16x16x128_f8f6f4 v[240:243], v[128:135], v[96:103], v[28:31], v183, v183 op_sel_hi:[0,0,0]
	global_load_lds_dwordx4 v169, s[6:7]
	v_mfma_scale_f32_16x16x128_f8f6f4 v[244:247], v[136:143], v[96:103], v[24:27], v183, v183 op_sel_hi:[0,0,0]
	v_mfma_scale_f32_16x16x128_f8f6f4 v[248:251], v[128:135], v[104:111], v[12:15], v183, v183 op_sel_hi:[0,0,0]
	s_mov_b32 m0, s11
	v_mfma_scale_f32_16x16x128_f8f6f4 v[172:175], v[136:143], v[104:111], v[8:11], v183, v183 op_sel_hi:[0,0,0]
	global_load_lds_dwordx4 v181, s[6:7]
	s_setprio 0
	s_barrier
	s_add_u32 s30, s8, s20
	s_addc_u32 s31, s9, s21
	s_nop 2
	v_mov_b32_e32 v8, v180
	s_add_i32 s35, s35, s33
	s_mov_b32 s100, s35
	s_nop 0
	v_mov_b32_e32 v8, v168
	s_add_i32 s101, s35, 0x2000
	s_nop 0
	s_waitcnt vmcnt(4)
	s_barrier
	s_setprio 1
	v_mfma_scale_f32_16x16x128_f8f6f4 v[52:55], v[64:71], v[72:79], v[52:55], v183, v183 op_sel_hi:[0,0,0]
	v_mfma_scale_f32_16x16x128_f8f6f4 v[48:51], v[64:71], v[88:95], v[48:51], v183, v183 op_sel_hi:[0,0,0]
	v_mfma_scale_f32_16x16x128_f8f6f4 v[36:39], v[80:87], v[72:79], v[36:39], v183, v183 op_sel_hi:[0,0,0]
	v_mfma_scale_f32_16x16x128_f8f6f4 v[32:35], v[80:87], v[88:95], v[32:35], v183, v183 op_sel_hi:[0,0,0]
	s_mov_b32 m0, s100
	v_mfma_scale_f32_16x16x128_f8f6f4 v[20:23], v[96:103], v[72:79], v[20:23], v183, v183 op_sel_hi:[0,0,0]
	global_load_lds_dwordx4 v180, s[30:31]
	v_mfma_scale_f32_16x16x128_f8f6f4 v[16:19], v[96:103], v[88:95], v[16:19], v183, v183 op_sel_hi:[0,0,0]
	v_mfma_scale_f32_16x16x128_f8f6f4 v[4:7], v[104:111], v[72:79], v[4:7], v183, v183 op_sel_hi:[0,0,0]
	s_mov_b32 m0, s101
	v_mfma_scale_f32_16x16x128_f8f6f4 v[0:3], v[104:111], v[88:95], v[0:3], v183, v183 op_sel_hi:[0,0,0]
	global_load_lds_dwordx4 v168, s[30:31]
	s_setprio 0
	s_add_i32 s35, 0, 0x18000
	v_add_u32_e32 v24, s35, v170
	s_barrier
	ds_read_b128 v[8:11], v24
	ds_read_b128 v[12:15], v24 offset:1024
	ds_read_b128 v[128:131], v24 offset:2048
	ds_read_b128 v[132:135], v24 offset:3072
	s_add_u32 s36, s6, 0x20000
	v_mov_b32_e32 v64, v169
	ds_read_b128 v[24:27], v182 offset:32768
	ds_read_b128 v[28:31], v182 offset:33792
	ds_read_b128 v[40:43], v182 offset:34816
	ds_read_b128 v[44:47], v182 offset:35840
	ds_read_b128 v[56:59], v182 offset:36864
	ds_read_b128 v[60:63], v182 offset:37888
	ds_read_b128 v[136:139], v182 offset:38912
	ds_read_b128 v[140:143], v182 offset:39936
	s_addc_u32 s37, s7, 0
	s_nop 0
	v_mov_b32_e32 v64, v181
	s_nop 0
	s_waitcnt lgkmcnt(8)
	s_barrier
	s_waitcnt lgkmcnt(0)
	s_setprio 1
	s_waitcnt lgkmcnt(0)
	v_mfma_scale_f32_16x16x128_f8f6f4 v[120:123], v[8:15], v[24:31], v[120:123], v183, v183 op_sel_hi:[0,0,0]
	v_mfma_scale_f32_16x16x128_f8f6f4 v[124:127], v[128:135], v[24:31], v[124:127], v183, v183 op_sel_hi:[0,0,0]
	v_mfma_scale_f32_16x16x128_f8f6f4 v[108:111], v[8:15], v[40:47], v[176:179], v183, v183 op_sel_hi:[0,0,0]
	v_mfma_scale_f32_16x16x128_f8f6f4 v[104:107], v[128:135], v[40:47], v[192:195], v183, v183 op_sel_hi:[0,0,0]
	s_mov_b32 m0, s14
	v_mfma_scale_f32_16x16x128_f8f6f4 v[92:95], v[8:15], v[56:63], v[196:199], v183, v183 op_sel_hi:[0,0,0]
	global_load_lds_dwordx4 v169, s[36:37]
	v_mfma_scale_f32_16x16x128_f8f6f4 v[88:91], v[128:135], v[56:63], v[200:203], v183, v183 op_sel_hi:[0,0,0]
	v_mfma_scale_f32_16x16x128_f8f6f4 v[76:79], v[8:15], v[136:143], v[204:207], v183, v183 op_sel_hi:[0,0,0]
	s_mov_b32 m0, s15
	s_nop 5
	v_mov_b32_e32 v200, v170
	v_mfma_scale_f32_16x16x128_f8f6f4 v[72:75], v[128:135], v[136:143], v[208:211], v183, v183 op_sel_hi:[0,0,0]
	global_load_lds_dwordx4 v181, s[36:37]
	s_setprio 0
	s_barrier
	s_add_i32 s36, 0, 0x1c000
	v_add_u32_e32 v64, s36, v200
	v_mov_b32_e32 v170, v180
	ds_read_b128 v[144:147], v64
	ds_read_b128 v[148:151], v64 offset:1024
	ds_read_b128 v[152:155], v64 offset:2048
	ds_read_b128 v[156:159], v64 offset:3072
	s_add_i32 s35, s35, s33
	v_lshl_add_u64 v[64:65], s[8:9], 0, v[170:171]
	v_lshl_add_u64 v[64:65], v[64:65], 0, s[62:63]
	v_mov_b32_e32 v170, v168
	v_lshl_add_u64 v[64:65], s[8:9], 0, v[170:171]
	v_lshl_add_u64 v[64:65], v[64:65], 0, s[62:63]
	s_barrier
	s_waitcnt lgkmcnt(0)
	s_setprio 1
	s_waitcnt lgkmcnt(0)
	v_mfma_scale_f32_16x16x128_f8f6f4 v[116:119], v[24:31], v[144:151], v[116:119], v183, v183 op_sel_hi:[0,0,0]
	v_mfma_scale_f32_16x16x128_f8f6f4 v[112:115], v[24:31], v[152:159], v[112:115], v183, v183 op_sel_hi:[0,0,0]
	v_mfma_scale_f32_16x16x128_f8f6f4 v[100:103], v[40:47], v[144:151], v[212:215], v183, v183 op_sel_hi:[0,0,0]
	v_mfma_scale_f32_16x16x128_f8f6f4 v[96:99], v[40:47], v[152:159], v[216:219], v183, v183 op_sel_hi:[0,0,0]
	s_add_u32 s98, s8, s62
	s_addc_u32 s99, s9, s63
	s_mov_b32 m0, s35
	s_nop 5
	v_mov_b32_e32 v212, v168
	v_mfma_scale_f32_16x16x128_f8f6f4 v[84:87], v[56:63], v[144:151], v[220:223], v183, v183 op_sel_hi:[0,0,0]
	global_load_lds_dwordx4 v180, s[98:99]
	v_mfma_scale_f32_16x16x128_f8f6f4 v[80:83], v[56:63], v[152:159], v[160:163], v183, v183 op_sel_hi:[0,0,0]
	v_mfma_scale_f32_16x16x128_f8f6f4 v[68:71], v[136:143], v[144:151], v[164:167], v183, v183 op_sel_hi:[0,0,0]
	s_add_i32 m0, s35, 0x2000
	v_mfma_scale_f32_16x16x128_f8f6f4 v[64:67], v[136:143], v[152:159], v[184:187], v183, v183 op_sel_hi:[0,0,0]
	global_load_lds_dwordx4 v168, s[98:99]
	s_setprio 0
	v_mov_b32_e32 v170, v169
	s_barrier
	ds_read_b128 v[136:139], v182 offset:49152
	ds_read_b128 v[140:143], v182 offset:50176
	ds_read_b128 v[160:163], v182 offset:51200
	ds_read_b128 v[164:167], v182 offset:52224
	ds_read_b128 v[184:187], v182 offset:53248
	ds_read_b128 v[188:191], v182 offset:54272
	ds_read_b128 v[192:195], v182 offset:55296
	ds_read_b128 v[196:199], v182 offset:56320
	v_lshl_add_u64 v[24:25], s[6:7], 0, v[170:171]
	v_lshl_add_u64 v[24:25], v[24:25], 0, s[62:63]
	v_mov_b32_e32 v170, v181
	v_lshl_add_u64 v[24:25], s[6:7], 0, v[170:171]
	v_lshl_add_u64 v[24:25], v[24:25], 0, s[62:63]
	s_barrier
	s_waitcnt lgkmcnt(0)
	s_setprio 1
	s_waitcnt lgkmcnt(0)
	v_mfma_scale_f32_16x16x128_f8f6f4 v[60:63], v[8:15], v[136:143], v[224:227], v183, v183 op_sel_hi:[0,0,0]
	v_mfma_scale_f32_16x16x128_f8f6f4 v[56:59], v[128:135], v[136:143], v[228:231], v183, v183 op_sel_hi:[0,0,0]
	v_mfma_scale_f32_16x16x128_f8f6f4 v[44:47], v[8:15], v[160:167], v[232:235], v183, v183 op_sel_hi:[0,0,0]
	v_mfma_scale_f32_16x16x128_f8f6f4 v[40:43], v[128:135], v[160:167], v[236:239], v183, v183 op_sel_hi:[0,0,0]
	s_add_u32 s98, s6, s62
	s_addc_u32 s99, s7, s63
	s_mov_b32 m0, s16
	v_mfma_scale_f32_16x16x128_f8f6f4 v[28:31], v[8:15], v[184:191], v[240:243], v183, v183 op_sel_hi:[0,0,0]
	global_load_lds_dwordx4 v169, s[98:99]
	v_mfma_scale_f32_16x16x128_f8f6f4 v[24:27], v[128:135], v[184:191], v[244:247], v183, v183 op_sel_hi:[0,0,0]
	v_mfma_scale_f32_16x16x128_f8f6f4 v[12:15], v[8:15], v[192:199], v[248:251], v183, v183 op_sel_hi:[0,0,0]
	s_mov_b32 m0, s17
	v_mfma_scale_f32_16x16x128_f8f6f4 v[8:11], v[128:135], v[192:199], v[172:175], v183, v183 op_sel_hi:[0,0,0]
	global_load_lds_dwordx4 v181, s[98:99]
	s_setprio 0
	s_barrier
	v_mov_b32_e32 v170, v180
	s_add_i32 s6, s36, s33
	v_lshl_add_u64 v[128:129], s[30:31], 0, v[170:171]
	v_lshl_add_u64 v[128:129], v[128:129], 0, s[62:63]
	s_mov_b32 s100, s6
	v_mov_b32_e32 v170, v168
	s_add_i32 s101, s6, 0x2000
	v_lshl_add_u64 v[128:129], s[30:31], 0, v[170:171]
	v_lshl_add_u64 v[128:129], v[128:129], 0, s[62:63]
	s_waitcnt vmcnt(4)
	s_barrier
	s_setprio 1
	v_mfma_scale_f32_16x16x128_f8f6f4 v[52:55], v[136:143], v[144:151], v[52:55], v183, v183 op_sel_hi:[0,0,0]
	v_mfma_scale_f32_16x16x128_f8f6f4 v[48:51], v[136:143], v[152:159], v[48:51], v183, v183 op_sel_hi:[0,0,0]
	v_mfma_scale_f32_16x16x128_f8f6f4 v[36:39], v[160:167], v[144:151], v[36:39], v183, v183 op_sel_hi:[0,0,0]
	v_mfma_scale_f32_16x16x128_f8f6f4 v[32:35], v[160:167], v[152:159], v[32:35], v183, v183 op_sel_hi:[0,0,0]
	s_add_u32 s98, s30, s62
	s_addc_u32 s99, s31, s63
	s_mov_b32 m0, s100
	v_mfma_scale_f32_16x16x128_f8f6f4 v[20:23], v[184:191], v[144:151], v[20:23], v183, v183 op_sel_hi:[0,0,0]
	global_load_lds_dwordx4 v180, s[98:99]
	v_mfma_scale_f32_16x16x128_f8f6f4 v[16:19], v[184:191], v[152:159], v[16:19], v183, v183 op_sel_hi:[0,0,0]
	v_mfma_scale_f32_16x16x128_f8f6f4 v[4:7], v[192:199], v[144:151], v[4:7], v183, v183 op_sel_hi:[0,0,0]
	s_mov_b32 m0, s101
	v_mfma_scale_f32_16x16x128_f8f6f4 v[0:3], v[192:199], v[152:159], v[0:3], v183, v183 op_sel_hi:[0,0,0]
	global_load_lds_dwordx4 v168, s[98:99]
	s_setprio 0
	s_add_u32 s4, s4, 0x100
	s_addc_u32 s5, s5, 0
	s_add_u32 s25, s25, 0x100
	s_addc_u32 s27, s27, 0
	s_cmp_ge_i32 s34, s13
	s_mov_b32 s6, s34
	s_barrier
	s_cbranch_scc0 .LBB0_3995

.LBB0_4066:
	s_add_i32 s34, s6, 2
	s_add_u32 s8, s4, 0xfffe0080
	s_addc_u32 s7, s5, -1
	s_add_i32 s30, 0, 0x10000
	v_add_u32_e32 v140, s30, v181
	ds_read_b128 v[128:131], v140
	ds_read_b128 v[132:135], v140 offset:1024
	ds_read_b128 v[136:139], v140 offset:2048
	ds_read_b128 v[140:143], v140 offset:3072
	s_cmp_eq_u32 s12, s6
	s_cselect_b32 s6, s52, s8
	s_cselect_b32 s7, s53, s7
	s_cselect_b32 s9, s55, s27
	s_cselect_b32 s8, s54, s25
	v_mov_b32_e32 v168, v169
	ds_read_b128 v[144:147], v182
	ds_read_b128 v[148:151], v182 offset:1024
	ds_read_b128 v[152:155], v182 offset:2048
	ds_read_b128 v[156:159], v182 offset:3072
	ds_read_b128 v[160:163], v182 offset:4096
	ds_read_b128 v[164:167], v182 offset:5120
	ds_read_b128 v[184:187], v182 offset:6144
	ds_read_b128 v[188:191], v182 offset:7168
	s_add_i32 m0, s3, 0xc000
	s_nop 0
	global_load_lds_dwordx4 v168, s[4:5]
	v_mov_b32_e32 v168, v200
	s_add_i32 m0, s3, 0xe000
	s_nop 0
	global_load_lds_dwordx4 v168, s[4:5]
	s_waitcnt lgkmcnt(8)
	s_barrier
	s_waitcnt lgkmcnt(0)
	s_setprio 1
	s_waitcnt lgkmcnt(0)
	v_mfma_scale_f32_16x16x128_f8f6f4 v[120:123], v[128:135], v[144:151], v[120:123], v183, v183 op_sel_hi:[0,0,0]
	v_mov_b32_e32 v170, v200
	v_mfma_scale_f32_16x16x128_f8f6f4 v[124:127], v[136:143], v[144:151], v[124:127], v183, v183 op_sel_hi:[0,0,0]
	v_mfma_scale_f32_16x16x128_f8f6f4 v[200:203], v[128:135], v[160:167], v[92:95], v183, v183 op_sel_hi:[0,0,0]
	v_mfma_scale_f32_16x16x128_f8f6f4 v[192:195], v[128:135], v[152:159], v[108:111], v183, v183 op_sel_hi:[0,0,0]
	v_mfma_scale_f32_16x16x128_f8f6f4 v[196:199], v[136:143], v[152:159], v[104:107], v183, v183 op_sel_hi:[0,0,0]
	v_mfma_scale_f32_16x16x128_f8f6f4 v[204:207], v[136:143], v[160:167], v[88:91], v183, v183 op_sel_hi:[0,0,0]
	v_mfma_scale_f32_16x16x128_f8f6f4 v[208:211], v[128:135], v[184:191], v[76:79], v183, v183 op_sel_hi:[0,0,0]
	v_mfma_scale_f32_16x16x128_f8f6f4 v[212:215], v[136:143], v[184:191], v[72:75], v183, v183 op_sel_hi:[0,0,0]
	s_setprio 0
	s_barrier
	s_add_i32 s35, 0, 0x14000
	v_add_u32_e32 v92, s35, v181
	v_mov_b32_e32 v104, v216
	s_add_i32 s30, s30, s33
	s_nop 0
	ds_read_b128 v[72:75], v92
	ds_read_b128 v[76:79], v92 offset:1024
	ds_read_b128 v[88:91], v92 offset:2048
	ds_read_b128 v[92:95], v92 offset:3072
	s_mov_b32 m0, s30
	s_nop 0
	global_load_lds_dwordx4 v104, s[8:9]
	v_mov_b32_e32 v104, v180
	s_add_i32 m0, s30, 0x2000
	s_nop 0
	global_load_lds_dwordx4 v104, s[8:9]
	s_barrier
	s_waitcnt lgkmcnt(0)
	s_setprio 1
	s_waitcnt lgkmcnt(0)
	v_mfma_scale_f32_16x16x128_f8f6f4 v[116:119], v[72:79], v[144:151], v[116:119], v183, v183 op_sel_hi:[0,0,0]
	v_mov_b32_e32 v168, v216
	v_mfma_scale_f32_16x16x128_f8f6f4 v[112:115], v[88:95], v[144:151], v[112:115], v183, v183 op_sel_hi:[0,0,0]
	v_mfma_scale_f32_16x16x128_f8f6f4 v[216:219], v[72:79], v[152:159], v[100:103], v183, v183 op_sel_hi:[0,0,0]
	v_mfma_scale_f32_16x16x128_f8f6f4 v[220:223], v[88:95], v[152:159], v[96:99], v183, v183 op_sel_hi:[0,0,0]
	v_mfma_scale_f32_16x16x128_f8f6f4 v[224:227], v[72:79], v[160:167], v[84:87], v183, v183 op_sel_hi:[0,0,0]
	v_mfma_scale_f32_16x16x128_f8f6f4 v[160:163], v[88:95], v[160:167], v[80:83], v183, v183 op_sel_hi:[0,0,0]
	v_mfma_scale_f32_16x16x128_f8f6f4 v[164:167], v[72:79], v[184:191], v[68:71], v183, v183 op_sel_hi:[0,0,0]
	v_mfma_scale_f32_16x16x128_f8f6f4 v[184:187], v[88:95], v[184:191], v[64:67], v183, v183 op_sel_hi:[0,0,0]
	s_setprio 0
	v_mov_b32_e32 v144, v169
	s_barrier
	s_nop 2
	ds_read_b128 v[64:67], v182 offset:16384
	ds_read_b128 v[68:71], v182 offset:17408
	ds_read_b128 v[80:83], v182 offset:18432
	ds_read_b128 v[84:87], v182 offset:19456
	ds_read_b128 v[96:99], v182 offset:20480
	ds_read_b128 v[100:103], v182 offset:21504
	ds_read_b128 v[104:107], v182 offset:22528
	ds_read_b128 v[108:111], v182 offset:23552
	s_nop 0
	v_mov_b32_e32 v144, v170
	s_nop 0
	s_barrier
	s_waitcnt lgkmcnt(0)
	s_setprio 1
	s_waitcnt lgkmcnt(0)
	v_mfma_scale_f32_16x16x128_f8f6f4 v[228:231], v[128:135], v[64:71], v[60:63], v183, v183 op_sel_hi:[0,0,0]
	v_mfma_scale_f32_16x16x128_f8f6f4 v[232:235], v[136:143], v[64:71], v[56:59], v183, v183 op_sel_hi:[0,0,0]
	v_mfma_scale_f32_16x16x128_f8f6f4 v[236:239], v[128:135], v[80:87], v[44:47], v183, v183 op_sel_hi:[0,0,0]
	v_mfma_scale_f32_16x16x128_f8f6f4 v[240:243], v[136:143], v[80:87], v[40:43], v183, v183 op_sel_hi:[0,0,0]
	s_mov_b32 m0, s3
	v_mfma_scale_f32_16x16x128_f8f6f4 v[244:247], v[128:135], v[96:103], v[28:31], v183, v183 op_sel_hi:[0,0,0]
	global_load_lds_dwordx4 v169, s[6:7]
	v_mfma_scale_f32_16x16x128_f8f6f4 v[248:251], v[136:143], v[96:103], v[24:27], v183, v183 op_sel_hi:[0,0,0]
	v_mfma_scale_f32_16x16x128_f8f6f4 v[172:175], v[128:135], v[104:111], v[12:15], v183, v183 op_sel_hi:[0,0,0]
	s_mov_b32 m0, s11
	v_mfma_scale_f32_16x16x128_f8f6f4 v[176:179], v[136:143], v[104:111], v[8:11], v183, v183 op_sel_hi:[0,0,0]
	global_load_lds_dwordx4 v170, s[6:7]
	s_setprio 0
	s_barrier
	s_add_u32 s30, s8, s20
	s_addc_u32 s31, s9, s21
	s_nop 2
	v_mov_b32_e32 v8, v168
	s_add_i32 s35, s35, s33
	s_mov_b32 s100, s35
	s_nop 0
	v_mov_b32_e32 v8, v180
	s_add_i32 s101, s35, 0x2000
	s_nop 0
	s_waitcnt vmcnt(4)
	s_barrier
	s_setprio 1
	v_mfma_scale_f32_16x16x128_f8f6f4 v[52:55], v[72:79], v[64:71], v[52:55], v183, v183 op_sel_hi:[0,0,0]
	v_mfma_scale_f32_16x16x128_f8f6f4 v[48:51], v[88:95], v[64:71], v[48:51], v183, v183 op_sel_hi:[0,0,0]
	v_mfma_scale_f32_16x16x128_f8f6f4 v[36:39], v[72:79], v[80:87], v[36:39], v183, v183 op_sel_hi:[0,0,0]
	v_mfma_scale_f32_16x16x128_f8f6f4 v[32:35], v[88:95], v[80:87], v[32:35], v183, v183 op_sel_hi:[0,0,0]
	s_mov_b32 m0, s100
	v_mfma_scale_f32_16x16x128_f8f6f4 v[20:23], v[72:79], v[96:103], v[20:23], v183, v183 op_sel_hi:[0,0,0]
	global_load_lds_dwordx4 v168, s[30:31]
	v_mfma_scale_f32_16x16x128_f8f6f4 v[16:19], v[88:95], v[96:103], v[16:19], v183, v183 op_sel_hi:[0,0,0]
	v_mfma_scale_f32_16x16x128_f8f6f4 v[4:7], v[72:79], v[104:111], v[4:7], v183, v183 op_sel_hi:[0,0,0]
	s_mov_b32 m0, s101
	v_mfma_scale_f32_16x16x128_f8f6f4 v[0:3], v[88:95], v[104:111], v[0:3], v183, v183 op_sel_hi:[0,0,0]
	global_load_lds_dwordx4 v180, s[30:31]
	s_setprio 0
	s_add_i32 s35, 0, 0x18000
	v_add_u32_e32 v24, s35, v181
	s_barrier
	ds_read_b128 v[8:11], v24
	ds_read_b128 v[12:15], v24 offset:1024
	ds_read_b128 v[128:131], v24 offset:2048
	ds_read_b128 v[132:135], v24 offset:3072
	s_add_u32 s36, s6, 0x20000
	v_mov_b32_e32 v64, v169
	ds_read_b128 v[24:27], v182 offset:32768
	ds_read_b128 v[28:31], v182 offset:33792
	ds_read_b128 v[40:43], v182 offset:34816
	ds_read_b128 v[44:47], v182 offset:35840
	ds_read_b128 v[56:59], v182 offset:36864
	ds_read_b128 v[60:63], v182 offset:37888
	ds_read_b128 v[136:139], v182 offset:38912
	ds_read_b128 v[140:143], v182 offset:39936
	s_addc_u32 s37, s7, 0
	s_nop 0
	v_mov_b32_e32 v64, v170
	s_nop 0
	s_waitcnt lgkmcnt(8)
	s_barrier
	s_waitcnt lgkmcnt(0)
	s_setprio 1
	s_waitcnt lgkmcnt(0)
	v_mfma_scale_f32_16x16x128_f8f6f4 v[120:123], v[8:15], v[24:31], v[120:123], v183, v183 op_sel_hi:[0,0,0]
	v_mfma_scale_f32_16x16x128_f8f6f4 v[124:127], v[128:135], v[24:31], v[124:127], v183, v183 op_sel_hi:[0,0,0]
	v_mfma_scale_f32_16x16x128_f8f6f4 v[108:111], v[8:15], v[40:47], v[192:195], v183, v183 op_sel_hi:[0,0,0]
	v_mfma_scale_f32_16x16x128_f8f6f4 v[104:107], v[128:135], v[40:47], v[196:199], v183, v183 op_sel_hi:[0,0,0]
	s_mov_b32 m0, s14
	v_mfma_scale_f32_16x16x128_f8f6f4 v[92:95], v[8:15], v[56:63], v[200:203], v183, v183 op_sel_hi:[0,0,0]
	global_load_lds_dwordx4 v169, s[36:37]
	v_mfma_scale_f32_16x16x128_f8f6f4 v[88:91], v[128:135], v[56:63], v[204:207], v183, v183 op_sel_hi:[0,0,0]
	s_nop 5
	v_mov_b32_e32 v200, v170
	v_mfma_scale_f32_16x16x128_f8f6f4 v[76:79], v[8:15], v[136:143], v[208:211], v183, v183 op_sel_hi:[0,0,0]
	s_mov_b32 m0, s15
	v_mfma_scale_f32_16x16x128_f8f6f4 v[72:75], v[128:135], v[136:143], v[212:215], v183, v183 op_sel_hi:[0,0,0]
	global_load_lds_dwordx4 v170, s[36:37]
	s_setprio 0
	s_barrier
	s_add_i32 s36, 0, 0x1c000
	v_add_u32_e32 v64, s36, v181
	v_mov_b32_e32 v170, v168
	ds_read_b128 v[144:147], v64
	ds_read_b128 v[148:151], v64 offset:1024
	ds_read_b128 v[152:155], v64 offset:2048
	ds_read_b128 v[156:159], v64 offset:3072
	s_add_i32 s35, s35, s33
	v_lshl_add_u64 v[64:65], s[8:9], 0, v[170:171]
	v_lshl_add_u64 v[64:65], v[64:65], 0, s[62:63]
	v_mov_b32_e32 v170, v180
	v_lshl_add_u64 v[64:65], s[8:9], 0, v[170:171]
	v_lshl_add_u64 v[64:65], v[64:65], 0, s[62:63]
	s_barrier
	s_waitcnt lgkmcnt(0)
	s_setprio 1
	s_waitcnt lgkmcnt(0)
	v_mfma_scale_f32_16x16x128_f8f6f4 v[116:119], v[144:151], v[24:31], v[116:119], v183, v183 op_sel_hi:[0,0,0]
	v_mfma_scale_f32_16x16x128_f8f6f4 v[112:115], v[152:159], v[24:31], v[112:115], v183, v183 op_sel_hi:[0,0,0]
	v_mfma_scale_f32_16x16x128_f8f6f4 v[100:103], v[144:151], v[40:47], v[216:219], v183, v183 op_sel_hi:[0,0,0]
	v_mfma_scale_f32_16x16x128_f8f6f4 v[96:99], v[152:159], v[40:47], v[220:223], v183, v183 op_sel_hi:[0,0,0]
	s_add_u32 s98, s8, s62
	s_addc_u32 s99, s9, s63
	s_mov_b32 m0, s35
	s_nop 5
	v_mov_b32_e32 v216, v168
	v_mfma_scale_f32_16x16x128_f8f6f4 v[84:87], v[144:151], v[56:63], v[224:227], v183, v183 op_sel_hi:[0,0,0]
	global_load_lds_dwordx4 v168, s[98:99]
	v_mfma_scale_f32_16x16x128_f8f6f4 v[80:83], v[152:159], v[56:63], v[160:163], v183, v183 op_sel_hi:[0,0,0]
	v_mfma_scale_f32_16x16x128_f8f6f4 v[68:71], v[144:151], v[136:143], v[164:167], v183, v183 op_sel_hi:[0,0,0]
	s_add_i32 m0, s35, 0x2000
	v_mfma_scale_f32_16x16x128_f8f6f4 v[64:67], v[152:159], v[136:143], v[184:187], v183, v183 op_sel_hi:[0,0,0]
	global_load_lds_dwordx4 v180, s[98:99]
	s_setprio 0
	v_mov_b32_e32 v170, v169
	s_barrier
	ds_read_b128 v[136:139], v182 offset:49152
	ds_read_b128 v[140:143], v182 offset:50176
	ds_read_b128 v[160:163], v182 offset:51200
	ds_read_b128 v[164:167], v182 offset:52224
	ds_read_b128 v[184:187], v182 offset:53248
	ds_read_b128 v[188:191], v182 offset:54272
	ds_read_b128 v[192:195], v182 offset:55296
	ds_read_b128 v[196:199], v182 offset:56320
	v_lshl_add_u64 v[24:25], s[6:7], 0, v[170:171]
	v_lshl_add_u64 v[24:25], v[24:25], 0, s[62:63]
	v_mov_b32_e32 v170, v200
	v_lshl_add_u64 v[24:25], s[6:7], 0, v[170:171]
	v_lshl_add_u64 v[24:25], v[24:25], 0, s[62:63]
	s_barrier
	s_waitcnt lgkmcnt(0)
	s_setprio 1
	s_waitcnt lgkmcnt(0)
	v_mfma_scale_f32_16x16x128_f8f6f4 v[60:63], v[8:15], v[136:143], v[228:231], v183, v183 op_sel_hi:[0,0,0]
	v_mfma_scale_f32_16x16x128_f8f6f4 v[56:59], v[128:135], v[136:143], v[232:235], v183, v183 op_sel_hi:[0,0,0]
	v_mfma_scale_f32_16x16x128_f8f6f4 v[44:47], v[8:15], v[160:167], v[236:239], v183, v183 op_sel_hi:[0,0,0]
	v_mfma_scale_f32_16x16x128_f8f6f4 v[40:43], v[128:135], v[160:167], v[240:243], v183, v183 op_sel_hi:[0,0,0]
	s_add_u32 s98, s6, s62
	s_addc_u32 s99, s7, s63
	s_mov_b32 m0, s16
	v_mfma_scale_f32_16x16x128_f8f6f4 v[28:31], v[8:15], v[184:191], v[244:247], v183, v183 op_sel_hi:[0,0,0]
	global_load_lds_dwordx4 v169, s[98:99]
	v_mfma_scale_f32_16x16x128_f8f6f4 v[24:27], v[128:135], v[184:191], v[248:251], v183, v183 op_sel_hi:[0,0,0]
	v_mfma_scale_f32_16x16x128_f8f6f4 v[12:15], v[8:15], v[192:199], v[172:175], v183, v183 op_sel_hi:[0,0,0]
	s_mov_b32 m0, s17
	v_mfma_scale_f32_16x16x128_f8f6f4 v[8:11], v[128:135], v[192:199], v[176:179], v183, v183 op_sel_hi:[0,0,0]
	global_load_lds_dwordx4 v200, s[98:99]
	s_setprio 0
	s_barrier
	v_mov_b32_e32 v170, v168
	s_add_i32 s6, s36, s33
	v_lshl_add_u64 v[128:129], s[30:31], 0, v[170:171]
	v_lshl_add_u64 v[128:129], v[128:129], 0, s[62:63]
	s_mov_b32 s100, s6
	v_mov_b32_e32 v170, v180
	s_add_i32 s101, s6, 0x2000
	v_lshl_add_u64 v[128:129], s[30:31], 0, v[170:171]
	v_lshl_add_u64 v[128:129], v[128:129], 0, s[62:63]
	s_waitcnt vmcnt(4)
	s_barrier
	s_setprio 1
	v_mfma_scale_f32_16x16x128_f8f6f4 v[52:55], v[144:151], v[136:143], v[52:55], v183, v183 op_sel_hi:[0,0,0]
	v_mfma_scale_f32_16x16x128_f8f6f4 v[48:51], v[152:159], v[136:143], v[48:51], v183, v183 op_sel_hi:[0,0,0]
	v_mfma_scale_f32_16x16x128_f8f6f4 v[36:39], v[144:151], v[160:167], v[36:39], v183, v183 op_sel_hi:[0,0,0]
	v_mfma_scale_f32_16x16x128_f8f6f4 v[32:35], v[152:159], v[160:167], v[32:35], v183, v183 op_sel_hi:[0,0,0]
	s_add_u32 s98, s30, s62
	s_addc_u32 s99, s31, s63
	s_mov_b32 m0, s100
	v_mfma_scale_f32_16x16x128_f8f6f4 v[20:23], v[144:151], v[184:191], v[20:23], v183, v183 op_sel_hi:[0,0,0]
	global_load_lds_dwordx4 v168, s[98:99]
	v_mfma_scale_f32_16x16x128_f8f6f4 v[16:19], v[152:159], v[184:191], v[16:19], v183, v183 op_sel_hi:[0,0,0]
	v_mfma_scale_f32_16x16x128_f8f6f4 v[4:7], v[144:151], v[192:199], v[4:7], v183, v183 op_sel_hi:[0,0,0]
	s_mov_b32 m0, s101
	v_mfma_scale_f32_16x16x128_f8f6f4 v[0:3], v[152:159], v[192:199], v[0:3], v183, v183 op_sel_hi:[0,0,0]
	global_load_lds_dwordx4 v180, s[98:99]
	s_setprio 0
	s_add_u32 s4, s4, 0x100
	s_addc_u32 s5, s5, 0
	s_add_u32 s25, s25, 0x100
	s_addc_u32 s27, s27, 0
	s_cmp_ge_i32 s34, s13
	s_mov_b32 s6, s34
	s_barrier
	s_cbranch_scc0 .LBB0_4066

.LBB0_4932:
	ds_read_b128 v[146:149], v141
	ds_read_b128 v[150:153], v141 offset:1024
	ds_read_b128 v[154:157], v141 offset:2048
	ds_read_b128 v[158:161], v141 offset:3072
	s_add_u32 s22, s20, 0xfffc0080
	s_addc_u32 s23, s21, -1
	s_cmp_eq_u32 s50, 12
	s_cselect_b32 s25, s15, s23
	s_cselect_b32 s24, s14, s22
	s_cselect_b32 s23, s17, s13
	s_cselect_b32 s22, s16, s11
	v_mov_b32_e32 v128, v138
	ds_read_b128 v[162:165], v142
	ds_read_b128 v[166:169], v142 offset:1024
	ds_read_b128 v[170:173], v142 offset:2048
	ds_read_b128 v[174:177], v142 offset:3072
	ds_read_b128 v[178:181], v142 offset:4096
	ds_read_b128 v[182:185], v142 offset:5120
	ds_read_b128 v[186:189], v142 offset:6144
	ds_read_b128 v[190:193], v142 offset:7168
	s_nop 0
	v_mov_b32_e32 v128, v139
	s_nop 0
	s_waitcnt lgkmcnt(8)
	s_barrier
	s_waitcnt lgkmcnt(0)
	s_setprio 1
	s_waitcnt lgkmcnt(0)
	v_mfma_scale_f32_16x16x128_f8f6f4 v[124:127], v[146:153], v[162:169], v[124:127], v143, v143 op_sel_hi:[0,0,0]
	v_mfma_scale_f32_16x16x128_f8f6f4 v[120:123], v[154:161], v[162:169], v[120:123], v143, v143 op_sel_hi:[0,0,0]
	v_mfma_scale_f32_16x16x128_f8f6f4 v[116:119], v[146:153], v[170:177], v[116:119], v143, v143 op_sel_hi:[0,0,0]
	v_mfma_scale_f32_16x16x128_f8f6f4 v[112:115], v[154:161], v[170:177], v[112:115], v143, v143 op_sel_hi:[0,0,0]
	s_add_i32 m0, s19, 0xc000
	v_mfma_scale_f32_16x16x128_f8f6f4 v[132:135], v[146:153], v[178:185], v[108:111], v143, v143 op_sel_hi:[0,0,0]
	global_load_lds_dwordx4 v138, s[20:21]
	v_mfma_scale_f32_16x16x128_f8f6f4 v[194:197], v[154:161], v[178:185], v[104:107], v143, v143 op_sel_hi:[0,0,0]
	v_mfma_scale_f32_16x16x128_f8f6f4 v[198:201], v[146:153], v[186:193], v[100:103], v143, v143 op_sel_hi:[0,0,0]
	s_add_i32 m0, s19, 0xe000
	v_mfma_scale_f32_16x16x128_f8f6f4 v[202:205], v[154:161], v[186:193], v[96:99], v143, v143 op_sel_hi:[0,0,0]
	global_load_lds_dwordx4 v139, s[20:21]
	s_setprio 0
	s_barrier
	v_mov_b32_e32 v128, v138
	s_add_i32 s51, s44, s28
	s_nop 2
	ds_read_b128 v[96:99], v144
	ds_read_b128 v[100:103], v144 offset:1024
	ds_read_b128 v[104:107], v144 offset:2048
	ds_read_b128 v[108:111], v144 offset:3072
	s_nop 0
	v_mov_b32_e32 v128, v139
	s_nop 0
	s_barrier
	s_waitcnt lgkmcnt(0)
	s_setprio 1
	s_waitcnt lgkmcnt(0)
	v_mfma_scale_f32_16x16x128_f8f6f4 v[206:209], v[96:103], v[162:169], v[60:63], v143, v143 op_sel_hi:[0,0,0]
	v_mfma_scale_f32_16x16x128_f8f6f4 v[162:165], v[104:111], v[162:169], v[56:59], v143, v143 op_sel_hi:[0,0,0]
	v_mfma_scale_f32_16x16x128_f8f6f4 v[166:169], v[96:103], v[170:177], v[52:55], v143, v143 op_sel_hi:[0,0,0]
	v_mfma_scale_f32_16x16x128_f8f6f4 v[170:173], v[104:111], v[170:177], v[48:51], v143, v143 op_sel_hi:[0,0,0]
	s_mov_b32 m0, s51
	v_mfma_scale_f32_16x16x128_f8f6f4 v[174:177], v[96:103], v[178:185], v[44:47], v143, v143 op_sel_hi:[0,0,0]
	global_load_lds_dwordx4 v138, s[22:23]
	v_mfma_scale_f32_16x16x128_f8f6f4 v[178:181], v[104:111], v[178:185], v[40:43], v143, v143 op_sel_hi:[0,0,0]
	v_mfma_scale_f32_16x16x128_f8f6f4 v[182:185], v[96:103], v[186:193], v[36:39], v143, v143 op_sel_hi:[0,0,0]
	s_add_i32 m0, s51, 0x2000
	v_mfma_scale_f32_16x16x128_f8f6f4 v[186:189], v[104:111], v[186:193], v[32:35], v143, v143 op_sel_hi:[0,0,0]
	global_load_lds_dwordx4 v139, s[22:23]
	s_setprio 0
	v_mov_b32_e32 v128, v138
	s_barrier
	s_nop 2
	ds_read_b128 v[32:35], v142 offset:16384
	ds_read_b128 v[36:39], v142 offset:17408
	ds_read_b128 v[40:43], v142 offset:18432
	ds_read_b128 v[44:47], v142 offset:19456
	ds_read_b128 v[48:51], v142 offset:20480
	ds_read_b128 v[52:55], v142 offset:21504
	ds_read_b128 v[56:59], v142 offset:22528
	ds_read_b128 v[60:63], v142 offset:23552
	s_nop 0
	v_mov_b32_e32 v128, v139
	s_nop 0
	s_barrier
	s_waitcnt lgkmcnt(0)
	s_setprio 1
	s_waitcnt lgkmcnt(0)
	v_mfma_scale_f32_16x16x128_f8f6f4 v[92:95], v[146:153], v[32:39], v[92:95], v143, v143 op_sel_hi:[0,0,0]
	v_mfma_scale_f32_16x16x128_f8f6f4 v[88:91], v[154:161], v[32:39], v[88:91], v143, v143 op_sel_hi:[0,0,0]
	v_mfma_scale_f32_16x16x128_f8f6f4 v[84:87], v[146:153], v[40:47], v[84:87], v143, v143 op_sel_hi:[0,0,0]
	v_mfma_scale_f32_16x16x128_f8f6f4 v[80:83], v[154:161], v[40:47], v[80:83], v143, v143 op_sel_hi:[0,0,0]
	s_mov_b32 m0, s19
	v_mfma_scale_f32_16x16x128_f8f6f4 v[76:79], v[146:153], v[48:55], v[76:79], v143, v143 op_sel_hi:[0,0,0]
	global_load_lds_dwordx4 v138, s[24:25]
	v_mfma_scale_f32_16x16x128_f8f6f4 v[72:75], v[154:161], v[48:55], v[72:75], v143, v143 op_sel_hi:[0,0,0]
	v_mfma_scale_f32_16x16x128_f8f6f4 v[190:193], v[146:153], v[56:63], v[68:71], v143, v143 op_sel_hi:[0,0,0]
	s_mov_b32 m0, s29
	v_mfma_scale_f32_16x16x128_f8f6f4 v[210:213], v[154:161], v[56:63], v[64:67], v143, v143 op_sel_hi:[0,0,0]
	global_load_lds_dwordx4 v139, s[24:25]
	s_setprio 0
	s_barrier
	s_add_u32 s52, s22, 0x40000
	s_addc_u32 s53, s23, 0
	s_nop 2
	v_mov_b32_e32 v64, v138
	s_add_i32 s51, s45, s28
	s_mov_b32 s100, s51
	s_nop 0
	v_mov_b32_e32 v64, v139
	s_add_i32 s101, s51, 0x2000
	s_nop 0
	s_waitcnt vmcnt(4)
	s_barrier
	s_setprio 1
	v_mfma_scale_f32_16x16x128_f8f6f4 v[214:217], v[96:103], v[32:39], v[28:31], v143, v143 op_sel_hi:[0,0,0]
	v_mfma_scale_f32_16x16x128_f8f6f4 v[218:221], v[104:111], v[32:39], v[24:27], v143, v143 op_sel_hi:[0,0,0]
	v_mfma_scale_f32_16x16x128_f8f6f4 v[222:225], v[96:103], v[40:47], v[20:23], v143, v143 op_sel_hi:[0,0,0]
	v_mfma_scale_f32_16x16x128_f8f6f4 v[226:229], v[104:111], v[40:47], v[16:19], v143, v143 op_sel_hi:[0,0,0]
	s_mov_b32 m0, s100
	v_mfma_scale_f32_16x16x128_f8f6f4 v[230:233], v[96:103], v[48:55], v[12:15], v143, v143 op_sel_hi:[0,0,0]
	global_load_lds_dwordx4 v138, s[52:53]
	v_mfma_scale_f32_16x16x128_f8f6f4 v[234:237], v[104:111], v[48:55], v[8:11], v143, v143 op_sel_hi:[0,0,0]
	v_mfma_scale_f32_16x16x128_f8f6f4 v[238:241], v[96:103], v[56:63], v[4:7], v143, v143 op_sel_hi:[0,0,0]
	s_mov_b32 m0, s101
	v_mfma_scale_f32_16x16x128_f8f6f4 v[242:245], v[104:111], v[56:63], v[0:3], v143, v143 op_sel_hi:[0,0,0]
	global_load_lds_dwordx4 v139, s[52:53]
	s_setprio 0
	s_add_i32 s51, 0, 0x18000
	s_nop 1
	v_add_u32_e32 v12, s51, v140
	s_barrier
	s_nop 0
	ds_read_b128 v[0:3], v12
	ds_read_b128 v[4:7], v12 offset:1024
	ds_read_b128 v[8:11], v12 offset:2048
	ds_read_b128 v[12:15], v12 offset:3072
	s_add_u32 s52, s24, 0x40000
	v_mov_b32_e32 v40, v138
	ds_read_b128 v[16:19], v142 offset:32768
	ds_read_b128 v[20:23], v142 offset:33792
	ds_read_b128 v[24:27], v142 offset:34816
	ds_read_b128 v[28:31], v142 offset:35840
	ds_read_b128 v[32:35], v142 offset:36864
	ds_read_b128 v[36:39], v142 offset:37888
	ds_read_b128 v[64:67], v142 offset:38912
	ds_read_b128 v[68:71], v142 offset:39936
	s_addc_u32 s53, s25, 0
	s_nop 0
	v_mov_b32_e32 v40, v139
	s_nop 0
	s_waitcnt lgkmcnt(8)
	s_barrier
	s_waitcnt lgkmcnt(0)
	s_setprio 1
	s_waitcnt lgkmcnt(0)
	v_mfma_scale_f32_16x16x128_f8f6f4 v[124:127], v[0:7], v[16:23], v[124:127], v143, v143 op_sel_hi:[0,0,0]
	v_mfma_scale_f32_16x16x128_f8f6f4 v[120:123], v[8:15], v[16:23], v[120:123], v143, v143 op_sel_hi:[0,0,0]
	v_mfma_scale_f32_16x16x128_f8f6f4 v[116:119], v[0:7], v[24:31], v[116:119], v143, v143 op_sel_hi:[0,0,0]
	v_mfma_scale_f32_16x16x128_f8f6f4 v[112:115], v[8:15], v[24:31], v[112:115], v143, v143 op_sel_hi:[0,0,0]
	s_mov_b32 m0, s30
	v_mfma_scale_f32_16x16x128_f8f6f4 v[108:111], v[0:7], v[32:39], v[132:135], v143, v143 op_sel_hi:[0,0,0]
	global_load_lds_dwordx4 v138, s[52:53]
	v_mfma_scale_f32_16x16x128_f8f6f4 v[104:107], v[8:15], v[32:39], v[194:197], v143, v143 op_sel_hi:[0,0,0]
	v_mfma_scale_f32_16x16x128_f8f6f4 v[100:103], v[0:7], v[64:71], v[198:201], v143, v143 op_sel_hi:[0,0,0]
	s_mov_b32 m0, s31
	v_mfma_scale_f32_16x16x128_f8f6f4 v[96:99], v[8:15], v[64:71], v[202:205], v143, v143 op_sel_hi:[0,0,0]
	global_load_lds_dwordx4 v139, s[52:53]
	s_setprio 0
	s_barrier
	s_add_i32 s52, 0, 0x1c000
	v_add_u32_e32 v40, s52, v140
	v_mov_b32_e32 v128, v138
	ds_read_b128 v[146:149], v40
	ds_read_b128 v[150:153], v40 offset:1024
	ds_read_b128 v[154:157], v40 offset:2048
	ds_read_b128 v[158:161], v40 offset:3072
	s_add_i32 s51, s51, s28
	v_lshl_add_u64 v[40:41], s[22:23], 0, v[128:129]
	v_lshl_add_u64 v[40:41], v[40:41], 0, s[6:7]
	v_mov_b32_e32 v128, v139
	v_lshl_add_u64 v[40:41], s[22:23], 0, v[128:129]
	v_lshl_add_u64 v[40:41], v[40:41], 0, s[6:7]
	s_barrier
	s_waitcnt lgkmcnt(0)
	s_setprio 1
	s_waitcnt lgkmcnt(0)
	v_mfma_scale_f32_16x16x128_f8f6f4 v[60:63], v[146:153], v[16:23], v[206:209], v143, v143 op_sel_hi:[0,0,0]
	v_mfma_scale_f32_16x16x128_f8f6f4 v[56:59], v[154:161], v[16:23], v[162:165], v143, v143 op_sel_hi:[0,0,0]
	v_mfma_scale_f32_16x16x128_f8f6f4 v[52:55], v[146:153], v[24:31], v[166:169], v143, v143 op_sel_hi:[0,0,0]
	v_mfma_scale_f32_16x16x128_f8f6f4 v[48:51], v[154:161], v[24:31], v[170:173], v143, v143 op_sel_hi:[0,0,0]
	s_add_u32 s98, s22, s6
	s_addc_u32 s99, s23, s7
	s_mov_b32 m0, s51
	v_mfma_scale_f32_16x16x128_f8f6f4 v[44:47], v[146:153], v[32:39], v[174:177], v143, v143 op_sel_hi:[0,0,0]
	global_load_lds_dwordx4 v138, s[98:99]
	v_mfma_scale_f32_16x16x128_f8f6f4 v[40:43], v[154:161], v[32:39], v[178:181], v143, v143 op_sel_hi:[0,0,0]
	v_mfma_scale_f32_16x16x128_f8f6f4 v[36:39], v[146:153], v[64:71], v[182:185], v143, v143 op_sel_hi:[0,0,0]
	s_add_i32 m0, s51, 0x2000
	v_mfma_scale_f32_16x16x128_f8f6f4 v[32:35], v[154:161], v[64:71], v[186:189], v143, v143 op_sel_hi:[0,0,0]
	global_load_lds_dwordx4 v139, s[98:99]
	s_setprio 0
	v_mov_b32_e32 v128, v138
	s_barrier
	ds_read_b128 v[16:19], v142 offset:49152
	ds_read_b128 v[20:23], v142 offset:50176
	ds_read_b128 v[162:165], v142 offset:51200
	ds_read_b128 v[166:169], v142 offset:52224
	ds_read_b128 v[170:173], v142 offset:53248
	ds_read_b128 v[174:177], v142 offset:54272
	ds_read_b128 v[178:181], v142 offset:55296
	ds_read_b128 v[182:185], v142 offset:56320
	v_lshl_add_u64 v[24:25], s[24:25], 0, v[128:129]
	v_lshl_add_u64 v[24:25], v[24:25], 0, s[6:7]
	v_mov_b32_e32 v128, v139
	v_lshl_add_u64 v[24:25], s[24:25], 0, v[128:129]
	v_lshl_add_u64 v[24:25], v[24:25], 0, s[6:7]
	s_barrier
	s_waitcnt lgkmcnt(0)
	s_setprio 1
	s_waitcnt lgkmcnt(0)
	v_mfma_scale_f32_16x16x128_f8f6f4 v[92:95], v[0:7], v[16:23], v[92:95], v143, v143 op_sel_hi:[0,0,0]
	v_mfma_scale_f32_16x16x128_f8f6f4 v[88:91], v[8:15], v[16:23], v[88:91], v143, v143 op_sel_hi:[0,0,0]
	v_mfma_scale_f32_16x16x128_f8f6f4 v[84:87], v[0:7], v[162:169], v[84:87], v143, v143 op_sel_hi:[0,0,0]
	v_mfma_scale_f32_16x16x128_f8f6f4 v[80:83], v[8:15], v[162:169], v[80:83], v143, v143 op_sel_hi:[0,0,0]
	s_add_u32 s98, s24, s6
	s_addc_u32 s99, s25, s7
	s_mov_b32 m0, s41
	v_mfma_scale_f32_16x16x128_f8f6f4 v[76:79], v[0:7], v[170:177], v[76:79], v143, v143 op_sel_hi:[0,0,0]
	global_load_lds_dwordx4 v138, s[98:99]
	v_mfma_scale_f32_16x16x128_f8f6f4 v[72:75], v[8:15], v[170:177], v[72:75], v143, v143 op_sel_hi:[0,0,0]
	v_mfma_scale_f32_16x16x128_f8f6f4 v[68:71], v[0:7], v[178:185], v[190:193], v143, v143 op_sel_hi:[0,0,0]
	s_mov_b32 m0, s42
	v_mfma_scale_f32_16x16x128_f8f6f4 v[64:67], v[8:15], v[178:185], v[210:213], v143, v143 op_sel_hi:[0,0,0]
	global_load_lds_dwordx4 v139, s[98:99]
	s_setprio 0
	s_barrier
	s_add_u32 s22, s22, 0x40080
	s_addc_u32 s23, s23, 0
	v_mov_b32_e32 v0, v138
	s_add_i32 s24, s52, s28
	s_nop 0
	v_mov_b32_e32 v0, v139
	s_nop 0
	s_waitcnt vmcnt(4)
	s_barrier
	s_setprio 1
	v_mfma_scale_f32_16x16x128_f8f6f4 v[28:31], v[146:153], v[16:23], v[214:217], v143, v143 op_sel_hi:[0,0,0]
	v_mfma_scale_f32_16x16x128_f8f6f4 v[24:27], v[154:161], v[16:23], v[218:221], v143, v143 op_sel_hi:[0,0,0]
	v_mfma_scale_f32_16x16x128_f8f6f4 v[20:23], v[146:153], v[162:169], v[222:225], v143, v143 op_sel_hi:[0,0,0]
	v_mfma_scale_f32_16x16x128_f8f6f4 v[16:19], v[154:161], v[162:169], v[226:229], v143, v143 op_sel_hi:[0,0,0]
	s_mov_b32 m0, s24
	v_mfma_scale_f32_16x16x128_f8f6f4 v[12:15], v[146:153], v[170:177], v[230:233], v143, v143 op_sel_hi:[0,0,0]
	global_load_lds_dwordx4 v138, s[22:23]
	v_mfma_scale_f32_16x16x128_f8f6f4 v[8:11], v[154:161], v[170:177], v[234:237], v143, v143 op_sel_hi:[0,0,0]
	v_mfma_scale_f32_16x16x128_f8f6f4 v[4:7], v[146:153], v[178:185], v[238:241], v143, v143 op_sel_hi:[0,0,0]
	s_add_i32 m0, s24, 0x2000
	v_mfma_scale_f32_16x16x128_f8f6f4 v[0:3], v[154:161], v[178:185], v[242:245], v143, v143 op_sel_hi:[0,0,0]
	global_load_lds_dwordx4 v139, s[22:23]
	s_setprio 0
	s_add_i32 s50, s50, 2
	s_add_u32 s20, s20, 0x100
	s_addc_u32 s21, s21, 0
	s_add_u32 s11, s11, 0x100
	s_addc_u32 s13, s13, 0
	s_cmp_gt_u32 s50, 13
	s_barrier
	s_cbranch_scc0 .LBB0_4932
	s_ashr_i32 s11, s18, 4
	s_mul_hi_i32 s13, s11, 0xc000
	s_mul_i32 s11, s11, 0xc000
	s_add_u32 s11, s37, s11
	s_addc_u32 s13, s38, s13
	s_lshl_b32 s20, s49, 8
	s_ashr_i32 s21, s20, 31
	s_lshl_b64 s[22:23], s[20:21], 2
	s_add_u32 s11, s11, s22
	v_mbcnt_lo_u32_b32 v134, -1, 0
	v_mbcnt_hi_u32_b32 v134, -1, v134
	s_addc_u32 s13, s13, s23
	v_ashrrev_i32_e32 v135, 4, v134
	s_add_u32 s22, s11, s46
	v_lshlrev_b32_e32 v132, 2, v135
	s_addc_u32 s23, s13, 0
	v_ashrrev_i32_e32 v133, 31, v132
	v_lshl_add_u64 v[132:133], v[132:133], 2, s[22:23]
	global_load_dwordx4 v[146:149], v[132:133], off
	global_load_dwordx4 v[150:153], v[132:133], off offset:64
	v_mov_b32_e32 v164, v129
	s_lshl_b32 s11, s18, 8
	v_mov_b32_e32 v165, v129
	s_add_i32 s22, s11, s39
	s_ashr_i32 s23, s22, 31
	s_lshl_b64 s[22:23], s[22:23], 11
	s_add_u32 s11, s35, s22
	s_addc_u32 s13, s36, s23
	v_mov_b32_e32 v162, v129
	v_lshlrev_b32_e32 v135, 3, v135
	s_add_u32 s11, s11, s20
	v_mov_b32_e32 v154, v129
	v_mov_b32_e32 v155, v129
	v_mov_b32_e32 v156, v129
	v_mov_b32_e32 v157, v129
	v_and_b32_e32 v128, 16, v134
	v_bfi_b32 v134, -16, v135, v134
	s_addc_u32 s13, s13, s21
	v_mov_b32_e32 v163, v129
	v_mov_b32_e32 v158, v129
	v_mov_b32_e32 v159, v129
	v_mov_b32_e32 v160, v129
	v_mov_b32_e32 v161, v129
	v_ashrrev_i32_e32 v135, 31, v134
	s_add_u32 s20, s11, s40
	v_lshlrev_b64 v[134:135], 11, v[134:135]
	s_addc_u32 s21, s13, 0
	v_lshl_add_u64 v[134:135], s[20:21], 0, v[134:135]
	v_lshl_add_u64 v[134:135], v[134:135], 0, v[128:129]
	v_add_co_u32_e32 v136, vcc, s34, v134
	s_mov_b32 s18, s12
	s_nop 0
	v_addc_co_u32_e32 v137, vcc, 0, v135, vcc
	s_mov_b32 s49, s10
	s_mov_b64 s[22:23], s[16:17]
	s_mov_b64 s[20:21], s[14:15]
	s_waitcnt vmcnt(0)
	v_pk_mul_f32 v[146:147], v[146:147], s[8:9] op_sel_hi:[1,0]
	v_pk_mul_f32 v[150:151], v[150:151], s[8:9] op_sel_hi:[1,0]
	v_pk_mul_f32 v[84:85], v[84:85], v[146:147]
	v_pk_mul_f32 v[80:81], v[80:81], v[150:151]
	v_cvt_pk_fp8_f32 v164, v84, v85
	v_cvt_pk_fp8_f32 v165, v80, v81
	v_pk_mul_f32 v[148:149], v[148:149], s[8:9] op_sel_hi:[1,0]
	v_pk_mul_f32 v[152:153], v[152:153], s[8:9] op_sel_hi:[1,0]
	v_pk_mul_f32 v[80:81], v[86:87], v[148:149]
	v_pk_mul_f32 v[72:73], v[72:73], v[150:151]
	v_cvt_pk_fp8_f32 v164, v80, v81 op_sel:[0,0,1]
	v_pk_mul_f32 v[80:81], v[82:83], v[152:153]
	v_pk_mul_f32 v[92:93], v[92:93], v[146:147]
	v_cvt_pk_fp8_f32 v165, v80, v81 op_sel:[0,0,1]
	v_pk_mul_f32 v[80:81], v[76:77], v[146:147]
	v_mov_b32_e32 v77, v129
	v_mov_b32_e32 v76, v129
	v_cvt_pk_fp8_f32 v77, v72, v73
	v_pk_mul_f32 v[72:73], v[78:79], v[148:149]
	v_pk_mul_f32 v[68:69], v[68:69], v[146:147]
	v_mov_b32_e32 v78, v129
	v_pk_mul_f32 v[124:125], v[124:125], v[146:147]
	v_pk_mul_f32 v[120:121], v[120:121], v[150:151]
	v_pk_mul_f32 v[116:117], v[116:117], v[146:147]
	v_pk_mul_f32 v[112:113], v[112:113], v[150:151]
	v_cvt_pk_fp8_f32 v162, v92, v93
	v_pk_mul_f32 v[88:89], v[88:89], v[150:151]
	v_cvt_pk_fp8_f32 v76, v80, v81
	v_cvt_pk_fp8_f32 v78, v68, v69
	v_pk_mul_f32 v[64:65], v[64:65], v[150:151]
	v_mov_b32_e32 v79, v129
	v_pk_mul_f32 v[108:109], v[108:109], v[146:147]
	v_pk_mul_f32 v[104:105], v[104:105], v[150:151]
	v_pk_mul_f32 v[100:101], v[100:101], v[146:147]
	v_pk_mul_f32 v[96:97], v[96:97], v[150:151]
	v_cvt_pk_fp8_f32 v154, v124, v125
	v_cvt_pk_fp8_f32 v155, v120, v121
	v_cvt_pk_fp8_f32 v156, v116, v117
	v_cvt_pk_fp8_f32 v157, v112, v113
	v_cvt_pk_fp8_f32 v163, v88, v89
	v_cvt_pk_fp8_f32 v79, v64, v65
	v_cvt_pk_fp8_f32 v158, v108, v109
	v_cvt_pk_fp8_f32 v159, v104, v105
	v_cvt_pk_fp8_f32 v160, v100, v101
	v_cvt_pk_fp8_f32 v161, v96, v97
	v_pk_mul_f32 v[88:89], v[94:95], v[148:149]
	v_pk_mul_f32 v[64:65], v[70:71], v[148:149]
	v_pk_mul_f32 v[126:127], v[126:127], v[148:149]
	v_pk_mul_f32 v[122:123], v[122:123], v[152:153]
	v_pk_mul_f32 v[118:119], v[118:119], v[148:149]
	v_pk_mul_f32 v[114:115], v[114:115], v[152:153]
	v_cvt_pk_fp8_f32 v162, v88, v89 op_sel:[0,0,1]
	v_pk_mul_f32 v[88:89], v[90:91], v[152:153]
	v_cvt_pk_fp8_f32 v76, v72, v73 op_sel:[0,0,1]
	v_pk_mul_f32 v[72:73], v[74:75], v[152:153]
	v_cvt_pk_fp8_f32 v78, v64, v65 op_sel:[0,0,1]
	v_pk_mul_f32 v[64:65], v[66:67], v[152:153]
	v_pk_mul_f32 v[110:111], v[110:111], v[148:149]
	v_pk_mul_f32 v[106:107], v[106:107], v[152:153]
	v_pk_mul_f32 v[102:103], v[102:103], v[148:149]
	v_pk_mul_f32 v[98:99], v[98:99], v[152:153]
	v_cvt_pk_fp8_f32 v154, v126, v127 op_sel:[0,0,1]
	v_cvt_pk_fp8_f32 v155, v122, v123 op_sel:[0,0,1]
	v_cvt_pk_fp8_f32 v156, v118, v119 op_sel:[0,0,1]
	v_cvt_pk_fp8_f32 v157, v114, v115 op_sel:[0,0,1]
	v_cvt_pk_fp8_f32 v163, v88, v89 op_sel:[0,0,1]
	v_cvt_pk_fp8_f32 v77, v72, v73 op_sel:[0,0,1]
	v_cvt_pk_fp8_f32 v79, v64, v65 op_sel:[0,0,1]
	v_cvt_pk_fp8_f32 v158, v110, v111 op_sel:[0,0,1]
	v_cvt_pk_fp8_f32 v159, v106, v107 op_sel:[0,0,1]
	v_cvt_pk_fp8_f32 v160, v102, v103 op_sel:[0,0,1]
	v_cvt_pk_fp8_f32 v161, v98, v99 op_sel:[0,0,1]
	v_add_co_u32_e32 v80, vcc, s47, v134
	v_permlane32_swap_b32_e32 v154, v156
	s_nop 0
	v_addc_co_u32_e32 v81, vcc, 0, v135, vcc
	v_permlane32_swap_b32_e32 v155, v157
	v_permlane32_swap_b32_e32 v162, v164
	v_permlane32_swap_b32_e32 v163, v165
	v_permlane32_swap_b32_e32 v76, v78
	v_permlane32_swap_b32_e32 v77, v79
	v_add_co_u32_e32 v82, vcc, s48, v134
	v_permlane32_swap_b32_e32 v158, v160
	v_permlane32_swap_b32_e32 v159, v161
	v_permlane16_swap_b32_e32 v154, v155
	v_permlane16_swap_b32_e32 v156, v157
	v_permlane16_swap_b32_e32 v162, v163
	v_permlane16_swap_b32_e32 v164, v165
	v_permlane16_swap_b32_e32 v76, v77
	v_permlane16_swap_b32_e32 v78, v79
	v_addc_co_u32_e32 v83, vcc, 0, v135, vcc
	v_permlane16_swap_b32_e32 v158, v159
	v_permlane16_swap_b32_e32 v160, v161
	global_store_dwordx4 v[134:135], v[154:157], off
	global_store_dwordx4 v[136:137], v[158:161], off
	global_store_dwordx4 v[80:81], v[162:165], off
	global_store_dwordx4 v[82:83], v[76:79], off
	global_load_dwordx4 v[64:67], v[132:133], off offset:512
	global_load_dwordx4 v[68:71], v[132:133], off offset:576
	v_mov_b32_e32 v75, v129
	v_mov_b32_e32 v72, v129
	v_mov_b32_e32 v73, v129
	v_mov_b32_e32 v74, v129
	s_and_b64 vcc, exec, s[4:5]
	s_waitcnt vmcnt(0)
	v_pk_mul_f32 v[64:65], v[64:65], s[8:9] op_sel_hi:[1,0]
	v_pk_mul_f32 v[68:69], v[68:69], s[8:9] op_sel_hi:[1,0]
	v_pk_mul_f32 v[70:71], v[70:71], s[8:9] op_sel_hi:[1,0]
	v_pk_mul_f32 v[48:49], v[48:49], v[68:69]
	v_pk_mul_f32 v[66:67], v[66:67], s[8:9] op_sel_hi:[1,0]
	v_cvt_pk_fp8_f32 v75, v48, v49
	v_pk_mul_f32 v[48:49], v[50:51], v[70:71]
	v_pk_mul_f32 v[40:41], v[40:41], v[68:69]
	v_pk_mul_f32 v[36:37], v[36:37], v[64:65]
	v_cvt_pk_fp8_f32 v75, v48, v49 op_sel:[0,0,1]
	v_pk_mul_f32 v[48:49], v[44:45], v[64:65]
	v_mov_b32_e32 v45, v129
	v_cvt_pk_fp8_f32 v45, v40, v41
	v_pk_mul_f32 v[40:41], v[46:47], v[66:67]
	v_mov_b32_e32 v46, v129
	v_cvt_pk_fp8_f32 v46, v36, v37
	v_pk_mul_f32 v[32:33], v[32:33], v[68:69]
	v_mov_b32_e32 v47, v129
	v_cvt_pk_fp8_f32 v47, v32, v33
	v_pk_mul_f32 v[32:33], v[38:39], v[66:67]
	v_pk_mul_f32 v[24:25], v[24:25], v[68:69]
	v_cvt_pk_fp8_f32 v46, v32, v33 op_sel:[0,0,1]
	v_pk_mul_f32 v[32:33], v[34:35], v[70:71]
	v_pk_mul_f32 v[20:21], v[20:21], v[64:65]
	v_cvt_pk_fp8_f32 v47, v32, v33 op_sel:[0,0,1]
	v_pk_mul_f32 v[32:33], v[28:29], v[64:65]
	v_mov_b32_e32 v29, v129
	v_cvt_pk_fp8_f32 v29, v24, v25
	v_pk_mul_f32 v[24:25], v[30:31], v[66:67]
	v_mov_b32_e32 v30, v129
	v_cvt_pk_fp8_f32 v30, v20, v21
	v_pk_mul_f32 v[16:17], v[16:17], v[68:69]
	v_mov_b32_e32 v31, v129
	v_cvt_pk_fp8_f32 v31, v16, v17
	v_pk_mul_f32 v[16:17], v[22:23], v[66:67]
	v_mov_b32_e32 v28, v129
	v_cvt_pk_fp8_f32 v30, v16, v17 op_sel:[0,0,1]
	v_pk_mul_f32 v[16:17], v[18:19], v[70:71]
	v_pk_mul_f32 v[8:9], v[8:9], v[68:69]
	v_cvt_pk_fp8_f32 v31, v16, v17 op_sel:[0,0,1]
	v_pk_mul_f32 v[16:17], v[12:13], v[64:65]
	v_mov_b32_e32 v13, v129
	v_pk_mul_f32 v[60:61], v[60:61], v[64:65]
	v_pk_mul_f32 v[56:57], v[56:57], v[68:69]
	v_pk_mul_f32 v[52:53], v[52:53], v[64:65]
	v_mov_b32_e32 v44, v129
	v_cvt_pk_fp8_f32 v28, v32, v33
	v_mov_b32_e32 v12, v129
	v_cvt_pk_fp8_f32 v13, v8, v9
	v_pk_mul_f32 v[8:9], v[14:15], v[66:67]
	v_pk_mul_f32 v[4:5], v[4:5], v[64:65]
	v_mov_b32_e32 v14, v129
	v_cvt_pk_fp8_f32 v72, v60, v61
	v_cvt_pk_fp8_f32 v73, v56, v57
	v_cvt_pk_fp8_f32 v74, v52, v53
	v_cvt_pk_fp8_f32 v44, v48, v49
	v_cvt_pk_fp8_f32 v12, v16, v17
	v_cvt_pk_fp8_f32 v14, v4, v5
	v_pk_mul_f32 v[0:1], v[0:1], v[68:69]
	v_mov_b32_e32 v15, v129
	v_cvt_pk_fp8_f32 v15, v0, v1
	v_pk_mul_f32 v[62:63], v[62:63], v[66:67]
	v_pk_mul_f32 v[58:59], v[58:59], v[70:71]
	v_pk_mul_f32 v[54:55], v[54:55], v[66:67]
	v_cvt_pk_fp8_f32 v28, v24, v25 op_sel:[0,0,1]
	v_pk_mul_f32 v[24:25], v[26:27], v[70:71]
	v_pk_mul_f32 v[0:1], v[6:7], v[66:67]
	v_cvt_pk_fp8_f32 v72, v62, v63 op_sel:[0,0,1]
	v_cvt_pk_fp8_f32 v73, v58, v59 op_sel:[0,0,1]
	v_cvt_pk_fp8_f32 v74, v54, v55 op_sel:[0,0,1]
	v_cvt_pk_fp8_f32 v44, v40, v41 op_sel:[0,0,1]
	v_pk_mul_f32 v[40:41], v[42:43], v[70:71]
	v_cvt_pk_fp8_f32 v29, v24, v25 op_sel:[0,0,1]
	v_cvt_pk_fp8_f32 v12, v8, v9 op_sel:[0,0,1]
	v_pk_mul_f32 v[8:9], v[10:11], v[70:71]
	v_cvt_pk_fp8_f32 v14, v0, v1 op_sel:[0,0,1]
	v_pk_mul_f32 v[0:1], v[2:3], v[70:71]
	v_cvt_pk_fp8_f32 v45, v40, v41 op_sel:[0,0,1]
	v_cvt_pk_fp8_f32 v13, v8, v9 op_sel:[0,0,1]
	v_cvt_pk_fp8_f32 v15, v0, v1 op_sel:[0,0,1]
	v_permlane32_swap_b32_e32 v72, v74
	v_permlane32_swap_b32_e32 v73, v75
	v_permlane32_swap_b32_e32 v28, v30
	v_permlane32_swap_b32_e32 v29, v31
	v_permlane16_swap_b32_e32 v72, v73
	v_permlane16_swap_b32_e32 v74, v75
	v_permlane32_swap_b32_e32 v44, v46
	v_permlane32_swap_b32_e32 v45, v47
	v_permlane16_swap_b32_e32 v28, v29
	v_permlane16_swap_b32_e32 v30, v31
	v_permlane32_swap_b32_e32 v12, v14
	v_permlane32_swap_b32_e32 v13, v15
	v_permlane16_swap_b32_e32 v44, v45
	v_permlane16_swap_b32_e32 v46, v47
	global_store_dwordx4 v[134:135], v[72:75], off offset:128
	global_store_dwordx4 v[136:137], v[44:47], off offset:128
	v_permlane16_swap_b32_e32 v12, v13
	v_permlane16_swap_b32_e32 v14, v15
	global_store_dwordx4 v[80:81], v[28:31], off offset:128
	global_store_dwordx4 v[82:83], v[12:15], off offset:128
	s_cbranch_vccz .LBB0_4925
	s_waitcnt vmcnt(0)
	v_readlane_b32 s0, v252, 2
	s_cmpk_gt_u32 s0, 0xff
	s_cbranch_scc1 .LBB0_4936
	s_barrier

.LBB0_5813:
	ds_read_b128 v[140:143], v134
	ds_read_b128 v[144:147], v134 offset:1024
	ds_read_b128 v[148:151], v134 offset:2048
	ds_read_b128 v[152:155], v134 offset:3072
	s_add_u32 s16, s14, 0xfffd0080
	s_addc_u32 s17, s15, -1
	s_cmp_eq_u32 s53, 8
	s_cselect_b32 s19, s13, s17
	s_cselect_b32 s18, s12, s16
	s_cselect_b32 s17, s11, s52
	s_cselect_b32 s16, s10, s51
	v_mov_b32_e32 v128, v132
	ds_read_b128 v[156:159], v135
	ds_read_b128 v[160:163], v135 offset:1024
	ds_read_b128 v[164:167], v135 offset:2048
	ds_read_b128 v[168:171], v135 offset:3072
	ds_read_b128 v[172:175], v135 offset:4096
	ds_read_b128 v[176:179], v135 offset:5120
	ds_read_b128 v[180:183], v135 offset:6144
	ds_read_b128 v[184:187], v135 offset:7168
	s_nop 0
	v_mov_b32_e32 v128, v133
	s_nop 0
	s_waitcnt lgkmcnt(8)
	s_barrier
	s_waitcnt lgkmcnt(0)
	s_setprio 1
	s_waitcnt lgkmcnt(0)
	v_mfma_scale_f32_16x16x128_f8f6f4 v[124:127], v[140:147], v[156:163], v[124:127], v136, v136 op_sel_hi:[0,0,0]
	v_mfma_scale_f32_16x16x128_f8f6f4 v[120:123], v[148:155], v[156:163], v[120:123], v136, v136 op_sel_hi:[0,0,0]
	v_mfma_scale_f32_16x16x128_f8f6f4 v[116:119], v[140:147], v[164:171], v[116:119], v136, v136 op_sel_hi:[0,0,0]
	v_mfma_scale_f32_16x16x128_f8f6f4 v[112:115], v[148:155], v[164:171], v[112:115], v136, v136 op_sel_hi:[0,0,0]
	s_mov_b32 m0, s38
	v_mfma_scale_f32_16x16x128_f8f6f4 v[188:191], v[140:147], v[172:179], v[108:111], v136, v136 op_sel_hi:[0,0,0]
	global_load_lds_dwordx4 v132, s[14:15]
	v_mfma_scale_f32_16x16x128_f8f6f4 v[192:195], v[148:155], v[172:179], v[104:107], v136, v136 op_sel_hi:[0,0,0]
	v_mfma_scale_f32_16x16x128_f8f6f4 v[196:199], v[140:147], v[180:187], v[100:103], v136, v136 op_sel_hi:[0,0,0]
	s_mov_b32 m0, s39
	v_mfma_scale_f32_16x16x128_f8f6f4 v[200:203], v[148:155], v[180:187], v[96:99], v136, v136 op_sel_hi:[0,0,0]
	global_load_lds_dwordx4 v133, s[14:15]
	s_setprio 0
	s_barrier
	v_mov_b32_e32 v128, v132
	s_nop 2
	ds_read_b128 v[96:99], v137
	ds_read_b128 v[100:103], v137 offset:1024
	ds_read_b128 v[104:107], v137 offset:2048
	ds_read_b128 v[108:111], v137 offset:3072
	s_nop 0
	v_mov_b32_e32 v128, v133
	s_nop 0
	s_barrier
	s_waitcnt lgkmcnt(0)
	s_setprio 1
	s_waitcnt lgkmcnt(0)
	v_mfma_scale_f32_16x16x128_f8f6f4 v[204:207], v[96:103], v[156:163], v[92:95], v136, v136 op_sel_hi:[0,0,0]
	v_mfma_scale_f32_16x16x128_f8f6f4 v[156:159], v[104:111], v[156:163], v[88:91], v136, v136 op_sel_hi:[0,0,0]
	v_mfma_scale_f32_16x16x128_f8f6f4 v[160:163], v[96:103], v[164:171], v[84:87], v136, v136 op_sel_hi:[0,0,0]
	v_mfma_scale_f32_16x16x128_f8f6f4 v[164:167], v[104:111], v[164:171], v[80:83], v136, v136 op_sel_hi:[0,0,0]
	s_mov_b32 m0, s40
	v_mfma_scale_f32_16x16x128_f8f6f4 v[168:171], v[96:103], v[172:179], v[76:79], v136, v136 op_sel_hi:[0,0,0]
	global_load_lds_dwordx4 v132, s[16:17]
	v_mfma_scale_f32_16x16x128_f8f6f4 v[172:175], v[104:111], v[172:179], v[72:75], v136, v136 op_sel_hi:[0,0,0]
	v_mfma_scale_f32_16x16x128_f8f6f4 v[176:179], v[96:103], v[180:187], v[68:71], v136, v136 op_sel_hi:[0,0,0]
	s_mov_b32 m0, s41
	v_mfma_scale_f32_16x16x128_f8f6f4 v[180:183], v[104:111], v[180:187], v[64:67], v136, v136 op_sel_hi:[0,0,0]
	global_load_lds_dwordx4 v133, s[16:17]
	s_setprio 0
	v_mov_b32_e32 v128, v132
	s_barrier
	s_nop 2
	ds_read_b128 v[64:67], v135 offset:16384
	ds_read_b128 v[68:71], v135 offset:17408
	ds_read_b128 v[72:75], v135 offset:18432
	ds_read_b128 v[76:79], v135 offset:19456
	ds_read_b128 v[80:83], v135 offset:20480
	ds_read_b128 v[84:87], v135 offset:21504
	ds_read_b128 v[88:91], v135 offset:22528
	ds_read_b128 v[92:95], v135 offset:23552
	s_nop 0
	v_mov_b32_e32 v128, v133
	s_nop 0
	s_barrier
	s_waitcnt lgkmcnt(0)
	s_setprio 1
	s_waitcnt lgkmcnt(0)
	v_mfma_scale_f32_16x16x128_f8f6f4 v[60:63], v[140:147], v[64:71], v[60:63], v136, v136 op_sel_hi:[0,0,0]
	v_mfma_scale_f32_16x16x128_f8f6f4 v[56:59], v[148:155], v[64:71], v[56:59], v136, v136 op_sel_hi:[0,0,0]
	v_mfma_scale_f32_16x16x128_f8f6f4 v[52:55], v[140:147], v[72:79], v[52:55], v136, v136 op_sel_hi:[0,0,0]
	v_mfma_scale_f32_16x16x128_f8f6f4 v[48:51], v[148:155], v[72:79], v[48:51], v136, v136 op_sel_hi:[0,0,0]
	s_mov_b32 m0, s24
	v_mfma_scale_f32_16x16x128_f8f6f4 v[184:187], v[140:147], v[80:87], v[44:47], v136, v136 op_sel_hi:[0,0,0]
	global_load_lds_dwordx4 v132, s[18:19]
	v_mfma_scale_f32_16x16x128_f8f6f4 v[208:211], v[148:155], v[80:87], v[40:43], v136, v136 op_sel_hi:[0,0,0]
	v_mfma_scale_f32_16x16x128_f8f6f4 v[212:215], v[140:147], v[88:95], v[36:39], v136, v136 op_sel_hi:[0,0,0]
	s_mov_b32 m0, s25
	v_mfma_scale_f32_16x16x128_f8f6f4 v[216:219], v[148:155], v[88:95], v[32:35], v136, v136 op_sel_hi:[0,0,0]
	global_load_lds_dwordx4 v133, s[18:19]
	s_setprio 0
	s_barrier
	s_add_u32 s54, s16, 0x30000
	s_nop 3
	v_mov_b32_e32 v32, v132
	s_addc_u32 s55, s17, 0
	s_nop 0
	v_mov_b32_e32 v32, v133
	s_nop 0
	s_waitcnt vmcnt(4)
	s_barrier
	s_setprio 1
	v_mfma_scale_f32_16x16x128_f8f6f4 v[220:223], v[96:103], v[64:71], v[28:31], v136, v136 op_sel_hi:[0,0,0]
	v_mfma_scale_f32_16x16x128_f8f6f4 v[224:227], v[104:111], v[64:71], v[24:27], v136, v136 op_sel_hi:[0,0,0]
	v_mfma_scale_f32_16x16x128_f8f6f4 v[228:231], v[96:103], v[72:79], v[20:23], v136, v136 op_sel_hi:[0,0,0]
	v_mfma_scale_f32_16x16x128_f8f6f4 v[232:235], v[104:111], v[72:79], v[16:19], v136, v136 op_sel_hi:[0,0,0]
	s_mov_b32 m0, s42
	v_mfma_scale_f32_16x16x128_f8f6f4 v[236:239], v[96:103], v[80:87], v[12:15], v136, v136 op_sel_hi:[0,0,0]
	global_load_lds_dwordx4 v132, s[54:55]
	v_mfma_scale_f32_16x16x128_f8f6f4 v[240:243], v[104:111], v[80:87], v[8:11], v136, v136 op_sel_hi:[0,0,0]
	v_mfma_scale_f32_16x16x128_f8f6f4 v[244:247], v[96:103], v[88:95], v[4:7], v136, v136 op_sel_hi:[0,0,0]
	s_mov_b32 m0, s43
	v_mfma_scale_f32_16x16x128_f8f6f4 v[248:251], v[104:111], v[88:95], v[0:3], v136, v136 op_sel_hi:[0,0,0]
	global_load_lds_dwordx4 v133, s[54:55]
	s_setprio 0
	s_barrier
	s_nop 4
	ds_read_b128 v[0:3], v138
	ds_read_b128 v[4:7], v138 offset:1024
	ds_read_b128 v[8:11], v138 offset:2048
	ds_read_b128 v[12:15], v138 offset:3072
	s_add_u32 s54, s18, 0x30000
	v_mov_b32_e32 v64, v132
	ds_read_b128 v[16:19], v135 offset:32768
	ds_read_b128 v[20:23], v135 offset:33792
	ds_read_b128 v[24:27], v135 offset:34816
	ds_read_b128 v[28:31], v135 offset:35840
	ds_read_b128 v[32:35], v135 offset:36864
	ds_read_b128 v[36:39], v135 offset:37888
	ds_read_b128 v[40:43], v135 offset:38912
	ds_read_b128 v[44:47], v135 offset:39936
	s_addc_u32 s55, s19, 0
	s_nop 0
	v_mov_b32_e32 v64, v133
	s_nop 0
	s_waitcnt lgkmcnt(8)
	s_barrier
	s_waitcnt lgkmcnt(0)
	s_setprio 1
	s_waitcnt lgkmcnt(0)
	v_mfma_scale_f32_16x16x128_f8f6f4 v[124:127], v[0:7], v[16:23], v[124:127], v136, v136 op_sel_hi:[0,0,0]
	v_mfma_scale_f32_16x16x128_f8f6f4 v[120:123], v[8:15], v[16:23], v[120:123], v136, v136 op_sel_hi:[0,0,0]
	v_mfma_scale_f32_16x16x128_f8f6f4 v[116:119], v[0:7], v[24:31], v[116:119], v136, v136 op_sel_hi:[0,0,0]
	v_mfma_scale_f32_16x16x128_f8f6f4 v[112:115], v[8:15], v[24:31], v[112:115], v136, v136 op_sel_hi:[0,0,0]
	s_mov_b32 m0, s26
	v_mfma_scale_f32_16x16x128_f8f6f4 v[108:111], v[0:7], v[32:39], v[188:191], v136, v136 op_sel_hi:[0,0,0]
	global_load_lds_dwordx4 v132, s[54:55]
	v_mfma_scale_f32_16x16x128_f8f6f4 v[104:107], v[8:15], v[32:39], v[192:195], v136, v136 op_sel_hi:[0,0,0]
	v_mfma_scale_f32_16x16x128_f8f6f4 v[100:103], v[0:7], v[40:47], v[196:199], v136, v136 op_sel_hi:[0,0,0]
	s_mov_b32 m0, s27
	v_mfma_scale_f32_16x16x128_f8f6f4 v[96:99], v[8:15], v[40:47], v[200:203], v136, v136 op_sel_hi:[0,0,0]
	global_load_lds_dwordx4 v133, s[54:55]
	s_setprio 0
	s_barrier
	v_mov_b32_e32 v128, v132
	ds_read_b128 v[140:143], v139
	ds_read_b128 v[144:147], v139 offset:1024
	ds_read_b128 v[148:151], v139 offset:2048
	ds_read_b128 v[152:155], v139 offset:3072
	v_lshl_add_u64 v[64:65], s[16:17], 0, v[128:129]
	v_lshl_add_u64 v[64:65], v[64:65], 0, s[4:5]
	v_mov_b32_e32 v128, v133
	v_lshl_add_u64 v[64:65], s[16:17], 0, v[128:129]
	v_lshl_add_u64 v[64:65], v[64:65], 0, s[4:5]
	s_barrier
	s_waitcnt lgkmcnt(0)
	s_setprio 1
	s_waitcnt lgkmcnt(0)
	v_mfma_scale_f32_16x16x128_f8f6f4 v[92:95], v[140:147], v[16:23], v[204:207], v136, v136 op_sel_hi:[0,0,0]
	v_mfma_scale_f32_16x16x128_f8f6f4 v[88:91], v[148:155], v[16:23], v[156:159], v136, v136 op_sel_hi:[0,0,0]
	v_mfma_scale_f32_16x16x128_f8f6f4 v[84:87], v[140:147], v[24:31], v[160:163], v136, v136 op_sel_hi:[0,0,0]
	v_mfma_scale_f32_16x16x128_f8f6f4 v[80:83], v[148:155], v[24:31], v[164:167], v136, v136 op_sel_hi:[0,0,0]
	s_add_u32 s98, s16, s4
	s_addc_u32 s99, s17, s5
	s_mov_b32 m0, s45
	v_mfma_scale_f32_16x16x128_f8f6f4 v[76:79], v[140:147], v[32:39], v[168:171], v136, v136 op_sel_hi:[0,0,0]
	global_load_lds_dwordx4 v132, s[98:99]
	v_mfma_scale_f32_16x16x128_f8f6f4 v[72:75], v[148:155], v[32:39], v[172:175], v136, v136 op_sel_hi:[0,0,0]
	v_mfma_scale_f32_16x16x128_f8f6f4 v[68:71], v[140:147], v[40:47], v[176:179], v136, v136 op_sel_hi:[0,0,0]
	s_mov_b32 m0, s46
	v_mfma_scale_f32_16x16x128_f8f6f4 v[64:67], v[148:155], v[40:47], v[180:183], v136, v136 op_sel_hi:[0,0,0]
	global_load_lds_dwordx4 v133, s[98:99]
	s_setprio 0
	v_mov_b32_e32 v128, v132
	s_barrier
	ds_read_b128 v[16:19], v135 offset:49152
	ds_read_b128 v[20:23], v135 offset:50176
	ds_read_b128 v[156:159], v135 offset:51200
	ds_read_b128 v[160:163], v135 offset:52224
	ds_read_b128 v[164:167], v135 offset:53248
	ds_read_b128 v[168:171], v135 offset:54272
	ds_read_b128 v[172:175], v135 offset:55296
	ds_read_b128 v[176:179], v135 offset:56320
	v_lshl_add_u64 v[24:25], s[18:19], 0, v[128:129]
	v_lshl_add_u64 v[24:25], v[24:25], 0, s[4:5]
	v_mov_b32_e32 v128, v133
	v_lshl_add_u64 v[24:25], s[18:19], 0, v[128:129]
	v_lshl_add_u64 v[24:25], v[24:25], 0, s[4:5]
	s_barrier
	s_waitcnt lgkmcnt(0)
	s_setprio 1
	s_waitcnt lgkmcnt(0)
	v_mfma_scale_f32_16x16x128_f8f6f4 v[60:63], v[0:7], v[16:23], v[60:63], v136, v136 op_sel_hi:[0,0,0]
	v_mfma_scale_f32_16x16x128_f8f6f4 v[56:59], v[8:15], v[16:23], v[56:59], v136, v136 op_sel_hi:[0,0,0]
	v_mfma_scale_f32_16x16x128_f8f6f4 v[52:55], v[0:7], v[156:163], v[52:55], v136, v136 op_sel_hi:[0,0,0]
	v_mfma_scale_f32_16x16x128_f8f6f4 v[48:51], v[8:15], v[156:163], v[48:51], v136, v136 op_sel_hi:[0,0,0]
	s_add_u32 s98, s18, s4
	s_addc_u32 s99, s19, s5
	s_mov_b32 m0, s35
	v_mfma_scale_f32_16x16x128_f8f6f4 v[44:47], v[0:7], v[164:171], v[184:187], v136, v136 op_sel_hi:[0,0,0]
	global_load_lds_dwordx4 v132, s[98:99]
	v_mfma_scale_f32_16x16x128_f8f6f4 v[40:43], v[8:15], v[164:171], v[208:211], v136, v136 op_sel_hi:[0,0,0]
	v_mfma_scale_f32_16x16x128_f8f6f4 v[36:39], v[0:7], v[172:179], v[212:215], v136, v136 op_sel_hi:[0,0,0]
	s_mov_b32 m0, s36
	v_mfma_scale_f32_16x16x128_f8f6f4 v[32:35], v[8:15], v[172:179], v[216:219], v136, v136 op_sel_hi:[0,0,0]
	global_load_lds_dwordx4 v133, s[98:99]
	s_setprio 0
	s_barrier
	s_add_u32 s16, s16, 0x30080
	s_addc_u32 s17, s17, 0
	v_mov_b32_e32 v0, v132
	s_add_i32 s18, s44, s23
	s_nop 0
	v_mov_b32_e32 v0, v133
	s_nop 0
	s_waitcnt vmcnt(4)
	s_barrier
	s_setprio 1
	v_mfma_scale_f32_16x16x128_f8f6f4 v[28:31], v[140:147], v[16:23], v[220:223], v136, v136 op_sel_hi:[0,0,0]
	v_mfma_scale_f32_16x16x128_f8f6f4 v[24:27], v[148:155], v[16:23], v[224:227], v136, v136 op_sel_hi:[0,0,0]
	v_mfma_scale_f32_16x16x128_f8f6f4 v[20:23], v[140:147], v[156:163], v[228:231], v136, v136 op_sel_hi:[0,0,0]
	v_mfma_scale_f32_16x16x128_f8f6f4 v[16:19], v[148:155], v[156:163], v[232:235], v136, v136 op_sel_hi:[0,0,0]
	s_mov_b32 m0, s18
	v_mfma_scale_f32_16x16x128_f8f6f4 v[12:15], v[140:147], v[164:171], v[236:239], v136, v136 op_sel_hi:[0,0,0]
	global_load_lds_dwordx4 v132, s[16:17]
	v_mfma_scale_f32_16x16x128_f8f6f4 v[8:11], v[148:155], v[164:171], v[240:243], v136, v136 op_sel_hi:[0,0,0]
	v_mfma_scale_f32_16x16x128_f8f6f4 v[4:7], v[140:147], v[172:179], v[244:247], v136, v136 op_sel_hi:[0,0,0]
	s_add_i32 m0, s18, 0x2000
	v_mfma_scale_f32_16x16x128_f8f6f4 v[0:3], v[148:155], v[172:179], v[248:251], v136, v136 op_sel_hi:[0,0,0]
	global_load_lds_dwordx4 v133, s[16:17]
	s_setprio 0
	s_add_i32 s53, s53, 2
	s_add_u32 s14, s14, 0x100
	s_addc_u32 s15, s15, 0
	s_add_u32 s51, s51, 0x100
	s_addc_u32 s52, s52, 0
	s_cmp_gt_u32 s53, 9
	s_barrier
	s_cbranch_scc0 .LBB0_5813
	v_pk_mul_f32 v[140:141], v[124:125], s[6:7] op_sel_hi:[1,0]
	v_pk_mul_f32 v[120:121], v[120:121], s[6:7] op_sel_hi:[1,0]
	v_mov_b32_e32 v125, v129
	v_cvt_pk_fp8_f32 v125, v120, v121
	v_pk_mul_f32 v[120:121], v[126:127], s[6:7] op_sel_hi:[1,0]
	v_pk_mul_f32 v[116:117], v[116:117], s[6:7] op_sel_hi:[1,0]
	v_mov_b32_e32 v126, v129
	v_cvt_pk_fp8_f32 v126, v116, v117
	v_pk_mul_f32 v[112:113], v[112:113], s[6:7] op_sel_hi:[1,0]
	v_mov_b32_e32 v127, v129
	v_cvt_pk_fp8_f32 v127, v112, v113
	v_pk_mul_f32 v[112:113], v[118:119], s[6:7] op_sel_hi:[1,0]
	v_pk_mul_f32 v[104:105], v[104:105], s[6:7] op_sel_hi:[1,0]
	v_cvt_pk_fp8_f32 v126, v112, v113 op_sel:[0,0,1]
	v_pk_mul_f32 v[112:113], v[114:115], s[6:7] op_sel_hi:[1,0]
	v_pk_mul_f32 v[100:101], v[100:101], s[6:7] op_sel_hi:[1,0]
	v_cvt_pk_fp8_f32 v127, v112, v113 op_sel:[0,0,1]
	v_pk_mul_f32 v[112:113], v[108:109], s[6:7] op_sel_hi:[1,0]
	v_mov_b32_e32 v109, v129
	v_cvt_pk_fp8_f32 v109, v104, v105
	v_pk_mul_f32 v[104:105], v[110:111], s[6:7] op_sel_hi:[1,0]
	v_mov_b32_e32 v110, v129
	v_cvt_pk_fp8_f32 v110, v100, v101
	v_pk_mul_f32 v[100:101], v[92:93], s[6:7] op_sel_hi:[1,0]
	v_pk_mul_f32 v[88:89], v[88:89], s[6:7] op_sel_hi:[1,0]
	v_mov_b32_e32 v93, v129
	v_cvt_pk_fp8_f32 v93, v88, v89
	v_pk_mul_f32 v[88:89], v[94:95], s[6:7] op_sel_hi:[1,0]
	v_pk_mul_f32 v[84:85], v[84:85], s[6:7] op_sel_hi:[1,0]
	v_mov_b32_e32 v94, v129
	v_cvt_pk_fp8_f32 v94, v84, v85
	v_pk_mul_f32 v[80:81], v[80:81], s[6:7] op_sel_hi:[1,0]
	v_mov_b32_e32 v95, v129
	v_cvt_pk_fp8_f32 v95, v80, v81
	v_pk_mul_f32 v[80:81], v[86:87], s[6:7] op_sel_hi:[1,0]
	v_pk_mul_f32 v[72:73], v[72:73], s[6:7] op_sel_hi:[1,0]
	v_cvt_pk_fp8_f32 v94, v80, v81 op_sel:[0,0,1]
	v_pk_mul_f32 v[80:81], v[82:83], s[6:7] op_sel_hi:[1,0]
	v_pk_mul_f32 v[68:69], v[68:69], s[6:7] op_sel_hi:[1,0]
	v_cvt_pk_fp8_f32 v95, v80, v81 op_sel:[0,0,1]
	v_pk_mul_f32 v[80:81], v[76:77], s[6:7] op_sel_hi:[1,0]
	v_mov_b32_e32 v77, v129
	v_cvt_pk_fp8_f32 v77, v72, v73
	v_pk_mul_f32 v[72:73], v[78:79], s[6:7] op_sel_hi:[1,0]
	v_mov_b32_e32 v78, v129
	v_cvt_pk_fp8_f32 v78, v68, v69
	v_pk_mul_f32 v[64:65], v[64:65], s[6:7] op_sel_hi:[1,0]
	v_mov_b32_e32 v79, v129
	v_cvt_pk_fp8_f32 v79, v64, v65
	v_pk_mul_f32 v[64:65], v[70:71], s[6:7] op_sel_hi:[1,0]
	v_pk_mul_f32 v[56:57], v[56:57], s[6:7] op_sel_hi:[1,0]
	v_cvt_pk_fp8_f32 v78, v64, v65 op_sel:[0,0,1]
	v_pk_mul_f32 v[64:65], v[66:67], s[6:7] op_sel_hi:[1,0]
	v_pk_mul_f32 v[52:53], v[52:53], s[6:7] op_sel_hi:[1,0]
	v_cvt_pk_fp8_f32 v79, v64, v65 op_sel:[0,0,1]
	v_pk_mul_f32 v[64:65], v[60:61], s[6:7] op_sel_hi:[1,0]
	v_mov_b32_e32 v61, v129
	v_cvt_pk_fp8_f32 v61, v56, v57
	v_pk_mul_f32 v[56:57], v[62:63], s[6:7] op_sel_hi:[1,0]
	v_mov_b32_e32 v62, v129
	v_cvt_pk_fp8_f32 v62, v52, v53
	v_pk_mul_f32 v[48:49], v[48:49], s[6:7] op_sel_hi:[1,0]
	v_mov_b32_e32 v63, v129
	v_cvt_pk_fp8_f32 v63, v48, v49
	s_lshl_b32 s14, s49, 8
	v_pk_mul_f32 v[48:49], v[54:55], s[6:7] op_sel_hi:[1,0]
	s_add_i32 s14, s14, s33
	v_cvt_pk_fp8_f32 v62, v48, v49 op_sel:[0,0,1]
	v_pk_mul_f32 v[48:49], v[50:51], s[6:7] op_sel_hi:[1,0]
	s_lshl_b32 s16, s50, 8
	s_ashr_i32 s15, s14, 31
	v_cvt_pk_fp8_f32 v63, v48, v49 op_sel:[0,0,1]
	v_pk_mul_f32 v[48:49], v[44:45], s[6:7] op_sel_hi:[1,0]
	v_pk_mul_f32 v[40:41], v[40:41], s[6:7] op_sel_hi:[1,0]
	v_mov_b32_e32 v45, v129
	s_ashr_i32 s17, s16, 31
	s_lshl_b64 s[18:19], s[14:15], 11
	v_cvt_pk_fp8_f32 v45, v40, v41
	v_pk_mul_f32 v[40:41], v[46:47], s[6:7] op_sel_hi:[1,0]
	v_pk_mul_f32 v[36:37], v[36:37], s[6:7] op_sel_hi:[1,0]
	v_mov_b32_e32 v46, v129
	s_add_u32 s15, s30, s18
	v_cvt_pk_fp8_f32 v46, v36, v37
	v_pk_mul_f32 v[36:37], v[28:29], s[6:7] op_sel_hi:[1,0]
	v_pk_mul_f32 v[24:25], v[24:25], s[6:7] op_sel_hi:[1,0]
	v_mov_b32_e32 v29, v129
	s_addc_u32 s18, s31, s19
	v_cvt_pk_fp8_f32 v29, v24, v25
	v_pk_mul_f32 v[24:25], v[30:31], s[6:7] op_sel_hi:[1,0]
	v_pk_mul_f32 v[20:21], v[20:21], s[6:7] op_sel_hi:[1,0]
	v_mov_b32_e32 v30, v129
	s_add_u32 s15, s15, s16
	v_cvt_pk_fp8_f32 v30, v20, v21
	v_pk_mul_f32 v[16:17], v[16:17], s[6:7] op_sel_hi:[1,0]
	v_mov_b32_e32 v31, v129
	s_addc_u32 s19, s18, s17
	v_cvt_pk_fp8_f32 v31, v16, v17
	s_add_u32 s18, s15, s34
	s_addc_u32 s19, s19, 0
	s_addk_i32 s14, 0x80
	v_pk_mul_f32 v[16:17], v[22:23], s[6:7] op_sel_hi:[1,0]
	s_ashr_i32 s15, s14, 31
	v_cvt_pk_fp8_f32 v30, v16, v17 op_sel:[0,0,1]
	v_pk_mul_f32 v[16:17], v[18:19], s[6:7] op_sel_hi:[1,0]
	v_mov_b32_e32 v124, v129
	v_mov_b32_e32 v108, v129
	v_pk_mul_f32 v[96:97], v[96:97], s[6:7] op_sel_hi:[1,0]
	v_mov_b32_e32 v111, v129
	v_mov_b32_e32 v92, v129
	s_lshl_b64 s[14:15], s[14:15], 11
	v_mov_b32_e32 v60, v129
	v_mov_b32_e32 v44, v129
	v_mov_b32_e32 v28, v129
	v_cvt_pk_fp8_f32 v31, v16, v17 op_sel:[0,0,1]
	v_pk_mul_f32 v[16:17], v[12:13], s[6:7] op_sel_hi:[1,0]
	v_pk_mul_f32 v[8:9], v[8:9], s[6:7] op_sel_hi:[1,0]
	v_mov_b32_e32 v13, v129
	v_mbcnt_lo_u32_b32 v128, -1, 0
	v_mbcnt_hi_u32_b32 v128, -1, v128
	v_cvt_pk_fp8_f32 v124, v140, v141
	v_ashrrev_i32_e32 v130, 1, v128
	v_cvt_pk_fp8_f32 v108, v112, v113
	v_cvt_pk_fp8_f32 v111, v96, v97
	v_cvt_pk_fp8_f32 v92, v100, v101
	v_mov_b32_e32 v76, v129
	v_cvt_pk_fp8_f32 v60, v64, v65
	v_cvt_pk_fp8_f32 v44, v48, v49
	v_pk_mul_f32 v[32:33], v[32:33], s[6:7] op_sel_hi:[1,0]
	v_mov_b32_e32 v47, v129
	s_add_u32 s14, s30, s14
	v_cvt_pk_fp8_f32 v28, v36, v37
	v_mov_b32_e32 v12, v129
	v_cvt_pk_fp8_f32 v13, v8, v9
	v_pk_mul_f32 v[8:9], v[14:15], s[6:7] op_sel_hi:[1,0]
	v_pk_mul_f32 v[4:5], v[4:5], s[6:7] op_sel_hi:[1,0]
	v_mov_b32_e32 v14, v129
	v_bfi_b32 v130, -16, v130, v128
	v_cvt_pk_fp8_f32 v76, v80, v81
	v_cvt_pk_fp8_f32 v47, v32, v33
	s_addc_u32 s15, s31, s15
	v_cvt_pk_fp8_f32 v12, v16, v17
	v_cvt_pk_fp8_f32 v14, v4, v5
	v_pk_mul_f32 v[0:1], v[0:1], s[6:7] op_sel_hi:[1,0]
	v_mov_b32_e32 v15, v129
	v_ashrrev_i32_e32 v131, 31, v130
	v_pk_mul_f32 v[96:97], v[102:103], s[6:7] op_sel_hi:[1,0]
	s_add_u32 s14, s14, s16
	v_cvt_pk_fp8_f32 v15, v0, v1
	v_lshlrev_b64 v[130:131], 11, v[130:131]
	v_cvt_pk_fp8_f32 v110, v96, v97 op_sel:[0,0,1]
	v_pk_mul_f32 v[96:97], v[98:99], s[6:7] op_sel_hi:[1,0]
	v_pk_mul_f32 v[32:33], v[38:39], s[6:7] op_sel_hi:[1,0]
	s_addc_u32 s15, s15, s17
	v_and_b32_e32 v128, 16, v128
	v_cvt_pk_fp8_f32 v124, v120, v121 op_sel:[0,0,1]
	v_pk_mul_f32 v[120:121], v[122:123], s[6:7] op_sel_hi:[1,0]
	v_cvt_pk_fp8_f32 v108, v104, v105 op_sel:[0,0,1]
	v_pk_mul_f32 v[104:105], v[106:107], s[6:7] op_sel_hi:[1,0]
	v_cvt_pk_fp8_f32 v111, v96, v97 op_sel:[0,0,1]
	v_lshl_add_u64 v[96:97], s[18:19], 0, v[130:131]
	v_cvt_pk_fp8_f32 v92, v88, v89 op_sel:[0,0,1]
	v_pk_mul_f32 v[88:89], v[90:91], s[6:7] op_sel_hi:[1,0]
	v_cvt_pk_fp8_f32 v60, v56, v57 op_sel:[0,0,1]
	v_pk_mul_f32 v[56:57], v[58:59], s[6:7] op_sel_hi:[1,0]
	v_cvt_pk_fp8_f32 v44, v40, v41 op_sel:[0,0,1]
	v_pk_mul_f32 v[40:41], v[42:43], s[6:7] op_sel_hi:[1,0]
	v_cvt_pk_fp8_f32 v46, v32, v33 op_sel:[0,0,1]
	v_pk_mul_f32 v[32:33], v[34:35], s[6:7] op_sel_hi:[1,0]
	s_add_u32 s14, s14, s34
	v_cvt_pk_fp8_f32 v28, v24, v25 op_sel:[0,0,1]
	v_pk_mul_f32 v[24:25], v[26:27], s[6:7] op_sel_hi:[1,0]
	v_pk_mul_f32 v[0:1], v[6:7], s[6:7] op_sel_hi:[1,0]
	v_cvt_pk_fp8_f32 v125, v120, v121 op_sel:[0,0,1]
	v_cvt_pk_fp8_f32 v109, v104, v105 op_sel:[0,0,1]
	v_lshl_add_u64 v[96:97], v[96:97], 0, v[128:129]
	v_cvt_pk_fp8_f32 v93, v88, v89 op_sel:[0,0,1]
	v_cvt_pk_fp8_f32 v76, v72, v73 op_sel:[0,0,1]
	v_pk_mul_f32 v[72:73], v[74:75], s[6:7] op_sel_hi:[1,0]
	v_cvt_pk_fp8_f32 v61, v56, v57 op_sel:[0,0,1]
	v_cvt_pk_fp8_f32 v45, v40, v41 op_sel:[0,0,1]
	v_cvt_pk_fp8_f32 v47, v32, v33 op_sel:[0,0,1]
	s_addc_u32 s15, s15, 0
	v_cvt_pk_fp8_f32 v29, v24, v25 op_sel:[0,0,1]
	v_cvt_pk_fp8_f32 v12, v8, v9 op_sel:[0,0,1]
	v_pk_mul_f32 v[8:9], v[10:11], s[6:7] op_sel_hi:[1,0]
	v_cvt_pk_fp8_f32 v14, v0, v1 op_sel:[0,0,1]
	v_pk_mul_f32 v[0:1], v[2:3], s[6:7] op_sel_hi:[1,0]
	v_add_co_u32_e32 v98, vcc, s29, v96
	v_cvt_pk_fp8_f32 v77, v72, v73 op_sel:[0,0,1]
	v_lshl_add_u64 v[32:33], s[14:15], 0, v[130:131]
	v_cvt_pk_fp8_f32 v13, v8, v9 op_sel:[0,0,1]
	v_cvt_pk_fp8_f32 v15, v0, v1 op_sel:[0,0,1]
	v_addc_co_u32_e32 v99, vcc, 0, v97, vcc
	v_lshl_add_u64 v[32:33], v[32:33], 0, v[128:129]
	v_add_co_u32_e32 v34, vcc, s29, v32
	v_permlane32_swap_b32_e32 v124, v126
	v_permlane32_swap_b32_e32 v125, v127
	v_permlane32_swap_b32_e32 v108, v110
	v_permlane32_swap_b32_e32 v109, v111
	v_permlane32_swap_b32_e32 v92, v94
	v_permlane32_swap_b32_e32 v93, v95
	v_permlane32_swap_b32_e32 v60, v62
	v_permlane32_swap_b32_e32 v61, v63
	v_permlane32_swap_b32_e32 v44, v46
	v_permlane32_swap_b32_e32 v45, v47
	v_addc_co_u32_e32 v35, vcc, 0, v33, vcc
	v_permlane32_swap_b32_e32 v28, v30
	v_permlane32_swap_b32_e32 v29, v31
	v_permlane16_swap_b32_e32 v124, v125
	v_permlane16_swap_b32_e32 v126, v127
	v_permlane16_swap_b32_e32 v108, v109
	v_permlane16_swap_b32_e32 v110, v111
	v_permlane16_swap_b32_e32 v92, v93
	v_permlane16_swap_b32_e32 v94, v95
	v_permlane32_swap_b32_e32 v76, v78
	v_permlane32_swap_b32_e32 v77, v79
	v_permlane16_swap_b32_e32 v60, v61
	v_permlane16_swap_b32_e32 v62, v63
	v_permlane16_swap_b32_e32 v44, v45
	v_permlane16_swap_b32_e32 v46, v47
	v_permlane16_swap_b32_e32 v28, v29
	v_permlane16_swap_b32_e32 v30, v31
	v_permlane32_swap_b32_e32 v12, v14
	v_permlane32_swap_b32_e32 v13, v15
	s_and_b64 vcc, exec, s[8:9]
	s_mov_b32 s50, s48
	s_mov_b32 s49, s47
	s_mov_b64 s[16:17], s[10:11]
	s_mov_b64 s[14:15], s[12:13]
	global_store_dwordx4 v[96:97], v[124:127], off
	global_store_dwordx4 v[98:99], v[108:111], off
	v_permlane16_swap_b32_e32 v76, v77
	v_permlane16_swap_b32_e32 v78, v79
	global_store_dwordx4 v[96:97], v[92:95], off offset:128
	global_store_dwordx4 v[98:99], v[76:79], off offset:128
	global_store_dwordx4 v[32:33], v[60:63], off
	global_store_dwordx4 v[34:35], v[44:47], off
	v_permlane16_swap_b32_e32 v12, v13
	v_permlane16_swap_b32_e32 v14, v15
	global_store_dwordx4 v[32:33], v[28:31], off offset:128
	global_store_dwordx4 v[34:35], v[12:15], off offset:128
	s_cbranch_vccz .LBB0_5808
	s_waitcnt vmcnt(0)
	v_readlane_b32 s0, v252, 2
	s_cmpk_gt_u32 s0, 0xff
	s_cbranch_scc1 .LBB0_5817
	s_barrier
